# v39 + streaming (nt) loads for the f32 inputs of the weight-conversion / prep code
# speedup vs baseline: 1.0190x; 1.0190x over previous
.LBB0_124:
	v_readlane_b32 s0, v253, 39
	v_readlane_b32 s1, v253, 40
	s_andn2_b64 vcc, exec, s[0:1]
	s_cbranch_vccnz .LBB0_345
	s_waitcnt lgkmcnt(0)
	s_barrier
	s_load_dwordx4 s[40:43], s[44:45], 0x10
	s_add_u32 s34, s74, 0x4d00000
	s_addc_u32 s35, s75, 0
	s_waitcnt lgkmcnt(0)
	s_add_u32 s0, s40, 0x1000
	s_addc_u32 s1, s41, 0
	s_abs_i32 s15, s30
	s_mul_hi_u32 s16, s15, s27
	s_mul_i32 s16, s16, s33
	s_sub_i32 s15, s15, s16
	s_ashr_i32 s14, s30, 31
	s_sub_i32 s16, s15, s33
	s_cmp_ge_u32 s15, s33
	s_cselect_b32 s15, s16, s15
	s_sub_i32 s16, s15, s33
	s_cmp_ge_u32 s15, s33
	s_cselect_b32 s15, s16, s15
	s_xor_b32 s15, s15, s14
	s_sub_i32 s14, s15, s14
	s_ashr_i32 s15, s14, 31
	s_and_b32 s29, s15, s72
	s_add_i32 s29, s29, s14
	s_cmpk_lt_i32 s29, 0x300
	s_cselect_b64 s[14:15], -1, 0
	s_cmpk_gt_i32 s29, 0x2ff
	s_cbranch_scc1 .LBB0_139
	s_mul_hi_i32 s16, s29, 0x2aaaaaab
	s_lshr_b32 s17, s16, 31
	s_ashr_i32 s16, s16, 3
	s_add_i32 s16, s16, s17
	s_mul_i32 s17, s16, 0xffffffd0
	s_add_i32 s17, s17, s29
	s_lshl_b32 s38, s17, 5
	s_ashr_i32 s39, s38, 31
	s_lshl_b32 s16, s16, 6
	v_lshrrev_b32_e32 v0, 3, v198
	s_lshl_b64 s[36:37], s[38:39], 2
	v_or_b32_e32 v4, s16, v0
	s_add_u32 s36, s42, s36
	v_lshlrev_b32_e32 v0, 4, v198
	s_addc_u32 s37, s43, s37
	v_and_b32_e32 v0, 0x70, v0
	v_lshl_add_u64 v[2:3], s[36:37], 0, v[0:1]
	s_mov_b64 s[36:37], 0x2048000
	v_lshl_add_u64 v[2:3], v[2:3], 0, s[36:37]
	v_mad_i64_i32 v[6:7], s[36:37], v4, s11, v[2:3]
	global_load_dwordx4 v[30:33], v[6:7], off nt
	s_cmp_lg_u64 s[40:41], 0
	s_cselect_b64 s[48:49], -1, 0
	s_cmp_eq_u64 s[40:41], 0
	v_ashrrev_i32_e32 v5, 31, v4
	v_or_b32_e32 v6, 8, v4
	s_cbranch_scc0 .LBB0_127
	s_getpc_b64 s[98:99]

.LBB0_129:
	v_mad_u64_u32 v[10:11], s[36:37], v6, s11, v[2:3]
	v_mov_b32_e32 v0, v11
	v_mad_u64_u32 v[6:7], s[36:37], v7, s11, v[0:1]
	v_mov_b32_e32 v11, v6
	v_or_b32_e32 v8, 16, v4
	v_mad_i64_i32 v[6:7], s[36:37], v8, s11, v[2:3]
	global_load_dwordx4 v[38:41], v[10:11], off nt
	global_load_dwordx4 v[34:37], v[6:7], off nt
	v_cndmask_b32_e64 v0, 0, 1, s[48:49]
	v_cmp_ne_u32_e64 s[36:37], 1, v0
	s_andn2_b64 vcc, exec, s[48:49]
	v_or_b32_e32 v6, 24, v4
	s_cbranch_vccz .LBB0_130
	s_getpc_b64 s[98:99]

.LBB0_132:
	v_mad_u64_u32 v[10:11], s[46:47], v6, s11, v[2:3]
	v_mov_b32_e32 v0, v11
	v_mad_u64_u32 v[6:7], s[46:47], v7, s11, v[0:1]
	v_mov_b32_e32 v11, v6
	v_or_b32_e32 v8, 32, v4
	v_mad_i64_i32 v[6:7], s[46:47], v8, s11, v[2:3]
	global_load_dwordx4 v[46:49], v[10:11], off nt
	global_load_dwordx4 v[42:45], v[6:7], off nt
	s_and_b64 vcc, exec, s[36:37]
	v_or_b32_e32 v6, 40, v4
	s_cbranch_vccz .LBB0_133
	s_getpc_b64 s[98:99]

.LBB0_135:
	v_mad_u64_u32 v[8:9], s[46:47], v6, s11, v[2:3]
	v_mov_b32_e32 v0, v9
	v_mad_u64_u32 v[6:7], s[46:47], v7, s11, v[0:1]
	v_mov_b32_e32 v9, v6
	v_or_b32_e32 v6, 48, v4
	v_mad_i64_i32 v[10:11], s[46:47], v6, s11, v[2:3]
	global_load_dwordx4 v[54:57], v[8:9], off nt
	global_load_dwordx4 v[50:53], v[10:11], off nt
	s_and_b64 vcc, exec, s[36:37]
	v_or_b32_e32 v4, 56, v4
	s_cbranch_vccz .LBB0_136
	s_getpc_b64 s[98:99]

.LBB0_138:
	v_mad_u64_u32 v[2:3], s[36:37], v4, s11, v[2:3]
	v_mov_b32_e32 v0, v3
	v_mad_u64_u32 v[4:5], s[36:37], v5, s11, v[0:1]
	v_mov_b32_e32 v3, v4
	global_load_dwordx4 v[58:61], v[2:3], off nt
	s_lshl_b64 s[36:37], s[38:39], 11
	s_add_u32 s29, s34, s36
	s_addc_u32 s31, s35, s37
	s_ashr_i32 s17, s16, 31
	s_lshl_b64 s[16:17], s[16:17], 1
	s_add_u32 s16, s29, s16
	s_addc_u32 s17, s31, s17

.LBB0_141:
	v_readlane_b32 s14, v252, 40
	s_sub_i32 s14, s30, s14
	s_ashr_i32 s15, s14, 31
	s_abs_i32 s14, s14
	s_mul_hi_u32 s29, s14, s27
	s_mul_i32 s29, s29, s33
	s_sub_i32 s14, s14, s29
	s_sub_i32 s29, s14, s33
	s_cmp_ge_u32 s14, s33
	s_cselect_b32 s14, s29, s14
	s_sub_i32 s29, s14, s33
	s_cmp_ge_u32 s14, s33
	s_cselect_b32 s14, s29, s14
	s_xor_b32 s14, s14, s15
	s_sub_i32 s14, s14, s15
	s_ashr_i32 s15, s14, 31
	s_and_b32 s29, s15, s72
	s_add_i32 s29, s29, s14
	s_cmpk_lt_i32 s29, 0x300
	s_cselect_b64 s[48:49], -1, 0
	s_cmpk_gt_i32 s29, 0x2ff
	s_cbranch_scc1 .LBB0_155
	s_mul_hi_i32 s14, s29, 0x2aaaaaab
	s_lshr_b32 s15, s14, 31
	s_ashr_i32 s14, s14, 3
	s_add_i32 s14, s14, s15
	s_mul_i32 s15, s14, 0xffffffd0
	s_add_i32 s15, s15, s29
	s_lshl_b32 s50, s15, 5
	s_ashr_i32 s51, s50, 31
	s_lshl_b32 s14, s14, 6
	v_lshrrev_b32_e32 v0, 3, v198
	s_lshl_b64 s[38:39], s[50:51], 2
	v_or_b32_e32 v64, s14, v0
	s_add_u32 s38, s42, s38
	v_lshlrev_b32_e32 v0, 4, v198
	s_addc_u32 s39, s43, s39
	v_and_b32_e32 v0, 0x70, v0
	v_lshl_add_u64 v[2:3], s[38:39], 0, v[0:1]
	s_mov_b64 s[38:39], 0x204b000
	v_lshl_add_u64 v[62:63], v[2:3], 0, s[38:39]
	v_mad_i64_i32 v[2:3], s[38:39], v64, s11, v[62:63]
	global_load_dwordx4 v[2:5], v[2:3], off nt
	s_cmp_lg_u64 s[40:41], 0
	s_cselect_b64 s[52:53], -1, 0
	s_cmp_eq_u64 s[40:41], 0
	v_ashrrev_i32_e32 v65, 31, v64
	v_or_b32_e32 v6, 8, v64
	s_cbranch_scc0 .LBB0_143
	s_getpc_b64 s[98:99]

.LBB0_145:
	v_mad_u64_u32 v[8:9], s[38:39], v6, s11, v[62:63]
	v_mov_b32_e32 v0, v9
	v_mad_u64_u32 v[6:7], s[38:39], v7, s11, v[0:1]
	v_or_b32_e32 v16, 16, v64
	v_mov_b32_e32 v9, v6
	v_mad_i64_i32 v[6:7], s[38:39], v16, s11, v[62:63]
	global_load_dwordx4 v[10:13], v[8:9], off nt
	s_nop 0
	global_load_dwordx4 v[6:9], v[6:7], off nt
	v_cndmask_b32_e64 v0, 0, 1, s[52:53]
	v_cmp_ne_u32_e64 s[38:39], 1, v0
	s_andn2_b64 vcc, exec, s[52:53]
	v_or_b32_e32 v14, 24, v64
	s_cbranch_vccz .LBB0_146
	s_getpc_b64 s[98:99]

.LBB0_148:
	v_mad_u64_u32 v[16:17], s[46:47], v14, s11, v[62:63]
	v_mov_b32_e32 v0, v17
	v_mad_u64_u32 v[14:15], s[46:47], v15, s11, v[0:1]
	v_or_b32_e32 v24, 32, v64
	v_mov_b32_e32 v17, v14
	v_mad_i64_i32 v[14:15], s[46:47], v24, s11, v[62:63]
	global_load_dwordx4 v[18:21], v[16:17], off nt
	s_nop 0
	global_load_dwordx4 v[14:17], v[14:15], off nt
	s_and_b64 vcc, exec, s[38:39]
	v_or_b32_e32 v22, 40, v64
	s_cbranch_vccz .LBB0_149
	s_getpc_b64 s[98:99]

.LBB0_151:
	v_mad_u64_u32 v[24:25], s[46:47], v22, s11, v[62:63]
	v_mov_b32_e32 v0, v25
	v_mad_u64_u32 v[22:23], s[46:47], v23, s11, v[0:1]
	v_or_b32_e32 v94, 48, v64
	v_mov_b32_e32 v25, v22
	v_mad_i64_i32 v[22:23], s[46:47], v94, s11, v[62:63]
	global_load_dwordx4 v[26:29], v[24:25], off nt
	s_nop 0
	global_load_dwordx4 v[22:25], v[22:23], off nt
	s_and_b64 vcc, exec, s[38:39]
	v_or_b32_e32 v64, 56, v64
	s_cbranch_vccz .LBB0_152
	s_getpc_b64 s[98:99]

.LBB0_154:
	v_mad_u64_u32 v[62:63], s[38:39], v64, s11, v[62:63]
	v_mov_b32_e32 v0, v63
	v_mad_u64_u32 v[64:65], s[38:39], v65, s11, v[0:1]
	v_mov_b32_e32 v63, v64
	global_load_dwordx4 v[62:65], v[62:63], off nt
	s_lshl_b64 s[38:39], s[50:51], 11
	s_add_u32 s29, s34, s38
	s_addc_u32 s38, s35, s39
	s_ashr_i32 s15, s14, 31
	s_lshl_b64 s[14:15], s[14:15], 1
	s_add_u32 s14, s29, s14
	s_addc_u32 s15, s38, s15
	s_add_u32 s14, s14, 0x300000
	s_addc_u32 s15, s15, 0

.LBB0_160:
	v_readlane_b32 s16, v252, 41
	s_sub_i32 s16, s30, s16
	s_ashr_i32 s17, s16, 31
	s_abs_i32 s16, s16
	s_mul_hi_u32 s29, s16, s27
	s_mul_i32 s29, s29, s33
	s_sub_i32 s16, s16, s29
	s_sub_i32 s29, s16, s33
	s_cmp_ge_u32 s16, s33
	s_cselect_b32 s16, s29, s16
	s_sub_i32 s29, s16, s33
	s_cmp_ge_u32 s16, s33
	s_cselect_b32 s16, s29, s16
	s_xor_b32 s16, s16, s17
	s_sub_i32 s16, s16, s17
	s_ashr_i32 s17, s16, 31
	s_and_b32 s29, s17, s72
	s_add_i32 s29, s29, s16
	s_cmpk_lt_i32 s29, 0x100
	s_cselect_b64 s[38:39], -1, 0
	s_cmpk_gt_i32 s29, 0xff
	s_cbranch_scc1 .LBB0_174
	s_ashr_i32 s16, s29, 31
	s_lshr_b32 s16, s16, 28
	s_add_i32 s16, s29, s16
	s_ashr_i32 s17, s16, 4
	s_lshl_b32 s16, s17, 6
	s_lshl_b32 s17, s17, 9
	s_lshl_b32 s29, s29, 5
	s_sub_i32 s48, s29, s17
	s_ashr_i32 s49, s48, 31
	v_lshrrev_b32_e32 v0, 3, v198
	s_lshl_b64 s[36:37], s[48:49], 2
	s_waitcnt vmcnt(7)
	v_or_b32_e32 v32, s16, v0
	s_add_u32 s36, s42, s36
	v_lshlrev_b32_e32 v0, 4, v198
	s_addc_u32 s37, s43, s37
	v_and_b32_e32 v0, 0x70, v0
	v_lshl_add_u64 v[30:31], s[36:37], 0, v[0:1]
	s_mov_b64 s[36:37], 0x204c800
	v_lshl_add_u64 v[30:31], v[30:31], 0, s[36:37]
	s_waitcnt vmcnt(5)
	v_mad_i64_i32 v[34:35], s[36:37], v32, s11, v[30:31]
	global_load_dwordx4 v[34:37], v[34:35], off nt
	s_cmp_lg_u64 s[40:41], 0
	s_cselect_b64 s[50:51], -1, 0
	s_cmp_eq_u64 s[40:41], 0
	v_ashrrev_i32_e32 v33, 31, v32
	v_or_b32_e32 v38, 8, v32
	s_cbranch_scc0 .LBB0_162
	s_getpc_b64 s[98:99]

.LBB0_164:
	v_mad_u64_u32 v[40:41], s[36:37], v38, s11, v[30:31]
	v_mov_b32_e32 v0, v41
	v_mad_u64_u32 v[38:39], s[36:37], v39, s11, v[0:1]
	s_waitcnt vmcnt(5)
	v_or_b32_e32 v48, 16, v32
	v_mov_b32_e32 v41, v38
	v_mad_i64_i32 v[38:39], s[36:37], v48, s11, v[30:31]
	global_load_dwordx4 v[42:45], v[40:41], off nt
	s_nop 0
	global_load_dwordx4 v[38:41], v[38:39], off nt
	v_cndmask_b32_e64 v0, 0, 1, s[50:51]
	v_cmp_ne_u32_e64 s[36:37], 1, v0
	s_andn2_b64 vcc, exec, s[50:51]
	v_or_b32_e32 v46, 24, v32
	s_cbranch_vccz .LBB0_165
	s_getpc_b64 s[98:99]

.LBB0_167:
	v_mad_u64_u32 v[48:49], s[46:47], v46, s11, v[30:31]
	v_mov_b32_e32 v0, v49
	v_mad_u64_u32 v[46:47], s[46:47], v47, s11, v[0:1]
	s_waitcnt vmcnt(5)
	v_or_b32_e32 v56, 32, v32
	v_mov_b32_e32 v49, v46
	v_mad_i64_i32 v[46:47], s[46:47], v56, s11, v[30:31]
	global_load_dwordx4 v[50:53], v[48:49], off nt
	s_nop 0
	global_load_dwordx4 v[46:49], v[46:47], off nt
	s_and_b64 vcc, exec, s[36:37]
	v_or_b32_e32 v54, 40, v32
	s_cbranch_vccz .LBB0_168
	s_getpc_b64 s[98:99]

.LBB0_170:
	v_mad_u64_u32 v[56:57], s[46:47], v54, s11, v[30:31]
	v_mov_b32_e32 v0, v57
	v_mad_u64_u32 v[54:55], s[46:47], v55, s11, v[0:1]
	v_or_b32_e32 v66, 48, v32
	v_mov_b32_e32 v57, v54
	v_mad_i64_i32 v[54:55], s[46:47], v66, s11, v[30:31]
	global_load_dwordx4 v[58:61], v[56:57], off nt
	s_nop 0
	global_load_dwordx4 v[54:57], v[54:55], off nt
	s_and_b64 vcc, exec, s[36:37]
	v_or_b32_e32 v32, 56, v32
	s_cbranch_vccz .LBB0_171
	s_getpc_b64 s[98:99]

.LBB0_173:
	v_mad_u64_u32 v[30:31], s[36:37], v32, s11, v[30:31]
	v_mov_b32_e32 v0, v31
	v_mad_u64_u32 v[32:33], s[36:37], v33, s11, v[0:1]
	v_mov_b32_e32 v31, v32
	global_load_dwordx4 v[66:69], v[30:31], off nt
	s_lshl_b64 s[36:37], s[48:49], 11
	s_add_u32 s29, s34, s36
	s_addc_u32 s36, s35, s37
	s_ashr_i32 s17, s16, 31
	s_lshl_b64 s[16:17], s[16:17], 1
	s_add_u32 s16, s29, s16
	s_addc_u32 s17, s36, s17
	s_add_u32 s16, s16, 0x600000
	s_addc_u32 s17, s17, 0

.LBB0_179:
	v_readlane_b32 s14, v252, 42
	s_sub_i32 s14, s30, s14
	s_ashr_i32 s15, s14, 31
	s_abs_i32 s14, s14
	s_mul_hi_u32 s29, s14, s27
	s_mul_i32 s29, s29, s33
	s_sub_i32 s14, s14, s29
	s_sub_i32 s29, s14, s33
	s_cmp_ge_u32 s14, s33
	s_cselect_b32 s14, s29, s14
	s_sub_i32 s29, s14, s33
	s_cmp_ge_u32 s14, s33
	s_cselect_b32 s14, s29, s14
	s_xor_b32 s14, s14, s15
	s_sub_i32 s14, s14, s15
	s_ashr_i32 s15, s14, 31
	s_and_b32 s29, s15, s72
	s_add_i32 s29, s29, s14
	s_cmpk_lt_i32 s29, 0x100
	s_cselect_b64 s[38:39], -1, 0
	s_cmpk_gt_i32 s29, 0xff
	s_cbranch_scc1 .LBB0_193
	s_ashr_i32 s14, s29, 31
	s_lshr_b32 s14, s14, 28
	s_add_i32 s14, s29, s14
	s_ashr_i32 s15, s14, 4
	s_lshl_b32 s14, s15, 6
	s_lshl_b32 s15, s15, 9
	s_lshl_b32 s29, s29, 5
	s_sub_i32 s48, s29, s15
	s_ashr_i32 s49, s48, 31
	v_lshrrev_b32_e32 v0, 3, v198
	s_lshl_b64 s[36:37], s[48:49], 2
	s_waitcnt vmcnt(7)
	v_or_b32_e32 v32, s14, v0
	s_add_u32 s36, s42, s36
	v_lshlrev_b32_e32 v0, 4, v198
	s_addc_u32 s37, s43, s37
	v_and_b32_e32 v0, 0x70, v0
	v_lshl_add_u64 v[2:3], s[36:37], 0, v[0:1]
	s_mov_b64 s[36:37], 0x2049800
	v_lshl_add_u64 v[30:31], v[2:3], 0, s[36:37]
	v_mad_i64_i32 v[2:3], s[36:37], v32, s11, v[30:31]
	global_load_dwordx4 v[2:5], v[2:3], off nt
	s_cmp_lg_u64 s[40:41], 0
	s_cselect_b64 s[50:51], -1, 0
	s_cmp_eq_u64 s[40:41], 0
	v_ashrrev_i32_e32 v33, 31, v32
	s_waitcnt vmcnt(6)
	v_or_b32_e32 v6, 8, v32
	s_cbranch_scc0 .LBB0_181
	s_getpc_b64 s[98:99]

.LBB0_183:
	v_mad_u64_u32 v[8:9], s[36:37], v6, s11, v[30:31]
	v_mov_b32_e32 v0, v9
	v_mad_u64_u32 v[6:7], s[36:37], v7, s11, v[0:1]
	s_waitcnt vmcnt(4)
	v_or_b32_e32 v16, 16, v32
	v_mov_b32_e32 v9, v6
	v_mad_i64_i32 v[6:7], s[36:37], v16, s11, v[30:31]
	global_load_dwordx4 v[10:13], v[8:9], off nt
	s_nop 0
	global_load_dwordx4 v[6:9], v[6:7], off nt
	v_cndmask_b32_e64 v0, 0, 1, s[50:51]
	v_cmp_ne_u32_e64 s[36:37], 1, v0
	s_andn2_b64 vcc, exec, s[50:51]
	v_or_b32_e32 v14, 24, v32
	s_cbranch_vccz .LBB0_184
	s_getpc_b64 s[98:99]

.LBB0_186:
	v_mad_u64_u32 v[16:17], s[46:47], v14, s11, v[30:31]
	v_mov_b32_e32 v0, v17
	v_mad_u64_u32 v[14:15], s[46:47], v15, s11, v[0:1]
	v_or_b32_e32 v20, 32, v32
	v_mov_b32_e32 v17, v14
	v_mad_i64_i32 v[14:15], s[46:47], v20, s11, v[30:31]
	global_load_dwordx4 v[22:25], v[16:17], off nt
	s_nop 0
	global_load_dwordx4 v[14:17], v[14:15], off nt
	s_and_b64 vcc, exec, s[36:37]
	v_or_b32_e32 v18, 40, v32
	s_cbranch_vccz .LBB0_187
	s_getpc_b64 s[98:99]

.LBB0_189:
	v_mad_u64_u32 v[20:21], s[46:47], v18, s11, v[30:31]
	v_mov_b32_e32 v0, v21
	v_mad_u64_u32 v[18:19], s[46:47], v19, s11, v[0:1]
	s_waitcnt vmcnt(5)
	v_or_b32_e32 v62, 48, v32
	v_mov_b32_e32 v21, v18
	v_mad_i64_i32 v[18:19], s[46:47], v62, s11, v[30:31]
	global_load_dwordx4 v[26:29], v[20:21], off nt
	s_nop 0
	global_load_dwordx4 v[18:21], v[18:19], off nt
	s_and_b64 vcc, exec, s[36:37]
	v_or_b32_e32 v32, 56, v32
	s_cbranch_vccz .LBB0_190
	s_getpc_b64 s[98:99]

.LBB0_192:
	v_mad_u64_u32 v[30:31], s[36:37], v32, s11, v[30:31]
	v_mov_b32_e32 v0, v31
	v_mad_u64_u32 v[32:33], s[36:37], v33, s11, v[0:1]
	v_mov_b32_e32 v31, v32
	global_load_dwordx4 v[30:33], v[30:31], off nt
	s_lshl_b64 s[36:37], s[48:49], 11
	s_add_u32 s29, s34, s36
	s_addc_u32 s36, s35, s37
	s_ashr_i32 s15, s14, 31
	s_lshl_b64 s[14:15], s[14:15], 1
	s_add_u32 s14, s29, s14
	s_addc_u32 s15, s36, s15
	s_add_u32 s14, s14, 0x700000
	s_addc_u32 s15, s15, 0

.LBB0_201:
	s_sub_i32 s29, s30, s59
	s_ashr_i32 s36, s29, 31
	s_abs_i32 s29, s29
	s_mul_hi_u32 s37, s29, s27
	s_mul_i32 s37, s37, s33
	s_sub_i32 s29, s29, s37
	s_sub_i32 s37, s29, s33
	s_cmp_ge_u32 s29, s33
	s_cselect_b32 s29, s37, s29
	s_sub_i32 s37, s29, s33
	s_cmp_ge_u32 s29, s33
	s_cselect_b32 s29, s37, s29
	s_xor_b32 s29, s29, s36
	s_sub_i32 s29, s29, s36
	s_ashr_i32 s36, s29, 31
	s_and_b32 s36, s36, s72
	s_add_i32 s29, s36, s29
	s_cmp_lt_i32 s29, 64
	s_cselect_b64 s[50:51], -1, 0
	s_cmp_gt_i32 s29, 63
	s_cbranch_scc1 .LBB0_215
	s_ashr_i32 s36, s29, 31
	s_lshr_b32 s36, s36, 30
	s_add_i32 s36, s29, s36
	s_ashr_i32 s36, s36, 2
	s_lshl_b32 s48, s36, 6
	s_lshl_b32 s36, s36, 7
	s_lshl_b32 s29, s29, 5
	s_sub_i32 s52, s29, s36
	s_ashr_i32 s53, s52, 31
	s_lshl_b64 s[54:55], s[52:53], 2
	s_add_u32 s36, s38, s54
	s_addc_u32 s37, s39, s55
	s_waitcnt vmcnt(0)
	v_or_b32_e32 v94, s48, v104
	v_mov_b64_e32 v[38:39], s[36:37]
	v_mad_i64_i32 v[38:39], s[36:37], v94, s11, v[38:39]
	v_lshl_add_u64 v[38:39], v[134:135], 0, v[38:39]
	v_add_co_u32_e32 v38, vcc, 0x204a000, v38
	v_cndmask_b32_e64 v0, 0, 1, s[16:17]
	s_nop 0
	v_addc_co_u32_e32 v39, vcc, 0, v39, vcc
	global_load_dwordx4 v[38:41], v[38:39], off nt
	v_ashrrev_i32_e32 v95, 31, v94
	v_cmp_ne_u32_e64 s[36:37], 1, v0
	s_andn2_b64 vcc, exec, s[16:17]
	v_or_b32_e32 v50, 8, v94
	s_cbranch_vccnz .LBB0_236
	v_lshl_add_u64 v[52:53], v[94:95], 2, s[0:1]
	v_ashrrev_i32_e32 v51, 31, v50
	global_load_dword v107, v[52:53], off
	v_lshl_add_u64 v[52:53], v[50:51], 2, s[0:1]
	global_load_dword v119, v[52:53], off
	s_cbranch_execnz .LBB0_205

.LBB0_205:
	s_add_u32 s46, s38, s54
	s_addc_u32 s47, s39, s55
	v_mov_b64_e32 v[52:53], s[46:47]
	v_mad_u64_u32 v[54:55], s[46:47], v50, s11, v[52:53]
	v_mov_b32_e32 v0, v55
	v_mad_u64_u32 v[50:51], s[46:47], v51, s11, v[0:1]
	v_mov_b32_e32 v55, v50
	v_lshl_add_u64 v[50:51], v[134:135], 0, v[54:55]
	s_waitcnt vmcnt(1)
	v_or_b32_e32 v68, 16, v94
	v_add_co_u32_e32 v50, vcc, 0x204a000, v50
	v_mad_i64_i32 v[52:53], s[46:47], v68, s11, v[52:53]
	s_nop 0
	v_addc_co_u32_e32 v51, vcc, 0, v51, vcc
	v_lshl_add_u64 v[52:53], v[134:135], 0, v[52:53]
	v_add_co_u32_e32 v54, vcc, 0x204a000, v52
	v_or_b32_e32 v66, 24, v94
	s_nop 0
	v_addc_co_u32_e32 v55, vcc, 0, v53, vcc
	global_load_dwordx4 v[50:53], v[50:51], off nt
	s_nop 0
	global_load_dwordx4 v[54:57], v[54:55], off nt
	s_and_b64 vcc, exec, s[36:37]
	s_cbranch_vccnz .LBB0_237
	v_ashrrev_i32_e32 v69, 31, v68
	v_lshl_add_u64 v[68:69], v[68:69], 2, s[0:1]
	v_ashrrev_i32_e32 v67, 31, v66
	global_load_dword v125, v[68:69], off
	v_lshl_add_u64 v[68:69], v[66:67], 2, s[0:1]
	global_load_dword v127, v[68:69], off
	s_cbranch_execnz .LBB0_208

.LBB0_208:
	s_add_u32 s46, s38, s54
	s_addc_u32 s47, s39, s55
	v_mov_b64_e32 v[68:69], s[46:47]
	v_mad_u64_u32 v[70:71], s[46:47], v66, s11, v[68:69]
	v_mov_b32_e32 v0, v71
	v_mad_u64_u32 v[66:67], s[46:47], v67, s11, v[0:1]
	v_mov_b32_e32 v71, v66
	v_lshl_add_u64 v[66:67], v[134:135], 0, v[70:71]
	v_or_b32_e32 v84, 32, v94
	v_add_co_u32_e32 v66, vcc, 0x204a000, v66
	v_mad_i64_i32 v[68:69], s[46:47], v84, s11, v[68:69]
	s_nop 0
	v_addc_co_u32_e32 v67, vcc, 0, v67, vcc
	v_lshl_add_u64 v[68:69], v[134:135], 0, v[68:69]
	v_add_co_u32_e32 v70, vcc, 0x204a000, v68
	v_or_b32_e32 v82, 40, v94
	s_nop 0
	v_addc_co_u32_e32 v71, vcc, 0, v69, vcc
	global_load_dwordx4 v[66:69], v[66:67], off nt
	s_nop 0
	global_load_dwordx4 v[70:73], v[70:71], off nt
	s_and_b64 vcc, exec, s[36:37]
	s_cbranch_vccnz .LBB0_238
	v_ashrrev_i32_e32 v85, 31, v84
	v_lshl_add_u64 v[84:85], v[84:85], 2, s[0:1]
	v_ashrrev_i32_e32 v83, 31, v82
	global_load_dword v133, v[84:85], off
	v_lshl_add_u64 v[84:85], v[82:83], 2, s[0:1]
	global_load_dword v136, v[84:85], off
	s_cbranch_execnz .LBB0_211

.LBB0_211:
	s_add_u32 s46, s38, s54
	s_addc_u32 s47, s39, s55
	v_mov_b64_e32 v[84:85], s[46:47]
	v_mad_u64_u32 v[86:87], s[46:47], v82, s11, v[84:85]
	v_mov_b32_e32 v0, v87
	v_mad_u64_u32 v[82:83], s[46:47], v83, s11, v[0:1]
	v_mov_b32_e32 v87, v82
	v_lshl_add_u64 v[82:83], v[134:135], 0, v[86:87]
	v_or_b32_e32 v96, 48, v94
	v_add_co_u32_e32 v82, vcc, 0x204a000, v82
	v_mad_i64_i32 v[84:85], s[46:47], v96, s11, v[84:85]
	s_nop 0
	v_addc_co_u32_e32 v83, vcc, 0, v83, vcc
	v_lshl_add_u64 v[84:85], v[134:135], 0, v[84:85]
	v_add_co_u32_e32 v86, vcc, 0x204a000, v84
	v_or_b32_e32 v94, 56, v94
	s_nop 0
	v_addc_co_u32_e32 v87, vcc, 0, v85, vcc
	global_load_dwordx4 v[82:85], v[82:83], off nt
	s_nop 0
	global_load_dwordx4 v[86:89], v[86:87], off nt
	s_and_b64 vcc, exec, s[36:37]
	s_cbranch_vccnz .LBB0_239
	v_ashrrev_i32_e32 v97, 31, v96
	v_lshl_add_u64 v[96:97], v[96:97], 2, s[0:1]
	v_ashrrev_i32_e32 v95, 31, v94
	global_load_dword v139, v[96:97], off
	v_lshl_add_u64 v[96:97], v[94:95], 2, s[0:1]
	global_load_dword v140, v[96:97], off
	s_cbranch_execnz .LBB0_214

.LBB0_214:
	s_add_u32 s36, s38, s54
	s_addc_u32 s37, s39, s55
	v_mov_b64_e32 v[96:97], s[36:37]
	v_mad_u64_u32 v[96:97], s[36:37], v94, s11, v[96:97]
	v_mov_b32_e32 v0, v97
	v_mad_u64_u32 v[94:95], s[36:37], v95, s11, v[0:1]
	v_mov_b32_e32 v97, v94
	v_lshl_add_u64 v[94:95], v[134:135], 0, v[96:97]
	s_mov_b32 s29, 0x204a000
	v_add_co_u32_e32 v94, vcc, s29, v94
	s_add_i32 s29, s58, s52
	s_nop 0
	v_addc_co_u32_e32 v95, vcc, 0, v95, vcc
	global_load_dwordx4 v[94:97], v[94:95], off nt
	s_add_i32 s36, s29, 0xffffff80
	s_ashr_i32 s37, s36, 31
	s_lshl_b64 s[36:37], s[36:37], 11
	s_add_u32 s29, s34, s36
	s_addc_u32 s46, s35, s37
	s_ashr_i32 s49, s48, 31
	s_lshl_b64 s[36:37], s[48:49], 1
	s_add_u32 s48, s29, s36
	s_addc_u32 s49, s46, s37

.LBB0_219:
	s_add_i32 s29, s59, 64
	s_ashr_i32 s36, s29, 31
	s_abs_i32 s29, s29
	s_mul_hi_u32 s37, s29, s27
	s_mul_i32 s37, s37, s33
	s_sub_i32 s29, s29, s37
	s_sub_i32 s37, s29, s33
	s_cmp_ge_u32 s29, s33
	s_cselect_b32 s29, s37, s29
	s_sub_i32 s37, s29, s33
	s_cmp_ge_u32 s29, s33
	s_cselect_b32 s29, s37, s29
	s_xor_b32 s29, s29, s36
	s_sub_i32 s29, s29, s36
	s_sub_i32 s36, s30, s29
	s_ashr_i32 s37, s36, 31
	s_abs_i32 s36, s36
	s_mul_hi_u32 s46, s36, s27
	s_mul_i32 s46, s46, s33
	s_sub_i32 s36, s36, s46
	s_sub_i32 s46, s36, s33
	s_cmp_ge_u32 s36, s33
	s_cselect_b32 s36, s46, s36
	s_sub_i32 s46, s36, s33
	s_cmp_ge_u32 s36, s33
	s_cselect_b32 s36, s46, s36
	s_xor_b32 s36, s36, s37
	s_sub_i32 s36, s36, s37
	s_ashr_i32 s37, s36, 31
	s_and_b32 s37, s37, s72
	s_add_i32 s36, s37, s36
	s_cmp_lt_i32 s36, 64
	s_cselect_b64 s[50:51], -1, 0
	s_cmp_gt_i32 s36, 63
	s_cbranch_scc1 .LBB0_233
	s_ashr_i32 s37, s36, 31
	s_lshr_b32 s37, s37, 30
	s_add_i32 s37, s36, s37
	s_ashr_i32 s37, s37, 2
	s_lshl_b32 s40, s37, 6
	s_lshl_b32 s37, s37, 7
	s_lshl_b32 s36, s36, 5
	s_sub_i32 s52, s36, s37
	s_ashr_i32 s53, s52, 31
	s_lshl_b64 s[54:55], s[52:53], 2
	s_add_u32 s36, s38, s54
	s_addc_u32 s37, s39, s55
	s_waitcnt vmcnt(0)
	v_or_b32_e32 v90, s40, v104
	v_mov_b64_e32 v[34:35], s[36:37]
	v_mad_i64_i32 v[34:35], s[36:37], v90, s11, v[34:35]
	v_lshl_add_u64 v[34:35], v[134:135], 0, v[34:35]
	v_add_co_u32_e32 v34, vcc, 0x204a000, v34
	v_cndmask_b32_e64 v0, 0, 1, s[16:17]
	s_nop 0
	v_addc_co_u32_e32 v35, vcc, 0, v35, vcc
	global_load_dwordx4 v[34:37], v[34:35], off offset:2048 nt
	v_ashrrev_i32_e32 v91, 31, v90
	v_cmp_ne_u32_e64 s[36:37], 1, v0
	s_andn2_b64 vcc, exec, s[16:17]
	v_or_b32_e32 v42, 8, v90
	s_cbranch_vccnz .LBB0_240
	v_lshl_add_u64 v[44:45], v[90:91], 2, s[0:1]
	v_ashrrev_i32_e32 v43, 31, v42
	global_load_dword v103, v[44:45], off
	v_lshl_add_u64 v[44:45], v[42:43], 2, s[0:1]
	global_load_dword v105, v[44:45], off
	s_cbranch_execnz .LBB0_223

.LBB0_223:
	s_add_u32 s46, s38, s54
	s_addc_u32 s47, s39, s55
	v_mov_b64_e32 v[44:45], s[46:47]
	v_mad_u64_u32 v[46:47], s[46:47], v42, s11, v[44:45]
	v_mov_b32_e32 v0, v47
	v_mad_u64_u32 v[42:43], s[46:47], v43, s11, v[0:1]
	v_mov_b32_e32 v47, v42
	v_lshl_add_u64 v[42:43], v[134:135], 0, v[46:47]
	s_waitcnt vmcnt(1)
	v_or_b32_e32 v60, 16, v90
	v_add_co_u32_e32 v42, vcc, 0x204a000, v42
	v_mad_i64_i32 v[44:45], s[46:47], v60, s11, v[44:45]
	s_nop 0
	v_addc_co_u32_e32 v43, vcc, 0, v43, vcc
	v_lshl_add_u64 v[44:45], v[134:135], 0, v[44:45]
	v_add_co_u32_e32 v46, vcc, 0x204a000, v44
	v_or_b32_e32 v58, 24, v90
	s_nop 0
	v_addc_co_u32_e32 v47, vcc, 0, v45, vcc
	global_load_dwordx4 v[42:45], v[42:43], off offset:2048 nt
	s_nop 0
	global_load_dwordx4 v[46:49], v[46:47], off offset:2048 nt
	s_and_b64 vcc, exec, s[36:37]
	s_cbranch_vccnz .LBB0_241
	v_ashrrev_i32_e32 v61, 31, v60
	v_lshl_add_u64 v[60:61], v[60:61], 2, s[0:1]
	v_ashrrev_i32_e32 v59, 31, v58
	global_load_dword v121, v[60:61], off
	v_lshl_add_u64 v[60:61], v[58:59], 2, s[0:1]
	global_load_dword v123, v[60:61], off
	s_cbranch_execnz .LBB0_226

.LBB0_226:
	s_add_u32 s46, s38, s54
	s_addc_u32 s47, s39, s55
	v_mov_b64_e32 v[60:61], s[46:47]
	v_mad_u64_u32 v[62:63], s[46:47], v58, s11, v[60:61]
	v_mov_b32_e32 v0, v63
	v_mad_u64_u32 v[58:59], s[46:47], v59, s11, v[0:1]
	v_mov_b32_e32 v63, v58
	v_lshl_add_u64 v[58:59], v[134:135], 0, v[62:63]
	v_or_b32_e32 v76, 32, v90
	v_add_co_u32_e32 v58, vcc, 0x204a000, v58
	v_mad_i64_i32 v[60:61], s[46:47], v76, s11, v[60:61]
	s_nop 0
	v_addc_co_u32_e32 v59, vcc, 0, v59, vcc
	v_lshl_add_u64 v[60:61], v[134:135], 0, v[60:61]
	v_add_co_u32_e32 v62, vcc, 0x204a000, v60
	v_or_b32_e32 v74, 40, v90
	s_nop 0
	v_addc_co_u32_e32 v63, vcc, 0, v61, vcc
	global_load_dwordx4 v[58:61], v[58:59], off offset:2048 nt
	s_nop 0
	global_load_dwordx4 v[62:65], v[62:63], off offset:2048 nt
	s_and_b64 vcc, exec, s[36:37]
	s_cbranch_vccnz .LBB0_242
	v_ashrrev_i32_e32 v77, 31, v76
	v_lshl_add_u64 v[76:77], v[76:77], 2, s[0:1]
	v_ashrrev_i32_e32 v75, 31, v74
	global_load_dword v129, v[76:77], off
	v_lshl_add_u64 v[76:77], v[74:75], 2, s[0:1]
	global_load_dword v131, v[76:77], off
	s_cbranch_execnz .LBB0_229

.LBB0_229:
	s_add_u32 s46, s38, s54
	s_addc_u32 s47, s39, s55
	v_mov_b64_e32 v[76:77], s[46:47]
	v_mad_u64_u32 v[78:79], s[46:47], v74, s11, v[76:77]
	v_mov_b32_e32 v0, v79
	v_mad_u64_u32 v[74:75], s[46:47], v75, s11, v[0:1]
	v_mov_b32_e32 v79, v74
	v_lshl_add_u64 v[74:75], v[134:135], 0, v[78:79]
	v_or_b32_e32 v92, 48, v90
	v_add_co_u32_e32 v74, vcc, 0x204a000, v74
	v_mad_i64_i32 v[76:77], s[46:47], v92, s11, v[76:77]
	s_nop 0
	v_addc_co_u32_e32 v75, vcc, 0, v75, vcc
	v_lshl_add_u64 v[76:77], v[134:135], 0, v[76:77]
	v_add_co_u32_e32 v78, vcc, 0x204a000, v76
	v_or_b32_e32 v90, 56, v90
	s_nop 0
	v_addc_co_u32_e32 v79, vcc, 0, v77, vcc
	global_load_dwordx4 v[74:77], v[74:75], off offset:2048 nt
	s_nop 0
	global_load_dwordx4 v[78:81], v[78:79], off offset:2048 nt
	s_and_b64 vcc, exec, s[36:37]
	s_cbranch_vccnz .LBB0_243
	v_ashrrev_i32_e32 v93, 31, v92
	v_lshl_add_u64 v[92:93], v[92:93], 2, s[0:1]
	v_ashrrev_i32_e32 v91, 31, v90
	global_load_dword v137, v[92:93], off
	v_lshl_add_u64 v[92:93], v[90:91], 2, s[0:1]
	global_load_dword v138, v[92:93], off
	s_cbranch_execnz .LBB0_232

.LBB0_232:
	s_add_u32 s36, s38, s54
	s_addc_u32 s37, s39, s55
	v_mov_b64_e32 v[92:93], s[36:37]
	v_mad_u64_u32 v[92:93], s[36:37], v90, s11, v[92:93]
	v_mov_b32_e32 v0, v93
	v_mad_u64_u32 v[90:91], s[36:37], v91, s11, v[0:1]
	v_mov_b32_e32 v93, v90
	v_lshl_add_u64 v[90:91], v[134:135], 0, v[92:93]
	s_mov_b32 s36, 0x204a000
	v_add_co_u32_e32 v90, vcc, s36, v90
	s_add_i32 s36, s58, s52
	s_nop 0
	v_addc_co_u32_e32 v91, vcc, 0, v91, vcc
	global_load_dwordx4 v[90:93], v[90:91], off offset:2048 nt
	s_ashr_i32 s37, s36, 31
	s_lshl_b64 s[36:37], s[36:37], 11
	s_add_u32 s46, s34, s36
	s_addc_u32 s47, s35, s37
	s_ashr_i32 s41, s40, 31
	s_lshl_b64 s[36:37], s[40:41], 1
	s_add_u32 s40, s46, s36
	s_addc_u32 s41, s47, s37

.LBB0_244:
	s_sub_i32 s29, s30, s59
	s_ashr_i32 s36, s29, 31
	s_abs_i32 s29, s29
	s_mul_hi_u32 s37, s29, s27
	s_mul_i32 s37, s37, s33
	s_sub_i32 s29, s29, s37
	s_sub_i32 s37, s29, s33
	s_cmp_ge_u32 s29, s33
	s_cselect_b32 s29, s37, s29
	s_sub_i32 s37, s29, s33
	s_cmp_ge_u32 s29, s33
	s_cselect_b32 s29, s37, s29
	s_xor_b32 s29, s29, s36
	s_sub_i32 s29, s29, s36
	s_ashr_i32 s36, s29, 31
	s_and_b32 s36, s36, s72
	v_lshlrev_b32_e32 v0, 2, v198
	s_add_i32 s29, s36, s29
	v_and_b32_e32 v0, 28, v0
	s_cmp_lt_i32 s29, 48
	s_waitcnt vmcnt(7)
	v_cndmask_b32_e64 v34, 0, 1, s[16:17]
	s_cselect_b64 s[38:39], -1, 0
	s_cmp_gt_i32 s29, 47
	v_lshlrev_b32_e32 v0, 2, v0
	v_cmp_ne_u32_e64 s[36:37], 1, v34
	s_cbranch_scc1 .LBB0_258
	s_mul_hi_i32 s16, s29, 0x55555556
	s_lshr_b32 s17, s16, 31
	s_add_i32 s16, s16, s17
	s_mul_i32 s17, s16, -3
	s_add_i32 s17, s17, s29
	s_lshl_b32 s40, s17, 5
	s_ashr_i32 s41, s40, 31
	s_lshl_b32 s16, s16, 6
	s_lshl_b64 s[46:47], s[40:41], 2
	s_add_u32 s46, s42, s46
	s_addc_u32 s47, s43, s47
	v_lshl_add_u64 v[34:35], s[46:47], 0, v[0:1]
	s_mov_b64 s[46:47], 0x204d000
	v_or_b32_e32 v36, s16, v104
	v_lshl_add_u64 v[34:35], v[34:35], 0, s[46:47]
	v_mad_i64_i32 v[38:39], s[46:47], v36, s11, v[34:35]
	global_load_dwordx4 v[58:61], v[38:39], off nt
	v_ashrrev_i32_e32 v37, 31, v36
	s_and_b64 vcc, exec, s[36:37]
	v_or_b32_e32 v38, 8, v36
	s_cbranch_vccz .LBB0_246
	s_getpc_b64 s[98:99]

.LBB0_248:
	s_waitcnt vmcnt(7)
	v_mad_u64_u32 v[42:43], s[46:47], v38, s11, v[34:35]
	v_mov_b32_e32 v38, v43
	v_mad_u64_u32 v[38:39], s[46:47], v39, s11, v[38:39]
	v_mov_b32_e32 v43, v38
	v_or_b32_e32 v40, 16, v36
	v_mad_i64_i32 v[38:39], s[46:47], v40, s11, v[34:35]
	global_load_dwordx4 v[74:77], v[42:43], off nt
	global_load_dwordx4 v[70:73], v[38:39], off nt
	s_and_b64 vcc, exec, s[36:37]
	v_or_b32_e32 v38, 24, v36
	s_cbranch_vccz .LBB0_249
	s_getpc_b64 s[98:99]

.LBB0_251:
	v_mad_u64_u32 v[42:43], s[46:47], v38, s11, v[34:35]
	v_mov_b32_e32 v38, v43
	v_mad_u64_u32 v[38:39], s[46:47], v39, s11, v[38:39]
	v_mov_b32_e32 v43, v38
	v_or_b32_e32 v40, 32, v36
	v_mad_i64_i32 v[38:39], s[46:47], v40, s11, v[34:35]
	global_load_dwordx4 v[82:85], v[42:43], off nt
	global_load_dwordx4 v[78:81], v[38:39], off nt
	s_and_b64 vcc, exec, s[36:37]
	v_or_b32_e32 v38, 40, v36
	s_cbranch_vccz .LBB0_252
	s_getpc_b64 s[98:99]

.LBB0_254:
	v_mad_u64_u32 v[40:41], s[46:47], v38, s11, v[34:35]
	v_mov_b32_e32 v38, v41
	v_mad_u64_u32 v[38:39], s[46:47], v39, s11, v[38:39]
	v_mov_b32_e32 v41, v38
	v_or_b32_e32 v38, 48, v36
	v_mad_i64_i32 v[42:43], s[46:47], v38, s11, v[34:35]
	global_load_dwordx4 v[90:93], v[40:41], off nt
	global_load_dwordx4 v[86:89], v[42:43], off nt
	s_and_b64 vcc, exec, s[36:37]
	v_or_b32_e32 v36, 56, v36
	s_cbranch_vccz .LBB0_255
	s_getpc_b64 s[98:99]

.LBB0_257:
	v_mad_u64_u32 v[34:35], s[46:47], v36, s11, v[34:35]
	v_mov_b32_e32 v36, v35
	v_mad_u64_u32 v[36:37], s[46:47], v37, s11, v[36:37]
	v_mov_b32_e32 v35, v36
	global_load_dwordx4 v[94:97], v[34:35], off nt
	s_lshl_b64 s[40:41], s[40:41], 11
	s_add_u32 s29, s34, s40
	s_addc_u32 s34, s35, s41
	s_ashr_i32 s17, s16, 31
	s_lshl_b64 s[16:17], s[16:17], 1
	s_add_u32 s16, s29, s16
	s_addc_u32 s17, s34, s17
	s_add_u32 s16, s16, 0xa00000
	s_addc_u32 s17, s17, 0

.LBB0_263:
	s_add_i32 s14, s59, 48
	s_ashr_i32 s15, s14, 31
	s_abs_i32 s14, s14
	s_mul_hi_u32 s29, s14, s27
	s_mul_i32 s29, s29, s33
	s_sub_i32 s14, s14, s29
	s_sub_i32 s29, s14, s33
	s_cmp_ge_u32 s14, s33
	s_cselect_b32 s14, s29, s14
	s_sub_i32 s29, s14, s33
	s_cmp_ge_u32 s14, s33
	s_cselect_b32 s14, s29, s14
	s_xor_b32 s14, s14, s15
	s_sub_i32 s29, s14, s15
	s_sub_i32 s14, s30, s29
	s_ashr_i32 s15, s14, 31
	s_abs_i32 s14, s14
	s_mul_hi_u32 s34, s14, s27
	s_mul_i32 s34, s34, s33
	s_sub_i32 s14, s14, s34
	s_sub_i32 s34, s14, s33
	s_cmp_ge_u32 s14, s33
	s_cselect_b32 s14, s34, s14
	s_sub_i32 s34, s14, s33
	s_cmp_ge_u32 s14, s33
	s_cselect_b32 s14, s34, s14
	s_xor_b32 s14, s14, s15
	s_sub_i32 s14, s14, s15
	s_ashr_i32 s15, s14, 31
	s_and_b32 s34, s15, s72
	s_add_i32 s34, s34, s14
	s_cmpk_lt_i32 s34, 0x600
	s_cselect_b64 s[38:39], -1, 0
	s_cmpk_gt_i32 s34, 0x5ff
	s_cbranch_scc1 .LBB0_277
	s_mul_hi_i32 s14, s34, 0x2aaaaaab
	s_lshr_b32 s15, s14, 31
	s_ashr_i32 s14, s14, 4
	s_add_i32 s14, s14, s15
	s_mul_i32 s15, s14, 0xffffffa0
	s_add_i32 s15, s15, s34
	s_lshl_b32 s40, s15, 5
	s_ashr_i32 s41, s40, 31
	s_lshl_b32 s14, s14, 6
	s_lshl_b64 s[34:35], s[40:41], 2
	s_add_u32 s34, s42, s34
	s_addc_u32 s35, s43, s35
	v_lshl_add_u64 v[2:3], s[34:35], 0, v[0:1]
	s_mov_b64 s[34:35], 0x204d120
	v_or_b32_e32 v4, s14, v104
	v_lshl_add_u64 v[2:3], v[2:3], 0, s[34:35]
	v_mad_i64_i32 v[6:7], s[34:35], v4, s11, v[2:3]
	global_load_dwordx4 v[34:37], v[6:7], off nt
	v_ashrrev_i32_e32 v5, 31, v4
	s_and_b64 vcc, exec, s[36:37]
	v_or_b32_e32 v6, 8, v4
	s_cbranch_vccz .LBB0_265
	s_getpc_b64 s[98:99]

.LBB0_267:
	v_mad_u64_u32 v[10:11], s[34:35], v6, s11, v[2:3]
	v_mov_b32_e32 v6, v11
	v_mad_u64_u32 v[6:7], s[34:35], v7, s11, v[6:7]
	v_mov_b32_e32 v11, v6
	v_or_b32_e32 v8, 16, v4
	v_mad_i64_i32 v[6:7], s[34:35], v8, s11, v[2:3]
	global_load_dwordx4 v[42:45], v[10:11], off nt
	global_load_dwordx4 v[38:41], v[6:7], off nt
	s_and_b64 vcc, exec, s[36:37]
	v_or_b32_e32 v6, 24, v4
	s_cbranch_vccz .LBB0_268
	s_getpc_b64 s[98:99]

.LBB0_270:
	v_mad_u64_u32 v[10:11], s[34:35], v6, s11, v[2:3]
	v_mov_b32_e32 v6, v11
	v_mad_u64_u32 v[6:7], s[34:35], v7, s11, v[6:7]
	v_mov_b32_e32 v11, v6
	v_or_b32_e32 v8, 32, v4
	v_mad_i64_i32 v[6:7], s[34:35], v8, s11, v[2:3]
	global_load_dwordx4 v[50:53], v[10:11], off nt
	global_load_dwordx4 v[46:49], v[6:7], off nt
	s_and_b64 vcc, exec, s[36:37]
	v_or_b32_e32 v6, 40, v4
	s_cbranch_vccz .LBB0_271
	s_getpc_b64 s[98:99]

.LBB0_273:
	v_mad_u64_u32 v[8:9], s[34:35], v6, s11, v[2:3]
	v_mov_b32_e32 v6, v9
	v_mad_u64_u32 v[6:7], s[34:35], v7, s11, v[6:7]
	v_mov_b32_e32 v9, v6
	v_or_b32_e32 v6, 48, v4
	v_mad_i64_i32 v[10:11], s[34:35], v6, s11, v[2:3]
	global_load_dwordx4 v[62:65], v[8:9], off nt
	global_load_dwordx4 v[54:57], v[10:11], off nt
	s_and_b64 vcc, exec, s[36:37]
	v_or_b32_e32 v4, 56, v4
	s_cbranch_vccz .LBB0_274
	s_getpc_b64 s[98:99]

.LBB0_276:
	v_mad_u64_u32 v[2:3], s[0:1], v4, s11, v[2:3]
	v_mov_b32_e32 v4, v3
	v_mad_u64_u32 v[4:5], s[0:1], v5, s11, v[4:5]
	v_mov_b32_e32 v3, v4
	global_load_dwordx4 v[66:69], v[2:3], off nt
	s_lshl_b64 s[0:1], s[40:41], 11
	s_add_u32 s34, s74, s0
	s_addc_u32 s35, s75, s1
	s_ashr_i32 s15, s14, 31
	s_lshl_b64 s[0:1], s[14:15], 1
	s_add_u32 s0, s34, s0
	s_addc_u32 s1, s35, s1
	s_add_u32 s14, s0, 0x4700000
	s_addc_u32 s15, s1, 0

.LBB0_285:
	s_sub_i32 s36, s30, s29
	s_ashr_i32 s37, s36, 31
	s_abs_i32 s36, s36
	s_mul_hi_u32 s41, s36, s27
	s_mul_i32 s41, s41, s33
	s_sub_i32 s36, s36, s41
	s_sub_i32 s41, s36, s33
	s_cmp_ge_u32 s36, s33
	s_cselect_b32 s36, s41, s36
	s_sub_i32 s41, s36, s33
	s_cmp_ge_u32 s36, s33
	s_cselect_b32 s36, s41, s36
	s_xor_b32 s36, s36, s37
	s_sub_i32 s36, s36, s37
	s_ashr_i32 s37, s36, 31
	s_and_b32 s41, s37, s72
	s_add_i32 s41, s41, s36
	s_cmpk_lt_i32 s41, 0x100
	s_cselect_b64 s[36:37], -1, 0
	s_cmpk_gt_i32 s41, 0xff
	s_cbranch_scc1 .LBB0_287
	s_add_u32 s16, s39, s0
	s_addc_u32 s17, s40, s1
	s_ashr_i32 s42, s41, 31
	s_lshr_b32 s42, s42, 27
	s_add_i32 s42, s41, s42
	s_load_dwordx2 s[16:17], s[16:17], 0x0
	s_ashr_i32 s43, s42, 5
	s_lshl_b32 s42, s43, 6
	s_lshl_b32 s43, s43, 10
	s_lshl_b32 s41, s41, 5
	s_sub_i32 s46, s41, s43
	s_ashr_i32 s47, s46, 31
	s_lshl_b64 s[48:49], s[46:47], 2
	s_waitcnt lgkmcnt(0)
	s_add_u32 s16, s16, s48
	s_waitcnt vmcnt(1)
	v_or_b32_e32 v26, s42, v104
	s_addc_u32 s17, s17, s49
	v_lshl_add_u64 v[2:3], s[16:17], 0, v[0:1]
	s_mov_b64 s[16:17], 0x200000
	v_ashrrev_i32_e32 v27, 31, v26
	v_lshl_add_u64 v[28:29], v[2:3], 0, s[16:17]
	v_lshlrev_b64 v[2:3], 12, v[26:27]
	v_or_b32_e32 v4, 8, v26
	v_or_b32_e32 v10, 16, v26
	v_or_b32_e32 v12, 24, v26
	v_or_b32_e32 v18, 32, v26
	v_or_b32_e32 v20, 40, v26
	s_waitcnt vmcnt(0)
	v_or_b32_e32 v30, 48, v26
	v_or_b32_e32 v26, 56, v26
	v_ashrrev_i32_e32 v5, 31, v4
	v_ashrrev_i32_e32 v11, 31, v10
	v_ashrrev_i32_e32 v13, 31, v12
	v_ashrrev_i32_e32 v19, 31, v18
	v_ashrrev_i32_e32 v21, 31, v20
	v_ashrrev_i32_e32 v31, 31, v30
	v_ashrrev_i32_e32 v27, 31, v26
	v_lshlrev_b64 v[4:5], 12, v[4:5]
	v_lshlrev_b64 v[10:11], 12, v[10:11]
	v_lshlrev_b64 v[12:13], 12, v[12:13]
	v_lshlrev_b64 v[18:19], 12, v[18:19]
	v_lshlrev_b64 v[20:21], 12, v[20:21]
	v_lshlrev_b64 v[30:31], 12, v[30:31]
	v_lshlrev_b64 v[26:27], 12, v[26:27]
	v_lshl_add_u64 v[2:3], v[28:29], 0, v[2:3]
	v_lshl_add_u64 v[6:7], v[28:29], 0, v[4:5]
	v_lshl_add_u64 v[10:11], v[28:29], 0, v[10:11]
	v_lshl_add_u64 v[14:15], v[28:29], 0, v[12:13]
	v_lshl_add_u64 v[18:19], v[28:29], 0, v[18:19]
	v_lshl_add_u64 v[22:23], v[28:29], 0, v[20:21]
	v_lshl_add_u64 v[30:31], v[28:29], 0, v[30:31]
	v_lshl_add_u64 v[32:33], v[28:29], 0, v[26:27]
	global_load_dwordx4 v[2:5], v[2:3], off nt
	s_nop 0
	global_load_dwordx4 v[6:9], v[6:7], off nt
	s_nop 0
	global_load_dwordx4 v[10:13], v[10:11], off nt
	s_nop 0
	global_load_dwordx4 v[14:17], v[14:15], off nt
	s_nop 0
	global_load_dwordx4 v[18:21], v[18:19], off nt
	s_nop 0
	global_load_dwordx4 v[22:25], v[22:23], off nt
	s_nop 0
	global_load_dwordx4 v[26:29], v[30:31], off nt
	s_nop 0
	global_load_dwordx4 v[30:33], v[32:33], off nt
	s_ashr_i32 s43, s42, 31
	s_lshl_b64 s[16:17], s[46:47], 10
	s_lshl_b64 s[42:43], s[42:43], 1
	s_add_u32 s16, s16, s42
	s_addc_u32 s17, s17, s43
	s_add_u32 s16, s35, s16
	s_addc_u32 s17, s38, s17

.LBB0_290:
	s_sub_i32 s0, s30, s29
	s_ashr_i32 s1, s0, 31
	s_abs_i32 s0, s0
	s_mul_hi_u32 s16, s0, s27
	s_mul_i32 s16, s16, s33
	s_sub_i32 s0, s0, s16
	s_sub_i32 s16, s0, s33
	s_cmp_ge_u32 s0, s33
	s_cselect_b32 s0, s16, s0
	s_sub_i32 s16, s0, s33
	s_cmp_ge_u32 s0, s33
	s_cselect_b32 s0, s16, s0
	s_xor_b32 s0, s0, s1
	s_sub_i32 s0, s0, s1
	s_ashr_i32 s1, s0, 31
	s_and_b32 s35, s1, s72
	s_add_i32 s35, s35, s0
	s_cmpk_lt_i32 s35, 0x200
	s_cselect_b64 s[16:17], -1, 0
	s_cmpk_gt_i32 s35, 0x1ff
	s_cbranch_scc1 .LBB0_292
	s_ashr_i32 s36, s35, 31
	s_lshr_b32 s36, s36, 27
	s_add_i32 s36, s35, s36
	s_load_dwordx2 s[0:1], s[44:45], 0x40
	s_ashr_i32 s37, s36, 5
	s_lshl_b32 s36, s37, 6
	s_lshl_b32 s37, s37, 10
	s_lshl_b32 s35, s35, 5
	s_sub_i32 s38, s35, s37
	s_ashr_i32 s39, s38, 31
	s_lshl_b64 s[40:41], s[38:39], 2
	s_waitcnt lgkmcnt(0)
	s_add_u32 s0, s0, s40
	s_waitcnt vmcnt(7)
	v_or_b32_e32 v2, s36, v104
	s_addc_u32 s1, s1, s41
	v_lshl_add_u64 v[4:5], s[0:1], 0, v[0:1]
	s_mov_b64 s[0:1], 0x400000
	v_ashrrev_i32_e32 v3, 31, v2
	s_waitcnt vmcnt(6)
	v_or_b32_e32 v8, 8, v2
	v_lshl_add_u64 v[4:5], v[4:5], 0, s[0:1]
	v_lshlrev_b64 v[6:7], 12, v[2:3]
	v_ashrrev_i32_e32 v9, 31, v8
	v_lshl_add_u64 v[6:7], v[4:5], 0, v[6:7]
	v_lshlrev_b64 v[8:9], 12, v[8:9]
	v_lshl_add_u64 v[8:9], v[4:5], 0, v[8:9]
	global_load_dwordx4 v[30:33], v[6:7], off nt
	global_load_dwordx4 v[26:29], v[8:9], off nt
	v_or_b32_e32 v6, 16, v2
	v_ashrrev_i32_e32 v7, 31, v6
	v_or_b32_e32 v8, 24, v2
	v_lshlrev_b64 v[6:7], 12, v[6:7]
	v_ashrrev_i32_e32 v9, 31, v8
	v_lshl_add_u64 v[6:7], v[4:5], 0, v[6:7]
	v_lshlrev_b64 v[8:9], 12, v[8:9]
	v_lshl_add_u64 v[8:9], v[4:5], 0, v[8:9]
	global_load_dwordx4 v[22:25], v[6:7], off nt
	global_load_dwordx4 v[18:21], v[8:9], off nt
	v_or_b32_e32 v6, 32, v2
	v_ashrrev_i32_e32 v7, 31, v6
	v_or_b32_e32 v8, 40, v2
	v_lshlrev_b64 v[6:7], 12, v[6:7]
	v_ashrrev_i32_e32 v9, 31, v8
	v_lshl_add_u64 v[6:7], v[4:5], 0, v[6:7]
	v_lshlrev_b64 v[8:9], 12, v[8:9]
	v_lshl_add_u64 v[8:9], v[4:5], 0, v[8:9]
	global_load_dwordx4 v[14:17], v[6:7], off nt
	global_load_dwordx4 v[10:13], v[8:9], off nt
	v_or_b32_e32 v6, 48, v2
	v_or_b32_e32 v2, 56, v2
	v_ashrrev_i32_e32 v7, 31, v6
	v_ashrrev_i32_e32 v3, 31, v2
	v_lshlrev_b64 v[6:7], 12, v[6:7]
	v_lshlrev_b64 v[2:3], 12, v[2:3]
	v_lshl_add_u64 v[6:7], v[4:5], 0, v[6:7]
	v_lshl_add_u64 v[2:3], v[4:5], 0, v[2:3]
	global_load_dwordx4 v[6:9], v[6:7], off nt
	s_nop 0
	global_load_dwordx4 v[2:5], v[2:3], off nt
	s_lshl_b64 s[0:1], s[38:39], 11
	s_add_u32 s35, s74, s0
	s_addc_u32 s38, s75, s1
	s_ashr_i32 s37, s36, 31
	s_lshl_b64 s[0:1], s[36:37], 1
	s_add_u32 s0, s35, s0
	s_addc_u32 s1, s38, s1
	s_add_u32 s0, s0, 0x4200000
	s_addc_u32 s1, s1, 0

.LBB0_300:
	s_ashr_i32 s36, s29, 31
	s_abs_i32 s29, s29
	s_mul_hi_u32 s37, s29, s27
	s_mul_i32 s37, s37, s33
	s_sub_i32 s29, s29, s37
	s_sub_i32 s37, s29, s33
	s_cmp_ge_u32 s29, s33
	s_cselect_b32 s29, s37, s29
	s_sub_i32 s37, s29, s33
	s_cmp_ge_u32 s29, s33
	s_cselect_b32 s29, s37, s29
	s_xor_b32 s29, s29, s36
	s_sub_i32 s29, s29, s36
	s_sub_i32 s36, s30, s29
	s_ashr_i32 s37, s36, 31
	s_abs_i32 s36, s36
	s_mul_hi_u32 s44, s36, s27
	s_mul_i32 s44, s44, s33
	s_sub_i32 s36, s36, s44
	s_sub_i32 s44, s36, s33
	s_cmp_ge_u32 s36, s33
	s_cselect_b32 s36, s44, s36
	s_sub_i32 s44, s36, s33
	s_cmp_ge_u32 s36, s33
	s_cselect_b32 s36, s44, s36
	s_xor_b32 s36, s36, s37
	s_sub_i32 s36, s36, s37
	s_ashr_i32 s37, s36, 31
	s_and_b32 s46, s37, s72
	s_add_i32 s46, s46, s36
	s_cmp_lt_i32 s46, 64
	v_cndmask_b32_e64 v0, 0, 1, s[38:39]
	s_cselect_b64 s[44:45], -1, 0
	s_cmp_gt_i32 s46, 63
	v_cmp_ne_u32_e64 s[36:37], 1, v0
	s_cbranch_scc1 .LBB0_314
	s_ashr_i32 s42, s46, 31
	s_lshr_b32 s42, s42, 30
	s_add_i32 s42, s46, s42
	s_ashr_i32 s43, s42, 2
	s_lshl_b32 s42, s43, 6
	s_lshl_b32 s43, s43, 7
	s_lshl_b32 s46, s46, 5
	s_sub_i32 s46, s46, s43
	s_ashr_i32 s47, s46, 31
	s_lshl_b64 s[48:49], s[46:47], 2
	s_add_u32 s50, s14, s48
	s_addc_u32 s51, s15, s49
	s_waitcnt vmcnt(0)
	v_or_b32_e32 v94, s42, v104
	v_mov_b64_e32 v[38:39], s[50:51]
	v_mad_i64_i32 v[38:39], s[50:51], v94, s3, v[38:39]
	v_lshl_add_u64 v[38:39], v[108:109], 0, v[38:39]
	v_add_co_u32_e32 v38, vcc, 0x1600000, v38
	v_ashrrev_i32_e32 v95, 31, v94
	s_nop 0
	v_addc_co_u32_e32 v39, vcc, 0, v39, vcc
	global_load_dwordx4 v[38:41], v[38:39], off nt
	s_and_b64 vcc, exec, s[36:37]
	v_or_b32_e32 v50, 8, v94
	s_cbranch_vccnz .LBB0_335
	v_lshl_add_u64 v[52:53], v[94:95], 2, s[16:17]
	v_ashrrev_i32_e32 v51, 31, v50
	global_load_dword v107, v[52:53], off
	v_lshl_add_u64 v[52:53], v[50:51], 2, s[16:17]
	global_load_dword v110, v[52:53], off
	s_cbranch_execnz .LBB0_304

.LBB0_304:
	s_add_u32 s50, s14, s48
	s_addc_u32 s51, s15, s49
	v_mov_b64_e32 v[52:53], s[50:51]
	v_mad_u64_u32 v[54:55], s[50:51], v50, s3, v[52:53]
	v_mov_b32_e32 v0, v55
	v_mad_u64_u32 v[50:51], s[50:51], v51, s3, v[0:1]
	v_mov_b32_e32 v55, v50
	v_lshl_add_u64 v[50:51], v[108:109], 0, v[54:55]
	v_or_b32_e32 v68, 16, v94
	v_add_co_u32_e32 v50, vcc, 0x1600000, v50
	v_mad_i64_i32 v[52:53], s[50:51], v68, s3, v[52:53]
	s_nop 0
	v_addc_co_u32_e32 v51, vcc, 0, v51, vcc
	v_lshl_add_u64 v[52:53], v[108:109], 0, v[52:53]
	v_add_co_u32_e32 v54, vcc, 0x1600000, v52
	v_or_b32_e32 v66, 24, v94
	s_nop 0
	v_addc_co_u32_e32 v55, vcc, 0, v53, vcc
	global_load_dwordx4 v[50:53], v[50:51], off nt
	s_nop 0
	global_load_dwordx4 v[54:57], v[54:55], off nt
	s_and_b64 vcc, exec, s[36:37]
	s_cbranch_vccnz .LBB0_336
	v_ashrrev_i32_e32 v69, 31, v68
	v_lshl_add_u64 v[68:69], v[68:69], 2, s[16:17]
	v_ashrrev_i32_e32 v67, 31, v66
	global_load_dword v113, v[68:69], off
	v_lshl_add_u64 v[68:69], v[66:67], 2, s[16:17]
	global_load_dword v114, v[68:69], off
	s_cbranch_execnz .LBB0_307

.LBB0_307:
	s_add_u32 s50, s14, s48
	s_addc_u32 s51, s15, s49
	v_mov_b64_e32 v[68:69], s[50:51]
	v_mad_u64_u32 v[70:71], s[50:51], v66, s3, v[68:69]
	v_mov_b32_e32 v0, v71
	v_mad_u64_u32 v[66:67], s[50:51], v67, s3, v[0:1]
	v_mov_b32_e32 v71, v66
	v_lshl_add_u64 v[66:67], v[108:109], 0, v[70:71]
	v_or_b32_e32 v84, 32, v94
	v_add_co_u32_e32 v66, vcc, 0x1600000, v66
	v_mad_i64_i32 v[68:69], s[50:51], v84, s3, v[68:69]
	s_nop 0
	v_addc_co_u32_e32 v67, vcc, 0, v67, vcc
	v_lshl_add_u64 v[68:69], v[108:109], 0, v[68:69]
	v_add_co_u32_e32 v70, vcc, 0x1600000, v68
	v_or_b32_e32 v82, 40, v94
	s_nop 0
	v_addc_co_u32_e32 v71, vcc, 0, v69, vcc
	global_load_dwordx4 v[66:69], v[66:67], off nt
	s_nop 0
	global_load_dwordx4 v[70:73], v[70:71], off nt
	s_and_b64 vcc, exec, s[36:37]
	s_cbranch_vccnz .LBB0_337
	v_ashrrev_i32_e32 v85, 31, v84
	v_lshl_add_u64 v[84:85], v[84:85], 2, s[16:17]
	v_ashrrev_i32_e32 v83, 31, v82
	global_load_dword v117, v[84:85], off
	v_lshl_add_u64 v[84:85], v[82:83], 2, s[16:17]
	global_load_dword v119, v[84:85], off
	s_cbranch_execnz .LBB0_310

.LBB0_310:
	s_add_u32 s50, s14, s48
	s_addc_u32 s51, s15, s49
	v_mov_b64_e32 v[84:85], s[50:51]
	v_mad_u64_u32 v[86:87], s[50:51], v82, s3, v[84:85]
	v_mov_b32_e32 v0, v87
	v_mad_u64_u32 v[82:83], s[50:51], v83, s3, v[0:1]
	v_mov_b32_e32 v87, v82
	v_lshl_add_u64 v[82:83], v[108:109], 0, v[86:87]
	v_or_b32_e32 v96, 48, v94
	v_add_co_u32_e32 v82, vcc, 0x1600000, v82
	v_mad_i64_i32 v[84:85], s[50:51], v96, s3, v[84:85]
	s_nop 0
	v_addc_co_u32_e32 v83, vcc, 0, v83, vcc
	v_lshl_add_u64 v[84:85], v[108:109], 0, v[84:85]
	v_add_co_u32_e32 v86, vcc, 0x1600000, v84
	v_or_b32_e32 v94, 56, v94
	s_nop 0
	v_addc_co_u32_e32 v87, vcc, 0, v85, vcc
	global_load_dwordx4 v[82:85], v[82:83], off nt
	s_nop 0
	global_load_dwordx4 v[86:89], v[86:87], off nt
	s_and_b64 vcc, exec, s[36:37]
	s_cbranch_vccnz .LBB0_338
	v_ashrrev_i32_e32 v97, 31, v96
	v_lshl_add_u64 v[96:97], v[96:97], 2, s[16:17]
	v_ashrrev_i32_e32 v95, 31, v94
	global_load_dword v125, v[96:97], off
	v_lshl_add_u64 v[96:97], v[94:95], 2, s[16:17]
	global_load_dword v127, v[96:97], off
	s_cbranch_execnz .LBB0_313

.LBB0_313:
	s_add_u32 s48, s14, s48
	s_addc_u32 s49, s15, s49
	v_mov_b64_e32 v[96:97], s[48:49]
	v_mad_u64_u32 v[96:97], s[48:49], v94, s3, v[96:97]
	v_mov_b32_e32 v0, v97
	v_mad_u64_u32 v[94:95], s[48:49], v95, s3, v[0:1]
	v_mov_b32_e32 v97, v94
	v_lshl_add_u64 v[94:95], v[108:109], 0, v[96:97]
	s_mov_b32 s43, 0x1600000
	v_add_co_u32_e32 v94, vcc, s43, v94
	s_add_i32 s43, s53, s46
	s_nop 0
	v_addc_co_u32_e32 v95, vcc, 0, v95, vcc
	global_load_dwordx4 v[94:97], v[94:95], off nt
	s_add_i32 s46, s43, 0xffffff80
	s_ashr_i32 s47, s46, 31
	s_lshl_b64 s[46:47], s[46:47], 11
	s_add_u32 s46, s35, s46
	s_addc_u32 s47, s52, s47
	s_ashr_i32 s43, s42, 31
	s_lshl_b64 s[42:43], s[42:43], 1
	s_add_u32 s42, s46, s42
	s_addc_u32 s43, s47, s43

.LBB0_318:
	s_add_i32 s29, s29, 64
	s_ashr_i32 s44, s29, 31
	s_abs_i32 s29, s29
	s_mul_hi_u32 s45, s29, s27
	s_mul_i32 s45, s45, s33
	s_sub_i32 s29, s29, s45
	s_sub_i32 s45, s29, s33
	s_cmp_ge_u32 s29, s33
	s_cselect_b32 s29, s45, s29
	s_sub_i32 s45, s29, s33
	s_cmp_ge_u32 s29, s33
	s_cselect_b32 s29, s45, s29
	s_xor_b32 s29, s29, s44
	s_sub_i32 s29, s29, s44
	s_sub_i32 s44, s30, s29
	s_ashr_i32 s45, s44, 31
	s_abs_i32 s44, s44
	s_mul_hi_u32 s46, s44, s27
	s_mul_i32 s46, s46, s33
	s_sub_i32 s44, s44, s46
	s_sub_i32 s46, s44, s33
	s_cmp_ge_u32 s44, s33
	s_cselect_b32 s44, s46, s44
	s_sub_i32 s46, s44, s33
	s_cmp_ge_u32 s44, s33
	s_cselect_b32 s44, s46, s44
	s_xor_b32 s44, s44, s45
	s_sub_i32 s44, s44, s45
	s_ashr_i32 s45, s44, 31
	s_and_b32 s46, s45, s72
	s_add_i32 s46, s46, s44
	s_cmp_lt_i32 s46, 64
	s_cselect_b64 s[44:45], -1, 0
	s_cmp_gt_i32 s46, 63
	s_cbranch_scc1 .LBB0_332
	s_ashr_i32 s40, s46, 31
	s_lshr_b32 s40, s40, 30
	s_add_i32 s40, s46, s40
	s_ashr_i32 s41, s40, 2
	s_lshl_b32 s40, s41, 6
	s_lshl_b32 s41, s41, 7
	s_lshl_b32 s46, s46, 5
	s_sub_i32 s46, s46, s41
	s_ashr_i32 s47, s46, 31
	s_lshl_b64 s[48:49], s[46:47], 2
	s_add_u32 s50, s14, s48
	s_addc_u32 s51, s15, s49
	s_waitcnt vmcnt(0)
	v_or_b32_e32 v90, s40, v104
	v_mov_b64_e32 v[34:35], s[50:51]
	v_mad_i64_i32 v[34:35], s[50:51], v90, s3, v[34:35]
	v_lshl_add_u64 v[34:35], v[108:109], 0, v[34:35]
	v_add_co_u32_e32 v34, vcc, 0x1602000, v34
	v_ashrrev_i32_e32 v91, 31, v90
	s_nop 0
	v_addc_co_u32_e32 v35, vcc, 0, v35, vcc
	global_load_dwordx4 v[34:37], v[34:35], off offset:3072 nt
	s_and_b64 vcc, exec, s[36:37]
	v_or_b32_e32 v42, 8, v90
	s_cbranch_vccnz .LBB0_339
	v_lshl_add_u64 v[44:45], v[90:91], 2, s[16:17]
	v_ashrrev_i32_e32 v43, 31, v42
	global_load_dword v103, v[44:45], off
	v_lshl_add_u64 v[44:45], v[42:43], 2, s[16:17]
	global_load_dword v105, v[44:45], off
	s_cbranch_execnz .LBB0_322

.LBB0_322:
	s_add_u32 s50, s14, s48
	s_addc_u32 s51, s15, s49
	v_mov_b64_e32 v[44:45], s[50:51]
	v_mad_u64_u32 v[46:47], s[50:51], v42, s3, v[44:45]
	v_mov_b32_e32 v0, v47
	v_mad_u64_u32 v[42:43], s[50:51], v43, s3, v[0:1]
	v_mov_b32_e32 v47, v42
	v_lshl_add_u64 v[42:43], v[108:109], 0, v[46:47]
	v_or_b32_e32 v60, 16, v90
	v_add_co_u32_e32 v42, vcc, 0x1602000, v42
	v_mad_i64_i32 v[44:45], s[50:51], v60, s3, v[44:45]
	s_nop 0
	v_addc_co_u32_e32 v43, vcc, 0, v43, vcc
	v_lshl_add_u64 v[44:45], v[108:109], 0, v[44:45]
	v_add_co_u32_e32 v46, vcc, 0x1602000, v44
	v_or_b32_e32 v58, 24, v90
	s_nop 0
	v_addc_co_u32_e32 v47, vcc, 0, v45, vcc
	global_load_dwordx4 v[42:45], v[42:43], off offset:3072 nt
	s_nop 0
	global_load_dwordx4 v[46:49], v[46:47], off offset:3072 nt
	s_and_b64 vcc, exec, s[36:37]
	s_cbranch_vccnz .LBB0_340
	v_ashrrev_i32_e32 v61, 31, v60
	v_lshl_add_u64 v[60:61], v[60:61], 2, s[16:17]
	v_ashrrev_i32_e32 v59, 31, v58
	global_load_dword v111, v[60:61], off
	v_lshl_add_u64 v[60:61], v[58:59], 2, s[16:17]
	global_load_dword v112, v[60:61], off
	s_cbranch_execnz .LBB0_325

.LBB0_325:
	s_add_u32 s50, s14, s48
	s_addc_u32 s51, s15, s49
	v_mov_b64_e32 v[60:61], s[50:51]
	v_mad_u64_u32 v[62:63], s[50:51], v58, s3, v[60:61]
	v_mov_b32_e32 v0, v63
	v_mad_u64_u32 v[58:59], s[50:51], v59, s3, v[0:1]
	v_mov_b32_e32 v63, v58
	v_lshl_add_u64 v[58:59], v[108:109], 0, v[62:63]
	v_or_b32_e32 v76, 32, v90
	v_add_co_u32_e32 v58, vcc, 0x1602000, v58
	v_mad_i64_i32 v[60:61], s[50:51], v76, s3, v[60:61]
	s_nop 0
	v_addc_co_u32_e32 v59, vcc, 0, v59, vcc
	v_lshl_add_u64 v[60:61], v[108:109], 0, v[60:61]
	v_add_co_u32_e32 v62, vcc, 0x1602000, v60
	v_or_b32_e32 v74, 40, v90
	s_nop 0
	v_addc_co_u32_e32 v63, vcc, 0, v61, vcc
	global_load_dwordx4 v[58:61], v[58:59], off offset:3072 nt
	s_nop 0
	global_load_dwordx4 v[62:65], v[62:63], off offset:3072 nt
	s_and_b64 vcc, exec, s[36:37]
	s_cbranch_vccnz .LBB0_341
	v_ashrrev_i32_e32 v77, 31, v76
	v_lshl_add_u64 v[76:77], v[76:77], 2, s[16:17]
	v_ashrrev_i32_e32 v75, 31, v74
	global_load_dword v115, v[76:77], off
	v_lshl_add_u64 v[76:77], v[74:75], 2, s[16:17]
	global_load_dword v116, v[76:77], off
	s_cbranch_execnz .LBB0_328

.LBB0_328:
	s_add_u32 s50, s14, s48
	s_addc_u32 s51, s15, s49
	v_mov_b64_e32 v[76:77], s[50:51]
	v_mad_u64_u32 v[78:79], s[50:51], v74, s3, v[76:77]
	v_mov_b32_e32 v0, v79
	v_mad_u64_u32 v[74:75], s[50:51], v75, s3, v[0:1]
	v_mov_b32_e32 v79, v74
	v_lshl_add_u64 v[74:75], v[108:109], 0, v[78:79]
	v_or_b32_e32 v92, 48, v90
	v_add_co_u32_e32 v74, vcc, 0x1602000, v74
	v_mad_i64_i32 v[76:77], s[50:51], v92, s3, v[76:77]
	s_nop 0
	v_addc_co_u32_e32 v75, vcc, 0, v75, vcc
	v_lshl_add_u64 v[76:77], v[108:109], 0, v[76:77]
	v_add_co_u32_e32 v78, vcc, 0x1602000, v76
	v_or_b32_e32 v90, 56, v90
	s_nop 0
	v_addc_co_u32_e32 v79, vcc, 0, v77, vcc
	global_load_dwordx4 v[74:77], v[74:75], off offset:3072 nt
	s_nop 0
	global_load_dwordx4 v[78:81], v[78:79], off offset:3072 nt
	s_and_b64 vcc, exec, s[36:37]
	s_cbranch_vccnz .LBB0_342
	v_ashrrev_i32_e32 v93, 31, v92
	v_lshl_add_u64 v[92:93], v[92:93], 2, s[16:17]
	v_ashrrev_i32_e32 v91, 31, v90
	global_load_dword v121, v[92:93], off
	v_lshl_add_u64 v[92:93], v[90:91], 2, s[16:17]
	global_load_dword v123, v[92:93], off
	s_cbranch_execnz .LBB0_331

.LBB0_331:
	s_add_u32 s36, s14, s48
	s_addc_u32 s37, s15, s49
	v_mov_b64_e32 v[92:93], s[36:37]
	v_mad_u64_u32 v[92:93], s[36:37], v90, s3, v[92:93]
	v_mov_b32_e32 v0, v93
	v_mad_u64_u32 v[90:91], s[36:37], v91, s3, v[0:1]
	v_mov_b32_e32 v93, v90
	v_lshl_add_u64 v[90:91], v[108:109], 0, v[92:93]
	s_mov_b32 s36, 0x1602000
	v_add_co_u32_e32 v90, vcc, s36, v90
	s_add_i32 s36, s53, s46
	s_nop 0
	v_addc_co_u32_e32 v91, vcc, 0, v91, vcc
	global_load_dwordx4 v[90:93], v[90:91], off offset:3072 nt
	s_ashr_i32 s37, s36, 31
	s_lshl_b64 s[36:37], s[36:37], 11
	s_add_u32 s46, s35, s36
	s_addc_u32 s47, s52, s37
	s_ashr_i32 s41, s40, 31
	s_lshl_b64 s[36:37], s[40:41], 1
	s_add_u32 s40, s46, s36
	s_addc_u32 s41, s47, s37

.LBB0_582:
	v_lshrrev_b64 v[8:9], 8, v[6:7]
	v_and_b32_e32 v8, -4, v8
	v_lshl_add_u64 v[8:9], s[48:49], 0, v[8:9]
	global_load_dword v0, v[8:9], off
	s_nop 0
	global_load_dwordx4 v[8:11], v[2:3], off nt
	v_lshl_add_u64 v[6:7], v[6:7], 0, s[4:5]
	s_mov_b64 s[54:55], 0xfffff
	v_cmp_lt_u64_e32 vcc, s[54:55], v[6:7]
	v_lshl_add_u64 v[2:3], v[2:3], 0, s[68:69]
	s_or_b64 s[50:51], vcc, s[50:51]
	s_waitcnt vmcnt(0)
	v_pk_mul_f32 v[8:9], v[0:1], v[8:9] op_sel_hi:[0,1]
	v_pk_mul_f32 v[10:11], v[0:1], v[10:11] op_sel_hi:[0,1]
	v_cvt_pk_bf16_f32 v8, v8, v9
	v_cvt_pk_bf16_f32 v9, v10, v11
	global_store_dwordx2 v[4:5], v[8:9], off sc1
	v_lshl_add_u64 v[4:5], v[4:5], 0, s[8:9]
	s_andn2_b64 exec, exec, s[50:51]
	s_cbranch_execnz .LBB0_582

.LBB0_585:
	s_ashr_i32 s35, s29, 31
	s_lshr_b32 s35, s35, 27
	s_add_i32 s35, s29, s35
	s_ashr_i32 s35, s35, 5
	s_lshl_b32 s48, s35, 6
	s_lshl_b32 s35, s35, 10
	s_sub_i32 s46, s31, s35
	v_or_b32_e32 v38, s48, v102
	s_ashr_i32 s47, s46, 31
	v_ashrrev_i32_e32 v39, 31, v38
	v_or_b32_e32 v10, 8, v38
	v_lshl_add_u64 v[54:55], s[46:47], 2, v[2:3]
	v_lshlrev_b64 v[6:7], 12, v[38:39]
	v_ashrrev_i32_e32 v11, 31, v10
	v_lshl_add_u64 v[6:7], v[54:55], 0, v[6:7]
	v_lshlrev_b64 v[10:11], 12, v[10:11]
	v_or_b32_e32 v14, 16, v38
	global_load_dwordx4 v[6:9], v[6:7], off nt
	v_lshl_add_u64 v[10:11], v[54:55], 0, v[10:11]
	v_ashrrev_i32_e32 v15, 31, v14
	global_load_dwordx4 v[10:13], v[10:11], off nt
	v_lshlrev_b64 v[14:15], 12, v[14:15]
	v_or_b32_e32 v34, 24, v38
	v_lshl_add_u64 v[14:15], v[54:55], 0, v[14:15]
	v_ashrrev_i32_e32 v35, 31, v34
	global_load_dwordx4 v[14:17], v[14:15], off nt
	v_lshlrev_b64 v[34:35], 12, v[34:35]
	v_or_b32_e32 v42, 32, v38
	v_lshl_add_u64 v[34:35], v[54:55], 0, v[34:35]
	v_ashrrev_i32_e32 v43, 31, v42
	global_load_dwordx4 v[34:37], v[34:35], off nt
	v_lshlrev_b64 v[42:43], 12, v[42:43]
	v_or_b32_e32 v46, 40, v38
	v_lshl_add_u64 v[42:43], v[54:55], 0, v[42:43]
	v_ashrrev_i32_e32 v47, 31, v46
	global_load_dwordx4 v[42:45], v[42:43], off nt
	v_lshlrev_b64 v[46:47], 12, v[46:47]
	v_or_b32_e32 v50, 48, v38
	v_lshl_add_u64 v[46:47], v[54:55], 0, v[46:47]
	v_ashrrev_i32_e32 v51, 31, v50
	global_load_dwordx4 v[46:49], v[46:47], off nt
	v_lshlrev_b64 v[50:51], 12, v[50:51]
	v_or_b32_e32 v38, 56, v38
	v_lshl_add_u64 v[50:51], v[54:55], 0, v[50:51]
	v_ashrrev_i32_e32 v39, 31, v38
	global_load_dwordx4 v[50:53], v[50:51], off nt
	v_lshlrev_b64 v[38:39], 12, v[38:39]
	v_lshl_add_u64 v[38:39], v[54:55], 0, v[38:39]
	global_load_dwordx4 v[54:57], v[38:39], off nt
	v_add_u32_e32 v0, v40, v71
	s_ashr_i32 s49, s48, 31
	s_add_i32 s29, s29, s72
	s_add_i32 s31, s31, s28
	s_cmpk_lt_i32 s29, 0x200
	s_waitcnt vmcnt(7)
	ds_write2_b32 v0, v6, v7 offset1:1
	ds_write2_b32 v0, v8, v9 offset0:2 offset1:3
	v_add_u32_e32 v6, 0x420, v0
	s_waitcnt vmcnt(6)
	ds_write2_b32 v6, v10, v11 offset1:1
	v_add_u32_e32 v6, 0x428, v0
	ds_write2_b32 v6, v12, v13 offset1:1
	v_add_u32_e32 v6, 0x840, v0
	v_lshl_add_u64 v[10:11], s[48:49], 1, v[4:5]
	s_waitcnt vmcnt(5)
	ds_write2_b32 v6, v14, v15 offset1:1
	v_add_u32_e32 v6, 0x848, v0
	ds_write2_b32 v6, v16, v17 offset1:1
	v_add_u32_e32 v6, 0xc60, v0
	s_waitcnt vmcnt(4)
	ds_write2_b32 v6, v34, v35 offset1:1
	v_add_u32_e32 v6, 0xc68, v0
	ds_write2_b32 v6, v36, v37 offset1:1
	v_add_u32_e32 v6, 0x1080, v0
	s_waitcnt vmcnt(3)
	ds_write2_b32 v6, v42, v43 offset1:1
	v_add_u32_e32 v6, 0x1088, v0
	ds_write2_b32 v6, v44, v45 offset1:1
	v_add_u32_e32 v6, 0x14a0, v0
	s_waitcnt vmcnt(2)
	ds_write2_b32 v6, v46, v47 offset1:1
	v_add_u32_e32 v6, 0x14a8, v0
	ds_write2_b32 v6, v48, v49 offset1:1
	v_add_u32_e32 v6, 0x18c0, v0
	v_add_u32_e32 v46, s46, v102
	s_waitcnt vmcnt(1)
	ds_write2_b32 v6, v50, v51 offset1:1
	v_add_u32_e32 v6, 0x18c8, v0
	ds_write2_b32 v6, v52, v53 offset1:1
	v_add_u32_e32 v6, 0x1ce0, v0
	v_add_u32_e32 v0, 0x1ce8, v0
	s_waitcnt vmcnt(0)
	ds_write2_b32 v6, v54, v55 offset1:1
	ds_write2_b32 v0, v56, v57 offset1:1
	s_waitcnt lgkmcnt(0)
	ds_read2_b32 v[12:13], v41 offset0:33 offset1:41
	ds_read2_b32 v[14:15], v41 offset1:8
	ds_read2_b32 v[16:17], v41 offset0:66 offset1:74
	ds_read2_b32 v[34:35], v41 offset0:99 offset1:107
	ds_read2_b32 v[36:37], v41 offset0:132 offset1:140
	ds_read2_b32 v[38:39], v41 offset0:165 offset1:173
	ds_read2_b32 v[42:43], v41 offset0:198 offset1:206
	ds_read2_b32 v[44:45], v41 offset0:231 offset1:239
	v_ashrrev_i32_e32 v47, 31, v46
	v_lshlrev_b64 v[48:49], 11, v[46:47]
	s_waitcnt lgkmcnt(6)
	v_cvt_pk_bf16_f32 v6, v14, v12
	s_waitcnt lgkmcnt(4)
	v_cvt_pk_bf16_f32 v7, v16, v34
	s_waitcnt lgkmcnt(2)
	v_cvt_pk_bf16_f32 v8, v36, v38
	s_waitcnt lgkmcnt(0)
	v_cvt_pk_bf16_f32 v9, v42, v44
	v_lshl_add_u64 v[48:49], v[10:11], 0, v[48:49]
	v_add_u32_e32 v12, 8, v46
	global_store_dwordx4 v[48:49], v[6:9], off sc1
	v_add_u32_e32 v48, 16, v46
	v_ashrrev_i32_e32 v49, 31, v48
	v_cvt_pk_bf16_f32 v6, v15, v13
	v_ashrrev_i32_e32 v13, 31, v12
	v_lshlrev_b64 v[12:13], 11, v[12:13]
	v_cvt_pk_bf16_f32 v7, v17, v35
	v_cvt_pk_bf16_f32 v8, v37, v39
	v_cvt_pk_bf16_f32 v9, v43, v45
	v_lshl_add_u64 v[12:13], v[10:11], 0, v[12:13]
	global_store_dwordx4 v[12:13], v[6:9], off sc1
	ds_read2_b32 v[12:13], v41 offset0:49 offset1:57
	ds_read2_b32 v[14:15], v41 offset0:16 offset1:24
	ds_read2_b32 v[16:17], v41 offset0:82 offset1:90
	ds_read2_b32 v[34:35], v41 offset0:115 offset1:123
	ds_read2_b32 v[36:37], v41 offset0:148 offset1:156
	ds_read2_b32 v[38:39], v41 offset0:181 offset1:189
	ds_read2_b32 v[42:43], v41 offset0:214 offset1:222
	ds_read2_b32 v[44:45], v41 offset0:247 offset1:255
	v_lshlrev_b64 v[48:49], 11, v[48:49]
	s_waitcnt lgkmcnt(6)
	v_cvt_pk_bf16_f32 v6, v14, v12
	s_waitcnt lgkmcnt(4)
	v_cvt_pk_bf16_f32 v7, v16, v34
	s_waitcnt lgkmcnt(2)
	v_cvt_pk_bf16_f32 v8, v36, v38
	s_waitcnt lgkmcnt(0)
	v_cvt_pk_bf16_f32 v9, v42, v44
	v_lshl_add_u64 v[48:49], v[10:11], 0, v[48:49]
	v_add_u32_e32 v12, 24, v46
	global_store_dwordx4 v[48:49], v[6:9], off sc1
	s_nop 1
	v_cvt_pk_bf16_f32 v6, v15, v13
	v_ashrrev_i32_e32 v13, 31, v12
	v_lshlrev_b64 v[12:13], 11, v[12:13]
	v_cvt_pk_bf16_f32 v7, v17, v35
	v_cvt_pk_bf16_f32 v8, v37, v39
	v_cvt_pk_bf16_f32 v9, v43, v45
	v_lshl_add_u64 v[10:11], v[10:11], 0, v[12:13]
	global_store_dwordx4 v[10:11], v[6:9], off sc1
	s_waitcnt lgkmcnt(0)
	s_cbranch_scc1 .LBB0_585

.LBB0_588:
	s_ashr_i32 s46, s29, 31
	s_lshr_b32 s46, s46, 26
	s_add_i32 s46, s29, s46
	s_and_b32 s48, s46, 0xffffffc0
	s_lshl_b32 s46, s46, 5
	s_and_b32 s46, s46, 0xfffff800
	s_sub_i32 s46, s35, s46
	v_or_b32_e32 v38, s48, v102
	s_ashr_i32 s47, s46, 31
	v_ashrrev_i32_e32 v39, 31, v38
	v_or_b32_e32 v10, 8, v38
	v_lshl_add_u64 v[54:55], s[46:47], 2, v[4:5]
	v_lshlrev_b64 v[6:7], 13, v[38:39]
	v_ashrrev_i32_e32 v11, 31, v10
	v_lshl_add_u64 v[6:7], v[54:55], 0, v[6:7]
	v_lshlrev_b64 v[10:11], 13, v[10:11]
	v_or_b32_e32 v14, 16, v38
	global_load_dwordx4 v[6:9], v[6:7], off nt
	v_lshl_add_u64 v[10:11], v[54:55], 0, v[10:11]
	v_ashrrev_i32_e32 v15, 31, v14
	global_load_dwordx4 v[10:13], v[10:11], off nt
	v_lshlrev_b64 v[14:15], 13, v[14:15]
	v_or_b32_e32 v34, 24, v38
	v_lshl_add_u64 v[14:15], v[54:55], 0, v[14:15]
	v_ashrrev_i32_e32 v35, 31, v34
	global_load_dwordx4 v[14:17], v[14:15], off nt
	v_lshlrev_b64 v[34:35], 13, v[34:35]
	v_or_b32_e32 v42, 32, v38
	v_lshl_add_u64 v[34:35], v[54:55], 0, v[34:35]
	v_ashrrev_i32_e32 v43, 31, v42
	global_load_dwordx4 v[34:37], v[34:35], off nt
	v_lshlrev_b64 v[42:43], 13, v[42:43]
	v_or_b32_e32 v46, 40, v38
	v_lshl_add_u64 v[42:43], v[54:55], 0, v[42:43]
	v_ashrrev_i32_e32 v47, 31, v46
	global_load_dwordx4 v[42:45], v[42:43], off nt
	v_lshlrev_b64 v[46:47], 13, v[46:47]
	v_or_b32_e32 v50, 48, v38
	v_lshl_add_u64 v[46:47], v[54:55], 0, v[46:47]
	v_ashrrev_i32_e32 v51, 31, v50
	global_load_dwordx4 v[46:49], v[46:47], off nt
	v_lshlrev_b64 v[50:51], 13, v[50:51]
	v_or_b32_e32 v38, 56, v38
	v_lshl_add_u64 v[50:51], v[54:55], 0, v[50:51]
	v_ashrrev_i32_e32 v39, 31, v38
	global_load_dwordx4 v[50:53], v[50:51], off nt
	v_lshlrev_b64 v[38:39], 13, v[38:39]
	v_lshl_add_u64 v[38:39], v[54:55], 0, v[38:39]
	global_load_dwordx4 v[54:57], v[38:39], off nt
	v_add_u32_e32 v0, v40, v71
	s_ashr_i32 s49, s48, 31
	s_add_i32 s29, s29, s72
	s_add_i32 s35, s35, s28
	s_cmpk_lt_i32 s29, 0x400
	s_waitcnt vmcnt(7)
	ds_write2_b32 v0, v6, v7 offset1:1
	ds_write2_b32 v0, v8, v9 offset0:2 offset1:3
	v_add_u32_e32 v6, 0x420, v0
	s_waitcnt vmcnt(6)
	ds_write2_b32 v6, v10, v11 offset1:1
	v_add_u32_e32 v6, 0x428, v0
	ds_write2_b32 v6, v12, v13 offset1:1
	v_add_u32_e32 v6, 0x840, v0
	v_lshl_add_u64 v[10:11], s[48:49], 1, v[2:3]
	s_waitcnt vmcnt(5)
	ds_write2_b32 v6, v14, v15 offset1:1
	v_add_u32_e32 v6, 0x848, v0
	ds_write2_b32 v6, v16, v17 offset1:1
	v_add_u32_e32 v6, 0xc60, v0
	s_waitcnt vmcnt(4)
	ds_write2_b32 v6, v34, v35 offset1:1
	v_add_u32_e32 v6, 0xc68, v0
	ds_write2_b32 v6, v36, v37 offset1:1
	v_add_u32_e32 v6, 0x1080, v0
	s_waitcnt vmcnt(3)
	ds_write2_b32 v6, v42, v43 offset1:1
	v_add_u32_e32 v6, 0x1088, v0
	ds_write2_b32 v6, v44, v45 offset1:1
	v_add_u32_e32 v6, 0x14a0, v0
	s_waitcnt vmcnt(2)
	ds_write2_b32 v6, v46, v47 offset1:1
	v_add_u32_e32 v6, 0x14a8, v0
	ds_write2_b32 v6, v48, v49 offset1:1
	v_add_u32_e32 v6, 0x18c0, v0
	v_add_u32_e32 v46, s46, v102
	s_waitcnt vmcnt(1)
	ds_write2_b32 v6, v50, v51 offset1:1
	v_add_u32_e32 v6, 0x18c8, v0
	ds_write2_b32 v6, v52, v53 offset1:1
	v_add_u32_e32 v6, 0x1ce0, v0
	v_add_u32_e32 v0, 0x1ce8, v0
	s_waitcnt vmcnt(0)
	ds_write2_b32 v6, v54, v55 offset1:1
	ds_write2_b32 v0, v56, v57 offset1:1
	s_waitcnt lgkmcnt(0)
	ds_read2_b32 v[12:13], v41 offset0:33 offset1:41
	ds_read2_b32 v[14:15], v41 offset1:8
	ds_read2_b32 v[16:17], v41 offset0:66 offset1:74
	ds_read2_b32 v[34:35], v41 offset0:99 offset1:107
	ds_read2_b32 v[36:37], v41 offset0:132 offset1:140
	ds_read2_b32 v[38:39], v41 offset0:165 offset1:173
	ds_read2_b32 v[42:43], v41 offset0:198 offset1:206
	ds_read2_b32 v[44:45], v41 offset0:231 offset1:239
	v_ashrrev_i32_e32 v47, 31, v46
	v_lshlrev_b64 v[48:49], 11, v[46:47]
	s_waitcnt lgkmcnt(6)
	v_cvt_pk_bf16_f32 v6, v14, v12
	s_waitcnt lgkmcnt(4)
	v_cvt_pk_bf16_f32 v7, v16, v34
	s_waitcnt lgkmcnt(2)
	v_cvt_pk_bf16_f32 v8, v36, v38
	s_waitcnt lgkmcnt(0)
	v_cvt_pk_bf16_f32 v9, v42, v44
	v_lshl_add_u64 v[48:49], v[10:11], 0, v[48:49]
	v_add_u32_e32 v12, 8, v46
	global_store_dwordx4 v[48:49], v[6:9], off sc1
	v_add_u32_e32 v48, 16, v46
	v_ashrrev_i32_e32 v49, 31, v48
	v_cvt_pk_bf16_f32 v6, v15, v13
	v_ashrrev_i32_e32 v13, 31, v12
	v_lshlrev_b64 v[12:13], 11, v[12:13]
	v_cvt_pk_bf16_f32 v7, v17, v35
	v_cvt_pk_bf16_f32 v8, v37, v39
	v_cvt_pk_bf16_f32 v9, v43, v45
	v_lshl_add_u64 v[12:13], v[10:11], 0, v[12:13]
	global_store_dwordx4 v[12:13], v[6:9], off sc1
	ds_read2_b32 v[12:13], v41 offset0:49 offset1:57
	ds_read2_b32 v[14:15], v41 offset0:16 offset1:24
	ds_read2_b32 v[16:17], v41 offset0:82 offset1:90
	ds_read2_b32 v[34:35], v41 offset0:115 offset1:123
	ds_read2_b32 v[36:37], v41 offset0:148 offset1:156
	ds_read2_b32 v[38:39], v41 offset0:181 offset1:189
	ds_read2_b32 v[42:43], v41 offset0:214 offset1:222
	ds_read2_b32 v[44:45], v41 offset0:247 offset1:255
	v_lshlrev_b64 v[48:49], 11, v[48:49]
	s_waitcnt lgkmcnt(6)
	v_cvt_pk_bf16_f32 v6, v14, v12
	s_waitcnt lgkmcnt(4)
	v_cvt_pk_bf16_f32 v7, v16, v34
	s_waitcnt lgkmcnt(2)
	v_cvt_pk_bf16_f32 v8, v36, v38
	s_waitcnt lgkmcnt(0)
	v_cvt_pk_bf16_f32 v9, v42, v44
	v_lshl_add_u64 v[48:49], v[10:11], 0, v[48:49]
	v_add_u32_e32 v12, 24, v46
	global_store_dwordx4 v[48:49], v[6:9], off sc1
	s_nop 1
	v_cvt_pk_bf16_f32 v6, v15, v13
	v_ashrrev_i32_e32 v13, 31, v12
	v_lshlrev_b64 v[12:13], 11, v[12:13]
	v_cvt_pk_bf16_f32 v7, v17, v35
	v_cvt_pk_bf16_f32 v8, v37, v39
	v_cvt_pk_bf16_f32 v9, v43, v45
	v_lshl_add_u64 v[10:11], v[10:11], 0, v[12:13]
	global_store_dwordx4 v[10:11], v[6:9], off sc1
	s_waitcnt lgkmcnt(0)
	s_cbranch_scc1 .LBB0_588

.LBB0_591:
	global_load_dwordx4 v[2:5], v[36:37], off offset:-2048 nt
	s_add_i32 s29, s29, s72
	s_cmpk_lt_i32 s29, 0x200
	s_waitcnt vmcnt(0)
	v_pk_mul_f32 v[6:7], v[4:5], v[4:5]
	v_pk_mul_f32 v[8:9], v[2:3], v[2:3]
	s_nop 0
	v_pk_mov_b32 v[10:11], v[8:9], v[6:7] op_sel:[1,0]
	v_mov_b32_e32 v9, v7
	v_pk_add_f32 v[48:49], v[10:11], v[8:9]
	global_load_dwordx4 v[10:13], v[36:37], off offset:-1024 nt
	v_pk_add_f32 v[48:49], v[48:49], v[48:49] op_sel:[0,1] op_sel_hi:[1,0]
	s_waitcnt vmcnt(0)
	v_pk_mul_f32 v[6:7], v[12:13], v[12:13]
	v_pk_mul_f32 v[8:9], v[10:11], v[10:11]
	s_nop 0
	v_pk_mov_b32 v[14:15], v[8:9], v[6:7] op_sel:[1,0]
	v_mov_b32_e32 v9, v7
	v_pk_add_f32 v[50:51], v[14:15], v[8:9]
	global_load_dwordx4 v[14:17], v[36:37], off nt
	global_load_dwordx4 v[6:9], v[36:37], off offset:1024 nt
	v_pk_add_f32 v[50:51], v[50:51], v[50:51] op_sel:[0,1] op_sel_hi:[1,0]
	v_lshl_add_u64 v[36:37], v[36:37], 0, s[76:77]
	s_waitcnt vmcnt(0)
	v_mul_f32_e32 v0, v6, v6
	v_mul_f32_e32 v52, v7, v7
	v_mov_b32_e32 v49, v0
	v_mov_b32_e32 v51, v52
	v_mul_f32_e32 v0, v15, v15
	v_mul_f32_e32 v53, v8, v8
	v_pk_add_f32 v[48:49], v[48:49], v[50:51]
	v_pk_fma_f32 v[50:51], v[14:15], v[14:15], v[0:1] op_sel_hi:[1,1,0]
	v_mul_f32_e32 v0, v17, v17
	v_mul_f32_e32 v54, v9, v9
	v_mov_b32_e32 v51, v53
	v_pk_fma_f32 v[52:53], v[16:17], v[16:17], v[0:1] op_sel_hi:[1,1,0]
	s_nop 0
	v_mov_b32_e32 v53, v54
	v_pk_add_f32 v[50:51], v[50:51], v[52:53]
	s_nop 0
	v_pk_add_f32 v[48:49], v[48:49], v[50:51]
	s_nop 0
	v_add_f32_e32 v0, v48, v49
	ds_bpermute_b32 v48, v42, v0
	s_waitcnt lgkmcnt(0)
	v_add_f32_e32 v0, v0, v48
	ds_bpermute_b32 v48, v43, v0
	s_waitcnt lgkmcnt(0)
	v_add_f32_e32 v0, v0, v48
	ds_bpermute_b32 v48, v44, v0
	s_waitcnt lgkmcnt(0)
	v_add_f32_e32 v0, v0, v48
	ds_bpermute_b32 v48, v45, v0
	s_waitcnt lgkmcnt(0)
	v_add_f32_e32 v0, v0, v48
	ds_bpermute_b32 v48, v46, v0
	s_waitcnt lgkmcnt(0)
	v_add_f32_e32 v0, v0, v48
	ds_bpermute_b32 v48, v47, v0
	s_waitcnt lgkmcnt(0)
	v_add_f32_e32 v0, v0, v48
	v_fmamk_f32 v0, v0, 0x3a800000, v196
	v_cmp_gt_f32_e32 vcc, s96, v0
	v_mul_f32_e32 v48, 0x4b800000, v0
	s_nop 0
	v_cndmask_b32_e32 v0, v0, v48, vcc
	v_rsq_f32_e32 v0, v0
	s_nop 0
	v_mul_f32_e32 v48, 0x45800000, v0
	v_cndmask_b32_e32 v0, v0, v48, vcc
	global_load_dwordx4 v[48:51], v[34:35], off nt
	v_pk_mul_f32 v[2:3], v[2:3], v[0:1] op_sel_hi:[1,0]
	v_pk_mul_f32 v[4:5], v[4:5], v[0:1] op_sel_hi:[1,0]
	v_pk_mul_f32 v[10:11], v[10:11], v[0:1] op_sel_hi:[1,0]
	v_pk_mul_f32 v[6:7], v[6:7], v[0:1] op_sel_hi:[1,0]
	s_waitcnt vmcnt(0)
	v_pk_mul_f32 v[2:3], v[48:49], v[2:3]
	v_pk_mul_f32 v[4:5], v[50:51], v[4:5]
	v_cvt_pk_bf16_f32 v2, v2, v3
	v_cvt_pk_bf16_f32 v3, v4, v5
	global_store_dwordx2 v[38:39], v[2:3], off offset:-1024 sc1
	global_load_dwordx4 v[2:5], v[34:35], off offset:1024 nt
	s_waitcnt vmcnt(0)
	v_pk_mul_f32 v[2:3], v[2:3], v[10:11]
	v_pk_mul_f32 v[10:11], v[12:13], v[0:1] op_sel_hi:[1,0]
	v_cvt_pk_bf16_f32 v2, v2, v3
	v_pk_mul_f32 v[4:5], v[4:5], v[10:11]
	v_pk_mul_f32 v[10:11], v[14:15], v[0:1] op_sel_hi:[1,0]
	v_cvt_pk_bf16_f32 v3, v4, v5
	global_store_dwordx2 v[38:39], v[2:3], off offset:-512 sc1
	global_load_dwordx4 v[2:5], v[34:35], off offset:2048 nt
	s_waitcnt vmcnt(0)
	v_pk_mul_f32 v[2:3], v[2:3], v[10:11]
	v_pk_mul_f32 v[10:11], v[16:17], v[0:1] op_sel_hi:[1,0]
	v_cvt_pk_bf16_f32 v2, v2, v3
	v_pk_mul_f32 v[4:5], v[4:5], v[10:11]
	s_nop 0
	v_cvt_pk_bf16_f32 v3, v4, v5
	global_store_dwordx2 v[38:39], v[2:3], off sc1
	global_load_dwordx4 v[2:5], v[34:35], off offset:3072 nt
	s_waitcnt vmcnt(0)
	v_pk_mul_f32 v[2:3], v[2:3], v[6:7]
	v_pk_mul_f32 v[6:7], v[8:9], v[0:1] op_sel_hi:[1,0]
	v_cvt_pk_bf16_f32 v2, v2, v3
	v_pk_mul_f32 v[4:5], v[4:5], v[6:7]
	s_nop 0
	v_cvt_pk_bf16_f32 v3, v4, v5
	global_store_dwordx2 v[38:39], v[2:3], off offset:512 sc1
	v_lshl_add_u64 v[38:39], v[38:39], 0, s[78:79]
	s_cbranch_scc1 .LBB0_591
	s_branch .LBB0_579
.LBB0_592:
	s_add_u32 s35, s74, 0x4d00000
	s_addc_u32 s58, s75, 0
	s_sub_i32 s14, s30, s52
	s_ashr_i32 s15, s14, 31
	s_abs_i32 s14, s14
	s_mul_hi_u32 s16, s14, s27
	s_mul_i32 s16, s16, s33
	s_sub_i32 s14, s14, s16
	s_sub_i32 s16, s14, s33
	s_cmp_ge_u32 s14, s33
	s_cselect_b32 s14, s16, s14
	s_sub_i32 s16, s14, s33
	s_cmp_ge_u32 s14, s33
	s_cselect_b32 s14, s16, s14
	s_xor_b32 s14, s14, s15
	s_sub_i32 s14, s14, s15
	s_load_dwordx4 s[40:43], s[44:45], 0x10
	s_ashr_i32 s15, s14, 31
	s_and_b32 s29, s15, s72
	s_add_i32 s29, s29, s14
	s_cmpk_lt_i32 s29, 0x300
	s_cselect_b64 s[14:15], -1, 0
	s_cmpk_gt_i32 s29, 0x2ff
	s_cbranch_scc1 .LBB0_606
	s_mul_hi_i32 s16, s29, 0x2aaaaaab
	s_lshr_b32 s17, s16, 31
	s_ashr_i32 s16, s16, 3
	s_add_i32 s16, s16, s17
	s_mul_i32 s17, s16, 0xffffffd0
	s_add_i32 s17, s17, s29
	s_lshl_b32 s38, s17, 5
	s_ashr_i32 s39, s38, 31
	s_lshl_b32 s16, s16, 6
	s_lshl_b64 s[36:37], s[38:39], 2
	s_waitcnt lgkmcnt(0)
	s_add_u32 s36, s42, s36
	s_addc_u32 s37, s43, s37
	v_lshlrev_b32_e32 v0, 2, v104
	v_or_b32_e32 v4, s16, v102
	v_lshl_add_u64 v[2:3], s[36:37], 0, v[0:1]
	v_mad_i64_i32 v[6:7], s[36:37], v4, s11, v[2:3]
	global_load_dwordx4 v[30:33], v[6:7], off nt
	s_cmp_lg_u64 s[40:41], 0
	v_ashrrev_i32_e32 v5, 31, v4
	s_cselect_b64 s[46:47], -1, 0
	s_cmp_eq_u64 s[40:41], 0
	v_lshl_add_u64 v[6:7], v[4:5], 2, s[40:41]
	v_or_b32_e32 v0, 8, v4
	s_cbranch_scc1 .LBB0_957
	global_load_dword v68, v[6:7], off
	global_load_dword v66, v[6:7], off offset:32
	v_ashrrev_i32_e32 v5, 31, v0
	s_cbranch_execnz .LBB0_596

.LBB0_596:
	v_mad_u64_u32 v[8:9], s[36:37], v0, s11, v[2:3]
	v_mov_b32_e32 v0, v9
	v_mad_u64_u32 v[10:11], s[36:37], v5, s11, v[0:1]
	v_mov_b32_e32 v9, v10
	v_or_b32_e32 v0, 16, v4
	v_mad_i64_i32 v[10:11], s[36:37], v0, s11, v[2:3]
	global_load_dwordx4 v[38:41], v[8:9], off nt
	global_load_dwordx4 v[34:37], v[10:11], off nt
	v_cndmask_b32_e64 v0, 0, 1, s[46:47]
	v_cmp_ne_u32_e64 s[36:37], 1, v0
	s_andn2_b64 vcc, exec, s[46:47]
	v_or_b32_e32 v0, 24, v4
	s_cbranch_vccnz .LBB0_958
	global_load_dword v76, v[6:7], off offset:64
	global_load_dword v74, v[6:7], off offset:96
	v_ashrrev_i32_e32 v5, 31, v0
	s_cbranch_execnz .LBB0_599

.LBB0_599:
	v_mad_u64_u32 v[8:9], s[46:47], v0, s11, v[2:3]
	v_mov_b32_e32 v0, v9
	v_mad_u64_u32 v[10:11], s[46:47], v5, s11, v[0:1]
	v_mov_b32_e32 v9, v10
	v_or_b32_e32 v0, 32, v4
	v_mad_i64_i32 v[10:11], s[46:47], v0, s11, v[2:3]
	global_load_dwordx4 v[46:49], v[8:9], off nt
	global_load_dwordx4 v[42:45], v[10:11], off nt
	s_and_b64 vcc, exec, s[36:37]
	v_or_b32_e32 v0, 40, v4
	s_cbranch_vccnz .LBB0_959
	global_load_dword v84, v[6:7], off offset:128
	global_load_dword v82, v[6:7], off offset:160
	v_ashrrev_i32_e32 v5, 31, v0
	s_cbranch_execnz .LBB0_602

.LBB0_602:
	v_mad_u64_u32 v[8:9], s[46:47], v0, s11, v[2:3]
	v_mov_b32_e32 v0, v9
	v_mad_u64_u32 v[10:11], s[46:47], v5, s11, v[0:1]
	v_mov_b32_e32 v9, v10
	v_or_b32_e32 v0, 48, v4
	v_mad_i64_i32 v[10:11], s[46:47], v0, s11, v[2:3]
	global_load_dwordx4 v[54:57], v[8:9], off nt
	global_load_dwordx4 v[50:53], v[10:11], off nt
	s_and_b64 vcc, exec, s[36:37]
	v_or_b32_e32 v0, 56, v4
	s_cbranch_vccnz .LBB0_960
	global_load_dword v92, v[6:7], off offset:192
	global_load_dword v90, v[6:7], off offset:224
	v_ashrrev_i32_e32 v5, 31, v0
	s_cbranch_execnz .LBB0_605

.LBB0_605:
	v_mad_u64_u32 v[2:3], s[36:37], v0, s11, v[2:3]
	v_mov_b32_e32 v0, v3
	v_mad_u64_u32 v[4:5], s[36:37], v5, s11, v[0:1]
	v_mov_b32_e32 v3, v4
	global_load_dwordx4 v[58:61], v[2:3], off nt
	s_lshl_b64 s[36:37], s[38:39], 11
	s_add_u32 s29, s35, s36
	s_addc_u32 s31, s58, s37
	s_ashr_i32 s17, s16, 31
	s_lshl_b64 s[16:17], s[16:17], 1
	s_add_u32 s16, s29, s16
	s_addc_u32 s17, s31, s17

.LBB0_608:
	s_add_i32 s14, s52, 0x300
	s_ashr_i32 s15, s14, 31
	s_abs_i32 s14, s14
	s_mul_hi_u32 s29, s14, s27
	s_mul_i32 s29, s29, s33
	s_sub_i32 s14, s14, s29
	s_sub_i32 s29, s14, s33
	s_cmp_ge_u32 s14, s33
	s_cselect_b32 s14, s29, s14
	s_sub_i32 s29, s14, s33
	s_cmp_ge_u32 s14, s33
	s_cselect_b32 s14, s29, s14
	s_xor_b32 s14, s14, s15
	s_sub_i32 s29, s14, s15
	s_sub_i32 s14, s30, s29
	s_ashr_i32 s15, s14, 31
	s_abs_i32 s14, s14
	s_mul_hi_u32 s38, s14, s27
	s_mul_i32 s38, s38, s33
	s_sub_i32 s14, s14, s38
	s_sub_i32 s38, s14, s33
	s_cmp_ge_u32 s14, s33
	s_cselect_b32 s14, s38, s14
	s_sub_i32 s38, s14, s33
	s_cmp_ge_u32 s14, s33
	s_cselect_b32 s14, s38, s14
	s_xor_b32 s14, s14, s15
	s_sub_i32 s14, s14, s15
	s_ashr_i32 s15, s14, 31
	s_and_b32 s38, s15, s72
	s_add_i32 s38, s38, s14
	s_cmpk_lt_i32 s38, 0x300
	s_cselect_b64 s[46:47], -1, 0
	s_cmpk_gt_i32 s38, 0x2ff
	s_cbranch_scc1 .LBB0_622
	s_mul_hi_i32 s14, s38, 0x2aaaaaab
	s_lshr_b32 s15, s14, 31
	s_ashr_i32 s14, s14, 3
	s_add_i32 s14, s14, s15
	s_mul_i32 s15, s14, 0xffffffd0
	s_add_i32 s15, s15, s38
	s_lshl_b32 s48, s15, 5
	s_ashr_i32 s49, s48, 31
	s_lshl_b32 s14, s14, 6
	s_lshl_b64 s[38:39], s[48:49], 2
	s_waitcnt lgkmcnt(0)
	s_add_u32 s38, s42, s38
	s_addc_u32 s39, s43, s39
	v_lshlrev_b32_e32 v0, 2, v104
	v_lshl_add_u64 v[2:3], s[38:39], 0, v[0:1]
	s_mov_b64 s[38:39], 0x3000
	v_or_b32_e32 v64, s14, v102
	v_lshl_add_u64 v[62:63], v[2:3], 0, s[38:39]
	v_mad_i64_i32 v[2:3], s[38:39], v64, s11, v[62:63]
	global_load_dwordx4 v[2:5], v[2:3], off nt
	s_cmp_lg_u64 s[40:41], 0
	v_ashrrev_i32_e32 v65, 31, v64
	s_cselect_b64 s[50:51], -1, 0
	s_cmp_eq_u64 s[40:41], 0
	v_lshl_add_u64 v[94:95], v[64:65], 2, s[40:41]
	v_or_b32_e32 v0, 8, v64
	s_cbranch_scc1 .LBB0_961
	global_load_dword v72, v[94:95], off
	global_load_dword v70, v[94:95], off offset:32
	v_ashrrev_i32_e32 v7, 31, v0
	s_cbranch_execnz .LBB0_612

.LBB0_612:
	v_mad_u64_u32 v[8:9], s[38:39], v0, s11, v[62:63]
	v_mov_b32_e32 v0, v9
	v_mad_u64_u32 v[6:7], s[38:39], v7, s11, v[0:1]
	v_or_b32_e32 v0, 16, v64
	v_mov_b32_e32 v9, v6
	v_mad_i64_i32 v[6:7], s[38:39], v0, s11, v[62:63]
	global_load_dwordx4 v[10:13], v[8:9], off nt
	s_nop 0
	global_load_dwordx4 v[6:9], v[6:7], off nt
	v_cndmask_b32_e64 v0, 0, 1, s[50:51]
	v_cmp_ne_u32_e64 s[38:39], 1, v0
	s_andn2_b64 vcc, exec, s[50:51]
	v_or_b32_e32 v0, 24, v64
	s_cbranch_vccnz .LBB0_962
	global_load_dword v80, v[94:95], off offset:64
	global_load_dword v78, v[94:95], off offset:96
	v_ashrrev_i32_e32 v15, 31, v0
	s_cbranch_execnz .LBB0_615

.LBB0_615:
	v_mad_u64_u32 v[16:17], s[50:51], v0, s11, v[62:63]
	v_mov_b32_e32 v0, v17
	v_mad_u64_u32 v[14:15], s[50:51], v15, s11, v[0:1]
	v_or_b32_e32 v0, 32, v64
	v_mov_b32_e32 v17, v14
	v_mad_i64_i32 v[14:15], s[50:51], v0, s11, v[62:63]
	global_load_dwordx4 v[18:21], v[16:17], off nt
	s_nop 0
	global_load_dwordx4 v[14:17], v[14:15], off nt
	s_and_b64 vcc, exec, s[38:39]
	v_or_b32_e32 v0, 40, v64
	s_cbranch_vccnz .LBB0_963
	global_load_dword v88, v[94:95], off offset:128
	global_load_dword v86, v[94:95], off offset:160
	v_ashrrev_i32_e32 v23, 31, v0
	s_cbranch_execnz .LBB0_618

.LBB0_618:
	v_mad_u64_u32 v[24:25], s[50:51], v0, s11, v[62:63]
	v_mov_b32_e32 v0, v25
	v_mad_u64_u32 v[22:23], s[50:51], v23, s11, v[0:1]
	v_or_b32_e32 v0, 48, v64
	v_mov_b32_e32 v25, v22
	v_mad_i64_i32 v[22:23], s[50:51], v0, s11, v[62:63]
	global_load_dwordx4 v[26:29], v[24:25], off nt
	s_nop 0
	global_load_dwordx4 v[22:25], v[22:23], off nt
	s_and_b64 vcc, exec, s[38:39]
	v_or_b32_e32 v0, 56, v64
	s_cbranch_vccnz .LBB0_964
	global_load_dword v96, v[94:95], off offset:192
	s_nop 0
	global_load_dword v94, v[94:95], off offset:224
	v_ashrrev_i32_e32 v65, 31, v0
	s_cbranch_execnz .LBB0_621

.LBB0_621:
	v_mad_u64_u32 v[62:63], s[38:39], v0, s11, v[62:63]
	v_mov_b32_e32 v0, v63
	v_mad_u64_u32 v[64:65], s[38:39], v65, s11, v[0:1]
	v_mov_b32_e32 v63, v64
	global_load_dwordx4 v[62:65], v[62:63], off nt
	s_lshl_b64 s[38:39], s[48:49], 11
	s_add_u32 s38, s35, s38
	s_addc_u32 s39, s58, s39
	s_ashr_i32 s15, s14, 31
	s_lshl_b64 s[14:15], s[14:15], 1
	s_add_u32 s14, s38, s14
	s_addc_u32 s15, s39, s15
	s_add_u32 s14, s14, 0x300000
	s_addc_u32 s15, s15, 0

.LBB0_627:
	s_addk_i32 s29, 0x300
	s_abs_i32 s17, s29
	s_ashr_i32 s16, s29, 31
	s_mul_hi_u32 s29, s17, s27
	s_mul_i32 s29, s29, s33
	s_sub_i32 s17, s17, s29
	s_sub_i32 s29, s17, s33
	s_cmp_ge_u32 s17, s33
	s_cselect_b32 s17, s29, s17
	s_sub_i32 s29, s17, s33
	s_cmp_ge_u32 s17, s33
	s_cselect_b32 s17, s29, s17
	s_xor_b32 s17, s17, s16
	s_sub_i32 s29, s17, s16
	s_sub_i32 s16, s30, s29
	s_ashr_i32 s17, s16, 31
	s_abs_i32 s16, s16
	s_mul_hi_u32 s36, s16, s27
	s_mul_i32 s36, s36, s33
	s_sub_i32 s16, s16, s36
	s_sub_i32 s36, s16, s33
	s_cmp_ge_u32 s16, s33
	s_cselect_b32 s16, s36, s16
	s_sub_i32 s36, s16, s33
	s_cmp_ge_u32 s16, s33
	s_cselect_b32 s16, s36, s16
	s_xor_b32 s16, s16, s17
	s_sub_i32 s16, s16, s17
	s_ashr_i32 s17, s16, 31
	s_and_b32 s36, s17, s72
	s_add_i32 s36, s36, s16
	s_cmpk_lt_i32 s36, 0x100
	s_cselect_b64 s[38:39], -1, 0
	s_cmpk_gt_i32 s36, 0xff
	s_cbranch_scc1 .LBB0_641
	s_ashr_i32 s16, s36, 31
	s_lshr_b32 s16, s16, 28
	s_add_i32 s16, s36, s16
	s_ashr_i32 s17, s16, 4
	s_lshl_b32 s16, s17, 6
	s_lshl_b32 s17, s17, 9
	s_lshl_b32 s36, s36, 5
	s_sub_i32 s46, s36, s17
	s_ashr_i32 s47, s46, 31
	s_lshl_b64 s[36:37], s[46:47], 2
	s_waitcnt lgkmcnt(0)
	s_add_u32 s36, s42, s36
	s_addc_u32 s37, s43, s37
	v_lshlrev_b32_e32 v0, 2, v104
	s_waitcnt vmcnt(7)
	v_lshl_add_u64 v[30:31], s[36:37], 0, v[0:1]
	s_mov_b64 s[36:37], 0x4800
	v_or_b32_e32 v32, s16, v102
	v_lshl_add_u64 v[30:31], v[30:31], 0, s[36:37]
	s_waitcnt vmcnt(5)
	v_mad_i64_i32 v[34:35], s[36:37], v32, s11, v[30:31]
	global_load_dwordx4 v[34:37], v[34:35], off nt
	s_cmp_lg_u64 s[40:41], 0
	v_ashrrev_i32_e32 v33, 31, v32
	s_cselect_b64 s[48:49], -1, 0
	s_cmp_eq_u64 s[40:41], 0
	v_lshl_add_u64 v[66:67], v[32:33], 2, s[40:41]
	v_or_b32_e32 v0, 8, v32
	s_cbranch_scc1 .LBB0_965
	global_load_dword v76, v[66:67], off
	global_load_dword v74, v[66:67], off offset:32
	v_ashrrev_i32_e32 v33, 31, v0
	s_cbranch_execnz .LBB0_631

.LBB0_631:
	v_mad_u64_u32 v[38:39], s[36:37], v0, s11, v[30:31]
	v_mov_b32_e32 v0, v39
	v_mad_u64_u32 v[40:41], s[36:37], v33, s11, v[0:1]
	v_or_b32_e32 v0, 16, v32
	v_mov_b32_e32 v39, v40
	v_mad_i64_i32 v[40:41], s[36:37], v0, s11, v[30:31]
	global_load_dwordx4 v[42:45], v[38:39], off nt
	s_nop 0
	global_load_dwordx4 v[38:41], v[40:41], off nt
	v_cndmask_b32_e64 v0, 0, 1, s[48:49]
	v_cmp_ne_u32_e64 s[36:37], 1, v0
	s_andn2_b64 vcc, exec, s[48:49]
	v_or_b32_e32 v0, 24, v32
	s_cbranch_vccnz .LBB0_966
	global_load_dword v84, v[66:67], off offset:64
	global_load_dword v82, v[66:67], off offset:96
	v_ashrrev_i32_e32 v33, 31, v0
	s_cbranch_execnz .LBB0_634

.LBB0_634:
	s_waitcnt vmcnt(7)
	v_mad_u64_u32 v[46:47], s[48:49], v0, s11, v[30:31]
	v_mov_b32_e32 v0, v47
	v_mad_u64_u32 v[48:49], s[48:49], v33, s11, v[0:1]
	v_or_b32_e32 v0, 32, v32
	v_mov_b32_e32 v47, v48
	v_mad_i64_i32 v[48:49], s[48:49], v0, s11, v[30:31]
	global_load_dwordx4 v[50:53], v[46:47], off nt
	s_nop 0
	global_load_dwordx4 v[46:49], v[48:49], off nt
	s_and_b64 vcc, exec, s[36:37]
	v_or_b32_e32 v0, 40, v32
	s_cbranch_vccnz .LBB0_967
	global_load_dword v92, v[66:67], off offset:128
	global_load_dword v90, v[66:67], off offset:160
	v_ashrrev_i32_e32 v33, 31, v0
	s_cbranch_execnz .LBB0_637

.LBB0_637:
	s_waitcnt vmcnt(7)
	v_mad_u64_u32 v[54:55], s[48:49], v0, s11, v[30:31]
	v_mov_b32_e32 v0, v55
	v_mad_u64_u32 v[56:57], s[48:49], v33, s11, v[0:1]
	v_or_b32_e32 v0, 48, v32
	v_mov_b32_e32 v55, v56
	v_mad_i64_i32 v[56:57], s[48:49], v0, s11, v[30:31]
	global_load_dwordx4 v[58:61], v[54:55], off nt
	s_nop 0
	global_load_dwordx4 v[54:57], v[56:57], off nt
	s_and_b64 vcc, exec, s[36:37]
	v_or_b32_e32 v0, 56, v32
	s_cbranch_vccnz .LBB0_968
	global_load_dword v114, v[66:67], off offset:192
	global_load_dword v112, v[66:67], off offset:224
	v_ashrrev_i32_e32 v33, 31, v0
	s_cbranch_execnz .LBB0_640

.LBB0_640:
	v_mad_u64_u32 v[30:31], s[36:37], v0, s11, v[30:31]
	v_mov_b32_e32 v0, v31
	v_mad_u64_u32 v[32:33], s[36:37], v33, s11, v[0:1]
	v_mov_b32_e32 v31, v32
	global_load_dwordx4 v[66:69], v[30:31], off nt
	s_lshl_b64 s[36:37], s[46:47], 11
	s_add_u32 s36, s35, s36
	s_addc_u32 s37, s58, s37
	s_ashr_i32 s17, s16, 31
	s_lshl_b64 s[16:17], s[16:17], 1
	s_add_u32 s16, s36, s16
	s_addc_u32 s17, s37, s17
	s_add_u32 s16, s16, 0x600000
	s_addc_u32 s17, s17, 0

.LBB0_646:
	s_addk_i32 s29, 0x100
	s_abs_i32 s15, s29
	s_ashr_i32 s14, s29, 31
	s_mul_hi_u32 s29, s15, s27
	s_mul_i32 s29, s29, s33
	s_sub_i32 s15, s15, s29
	s_sub_i32 s29, s15, s33
	s_cmp_ge_u32 s15, s33
	s_cselect_b32 s15, s29, s15
	s_sub_i32 s29, s15, s33
	s_cmp_ge_u32 s15, s33
	s_cselect_b32 s15, s29, s15
	s_xor_b32 s15, s15, s14
	s_sub_i32 s29, s15, s14
	s_sub_i32 s14, s30, s29
	s_ashr_i32 s15, s14, 31
	s_abs_i32 s14, s14
	s_mul_hi_u32 s36, s14, s27
	s_mul_i32 s36, s36, s33
	s_sub_i32 s14, s14, s36
	s_sub_i32 s36, s14, s33
	s_cmp_ge_u32 s14, s33
	s_cselect_b32 s14, s36, s14
	s_sub_i32 s36, s14, s33
	s_cmp_ge_u32 s14, s33
	s_cselect_b32 s14, s36, s14
	s_xor_b32 s14, s14, s15
	s_sub_i32 s14, s14, s15
	s_ashr_i32 s15, s14, 31
	s_and_b32 s36, s15, s72
	s_add_i32 s36, s36, s14
	s_cmpk_lt_i32 s36, 0x100
	s_cselect_b64 s[38:39], -1, 0
	s_cmpk_gt_i32 s36, 0xff
	s_cbranch_scc1 .LBB0_660
	s_ashr_i32 s14, s36, 31
	s_lshr_b32 s14, s14, 28
	s_add_i32 s14, s36, s14
	s_ashr_i32 s15, s14, 4
	s_lshl_b32 s14, s15, 6
	s_lshl_b32 s15, s15, 9
	s_lshl_b32 s36, s36, 5
	s_sub_i32 s46, s36, s15
	s_ashr_i32 s47, s46, 31
	s_lshl_b64 s[36:37], s[46:47], 2
	s_waitcnt lgkmcnt(0)
	s_add_u32 s36, s42, s36
	s_addc_u32 s37, s43, s37
	v_lshlrev_b32_e32 v0, 2, v104
	s_waitcnt vmcnt(7)
	v_lshl_add_u64 v[2:3], s[36:37], 0, v[0:1]
	s_mov_b64 s[36:37], 0x1800
	v_or_b32_e32 v32, s14, v102
	v_lshl_add_u64 v[30:31], v[2:3], 0, s[36:37]
	v_mad_i64_i32 v[2:3], s[36:37], v32, s11, v[30:31]
	global_load_dwordx4 v[2:5], v[2:3], off nt
	s_cmp_lg_u64 s[40:41], 0
	v_ashrrev_i32_e32 v33, 31, v32
	s_cselect_b64 s[48:49], -1, 0
	s_cmp_eq_u64 s[40:41], 0
	s_waitcnt vmcnt(1)
	v_lshl_add_u64 v[62:63], v[32:33], 2, s[40:41]
	v_or_b32_e32 v0, 8, v32
	s_cbranch_scc1 .LBB0_969
	global_load_dword v126, v[62:63], off
	global_load_dword v120, v[62:63], off offset:32
	v_ashrrev_i32_e32 v7, 31, v0
	s_cbranch_execnz .LBB0_650

.LBB0_650:
	v_mad_u64_u32 v[8:9], s[36:37], v0, s11, v[30:31]
	v_mov_b32_e32 v0, v9
	v_mad_u64_u32 v[6:7], s[36:37], v7, s11, v[0:1]
	v_or_b32_e32 v0, 16, v32
	v_mov_b32_e32 v9, v6
	v_mad_i64_i32 v[6:7], s[36:37], v0, s11, v[30:31]
	global_load_dwordx4 v[14:17], v[8:9], off nt
	s_nop 0
	global_load_dwordx4 v[6:9], v[6:7], off nt
	v_cndmask_b32_e64 v0, 0, 1, s[48:49]
	v_cmp_ne_u32_e64 s[36:37], 1, v0
	s_andn2_b64 vcc, exec, s[48:49]
	v_or_b32_e32 v0, 24, v32
	s_cbranch_vccnz .LBB0_970
	global_load_dword v132, v[62:63], off offset:64
	global_load_dword v128, v[62:63], off offset:96
	v_ashrrev_i32_e32 v11, 31, v0
	s_cbranch_execnz .LBB0_653

.LBB0_653:
	v_mad_u64_u32 v[12:13], s[48:49], v0, s11, v[30:31]
	v_mov_b32_e32 v0, v13
	v_mad_u64_u32 v[10:11], s[48:49], v11, s11, v[0:1]
	v_or_b32_e32 v0, 32, v32
	v_mov_b32_e32 v13, v10
	v_mad_i64_i32 v[10:11], s[48:49], v0, s11, v[30:31]
	global_load_dwordx4 v[22:25], v[12:13], off nt
	s_nop 0
	global_load_dwordx4 v[10:13], v[10:11], off nt
	s_and_b64 vcc, exec, s[36:37]
	v_or_b32_e32 v0, 40, v32
	s_cbranch_vccnz .LBB0_971
	global_load_dword v136, v[62:63], off offset:128
	global_load_dword v130, v[62:63], off offset:160
	v_ashrrev_i32_e32 v19, 31, v0
	s_cbranch_execnz .LBB0_656

.LBB0_656:
	v_mad_u64_u32 v[20:21], s[48:49], v0, s11, v[30:31]
	v_mov_b32_e32 v0, v21
	v_mad_u64_u32 v[18:19], s[48:49], v19, s11, v[0:1]
	v_or_b32_e32 v0, 48, v32
	v_mov_b32_e32 v21, v18
	v_mad_i64_i32 v[18:19], s[48:49], v0, s11, v[30:31]
	global_load_dwordx4 v[26:29], v[20:21], off nt
	s_nop 0
	global_load_dwordx4 v[18:21], v[18:19], off nt
	s_and_b64 vcc, exec, s[36:37]
	v_or_b32_e32 v0, 56, v32
	s_cbranch_vccnz .LBB0_972
	global_load_dword v138, v[62:63], off offset:192
	global_load_dword v134, v[62:63], off offset:224
	v_ashrrev_i32_e32 v33, 31, v0
	s_cbranch_execnz .LBB0_659

.LBB0_659:
	v_mad_u64_u32 v[30:31], s[36:37], v0, s11, v[30:31]
	v_mov_b32_e32 v0, v31
	v_mad_u64_u32 v[32:33], s[36:37], v33, s11, v[0:1]
	v_mov_b32_e32 v31, v32
	global_load_dwordx4 v[30:33], v[30:31], off nt
	s_lshl_b64 s[36:37], s[46:47], 11
	s_add_u32 s36, s35, s36
	s_addc_u32 s37, s58, s37
	s_ashr_i32 s15, s14, 31
	s_lshl_b64 s[14:15], s[14:15], 1
	s_add_u32 s14, s36, s14
	s_addc_u32 s15, s37, s15
	s_add_u32 s14, s14, 0x700000
	s_addc_u32 s15, s15, 0

.LBB0_668:
	s_sub_i32 s29, s30, s59
	s_ashr_i32 s36, s29, 31
	s_abs_i32 s29, s29
	s_mul_hi_u32 s37, s29, s27
	s_mul_i32 s37, s37, s33
	s_sub_i32 s29, s29, s37
	s_sub_i32 s37, s29, s33
	s_cmp_ge_u32 s29, s33
	s_cselect_b32 s29, s37, s29
	s_sub_i32 s37, s29, s33
	s_cmp_ge_u32 s29, s33
	s_cselect_b32 s29, s37, s29
	s_xor_b32 s29, s29, s36
	s_sub_i32 s29, s29, s36
	s_ashr_i32 s36, s29, 31
	s_and_b32 s36, s36, s72
	s_add_i32 s29, s36, s29
	s_cmp_lt_i32 s29, 64
	s_cselect_b64 s[50:51], -1, 0
	s_cmp_gt_i32 s29, 63
	s_cbranch_scc1 .LBB0_682
	s_ashr_i32 s36, s29, 31
	s_lshr_b32 s36, s36, 30
	s_add_i32 s36, s29, s36
	s_ashr_i32 s36, s36, 2
	s_lshl_b32 s48, s36, 6
	s_lshl_b32 s36, s36, 7
	s_lshl_b32 s29, s29, 5
	s_sub_i32 s52, s29, s36
	s_ashr_i32 s53, s52, 31
	s_lshl_b64 s[54:55], s[52:53], 2
	s_add_u32 s36, s38, s54
	s_addc_u32 s37, s39, s55
	s_waitcnt vmcnt(0)
	v_or_b32_e32 v94, s48, v102
	v_mov_b64_e32 v[38:39], s[36:37]
	v_mad_i64_i32 v[38:39], s[36:37], v94, s11, v[38:39]
	v_lshl_add_u64 v[38:39], v[140:141], 0, v[38:39]
	v_add_co_u32_e32 v38, vcc, 0x2000, v38
	v_ashrrev_i32_e32 v95, 31, v94
	s_nop 0
	v_addc_co_u32_e32 v39, vcc, 0, v39, vcc
	global_load_dwordx4 v[38:41], v[38:39], off nt
	v_cndmask_b32_e64 v0, 0, 1, s[16:17]
	v_cmp_ne_u32_e64 s[36:37], 1, v0
	s_andn2_b64 vcc, exec, s[16:17]
	v_lshl_add_u64 v[96:97], v[94:95], 2, s[40:41]
	v_or_b32_e32 v0, 8, v94
	s_cbranch_vccnz .LBB0_703
	global_load_dword v109, v[96:97], off
	global_load_dword v111, v[96:97], off offset:32
	v_ashrrev_i32_e32 v51, 31, v0
	s_cbranch_execnz .LBB0_672

.LBB0_672:
	s_add_u32 s56, s38, s54
	s_addc_u32 s57, s39, s55
	v_mov_b64_e32 v[52:53], s[56:57]
	v_mad_u64_u32 v[54:55], s[56:57], v0, s11, v[52:53]
	v_mov_b32_e32 v0, v55
	v_mad_u64_u32 v[50:51], s[56:57], v51, s11, v[0:1]
	v_mov_b32_e32 v55, v50
	v_lshl_add_u64 v[50:51], v[140:141], 0, v[54:55]
	v_or_b32_e32 v0, 16, v94
	v_add_co_u32_e32 v50, vcc, 0x2000, v50
	v_mad_i64_i32 v[52:53], s[56:57], v0, s11, v[52:53]
	s_nop 0
	v_addc_co_u32_e32 v51, vcc, 0, v51, vcc
	v_lshl_add_u64 v[52:53], v[140:141], 0, v[52:53]
	v_add_co_u32_e32 v54, vcc, 0x2000, v52
	v_or_b32_e32 v0, 24, v94
	s_nop 0
	v_addc_co_u32_e32 v55, vcc, 0, v53, vcc
	global_load_dwordx4 v[50:53], v[50:51], off nt
	s_nop 0
	global_load_dwordx4 v[54:57], v[54:55], off nt
	s_and_b64 vcc, exec, s[36:37]
	s_cbranch_vccnz .LBB0_704
	global_load_dword v127, v[96:97], off offset:64
	global_load_dword v129, v[96:97], off offset:96
	s_waitcnt vmcnt(5)
	v_ashrrev_i32_e32 v67, 31, v0
	s_cbranch_execnz .LBB0_675

.LBB0_675:
	s_add_u32 s56, s38, s54
	s_addc_u32 s57, s39, s55
	s_waitcnt vmcnt(3)
	v_mov_b64_e32 v[68:69], s[56:57]
	v_mad_u64_u32 v[70:71], s[56:57], v0, s11, v[68:69]
	v_mov_b32_e32 v0, v71
	v_mad_u64_u32 v[66:67], s[56:57], v67, s11, v[0:1]
	v_mov_b32_e32 v71, v66
	v_lshl_add_u64 v[66:67], v[140:141], 0, v[70:71]
	v_or_b32_e32 v0, 32, v94
	v_add_co_u32_e32 v66, vcc, 0x2000, v66
	v_mad_i64_i32 v[68:69], s[56:57], v0, s11, v[68:69]
	s_nop 0
	v_addc_co_u32_e32 v67, vcc, 0, v67, vcc
	v_lshl_add_u64 v[68:69], v[140:141], 0, v[68:69]
	v_add_co_u32_e32 v70, vcc, 0x2000, v68
	v_or_b32_e32 v0, 40, v94
	s_nop 0
	v_addc_co_u32_e32 v71, vcc, 0, v69, vcc
	global_load_dwordx4 v[66:69], v[66:67], off nt
	s_nop 0
	global_load_dwordx4 v[70:73], v[70:71], off nt
	s_and_b64 vcc, exec, s[36:37]
	s_cbranch_vccnz .LBB0_705
	global_load_dword v135, v[96:97], off offset:128
	global_load_dword v137, v[96:97], off offset:160
	v_ashrrev_i32_e32 v83, 31, v0
	s_cbranch_execnz .LBB0_678

.LBB0_678:
	s_add_u32 s56, s38, s54
	s_addc_u32 s57, s39, s55
	v_mov_b64_e32 v[84:85], s[56:57]
	v_mad_u64_u32 v[86:87], s[56:57], v0, s11, v[84:85]
	v_mov_b32_e32 v0, v87
	v_mad_u64_u32 v[82:83], s[56:57], v83, s11, v[0:1]
	v_mov_b32_e32 v87, v82
	v_lshl_add_u64 v[82:83], v[140:141], 0, v[86:87]
	v_or_b32_e32 v0, 48, v94
	v_add_co_u32_e32 v82, vcc, 0x2000, v82
	v_mad_i64_i32 v[84:85], s[56:57], v0, s11, v[84:85]
	s_nop 0
	v_addc_co_u32_e32 v83, vcc, 0, v83, vcc
	v_lshl_add_u64 v[84:85], v[140:141], 0, v[84:85]
	v_add_co_u32_e32 v86, vcc, 0x2000, v84
	v_or_b32_e32 v0, 56, v94
	s_nop 0
	v_addc_co_u32_e32 v87, vcc, 0, v85, vcc
	global_load_dwordx4 v[82:85], v[82:83], off nt
	s_nop 0
	global_load_dwordx4 v[86:89], v[86:87], off nt
	s_and_b64 vcc, exec, s[36:37]
	s_cbranch_vccnz .LBB0_706
	global_load_dword v143, v[96:97], off offset:192
	global_load_dword v144, v[96:97], off offset:224
	v_ashrrev_i32_e32 v95, 31, v0
	s_cbranch_execnz .LBB0_681

.LBB0_681:
	s_add_u32 s36, s38, s54
	s_addc_u32 s37, s39, s55
	v_mov_b64_e32 v[96:97], s[36:37]
	v_mad_u64_u32 v[96:97], s[36:37], v0, s11, v[96:97]
	v_mov_b32_e32 v0, v97
	v_mad_u64_u32 v[94:95], s[36:37], v95, s11, v[0:1]
	v_mov_b32_e32 v97, v94
	v_lshl_add_u64 v[94:95], v[140:141], 0, v[96:97]
	v_add_co_u32_e32 v94, vcc, s94, v94
	s_add_i32 s29, s34, s52
	s_nop 0
	v_addc_co_u32_e32 v95, vcc, 0, v95, vcc
	global_load_dwordx4 v[94:97], v[94:95], off nt
	s_add_i32 s36, s29, 0xffffff80
	s_ashr_i32 s37, s36, 31
	s_lshl_b64 s[36:37], s[36:37], 11
	s_add_u32 s29, s35, s36
	s_addc_u32 s52, s58, s37
	s_ashr_i32 s49, s48, 31
	s_lshl_b64 s[36:37], s[48:49], 1
	s_add_u32 s48, s29, s36
	s_addc_u32 s49, s52, s37

.LBB0_686:
	s_add_i32 s29, s59, 64
	s_ashr_i32 s36, s29, 31
	s_abs_i32 s29, s29
	s_mul_hi_u32 s37, s29, s27
	s_mul_i32 s37, s37, s33
	s_sub_i32 s29, s29, s37
	s_sub_i32 s37, s29, s33
	s_cmp_ge_u32 s29, s33
	s_cselect_b32 s29, s37, s29
	s_sub_i32 s37, s29, s33
	s_cmp_ge_u32 s29, s33
	s_cselect_b32 s29, s37, s29
	s_xor_b32 s29, s29, s36
	s_sub_i32 s29, s29, s36
	s_sub_i32 s36, s30, s29
	s_ashr_i32 s37, s36, 31
	s_abs_i32 s36, s36
	s_mul_hi_u32 s50, s36, s27
	s_mul_i32 s50, s50, s33
	s_sub_i32 s36, s36, s50
	s_sub_i32 s50, s36, s33
	s_cmp_ge_u32 s36, s33
	s_cselect_b32 s36, s50, s36
	s_sub_i32 s50, s36, s33
	s_cmp_ge_u32 s36, s33
	s_cselect_b32 s36, s50, s36
	s_xor_b32 s36, s36, s37
	s_sub_i32 s36, s36, s37
	s_ashr_i32 s37, s36, 31
	s_and_b32 s37, s37, s72
	s_add_i32 s36, s37, s36
	s_cmp_lt_i32 s36, 64
	s_cselect_b64 s[50:51], -1, 0
	s_cmp_gt_i32 s36, 63
	s_cbranch_scc1 .LBB0_700
	s_ashr_i32 s37, s36, 31
	s_lshr_b32 s37, s37, 30
	s_add_i32 s37, s36, s37
	s_ashr_i32 s37, s37, 2
	s_lshl_b32 s46, s37, 6
	s_lshl_b32 s37, s37, 7
	s_lshl_b32 s36, s36, 5
	s_sub_i32 s52, s36, s37
	s_ashr_i32 s53, s52, 31
	s_lshl_b64 s[54:55], s[52:53], 2
	s_add_u32 s36, s38, s54
	s_addc_u32 s37, s39, s55
	s_waitcnt vmcnt(0)
	v_or_b32_e32 v90, s46, v102
	v_mov_b64_e32 v[34:35], s[36:37]
	v_mad_i64_i32 v[34:35], s[36:37], v90, s11, v[34:35]
	v_lshl_add_u64 v[34:35], v[140:141], 0, v[34:35]
	v_add_co_u32_e32 v34, vcc, 0x2000, v34
	v_ashrrev_i32_e32 v91, 31, v90
	s_nop 0
	v_addc_co_u32_e32 v35, vcc, 0, v35, vcc
	global_load_dwordx4 v[34:37], v[34:35], off offset:2048 nt
	v_cndmask_b32_e64 v0, 0, 1, s[16:17]
	v_cmp_ne_u32_e64 s[36:37], 1, v0
	s_andn2_b64 vcc, exec, s[16:17]
	v_lshl_add_u64 v[92:93], v[90:91], 2, s[40:41]
	v_or_b32_e32 v0, 8, v90
	s_cbranch_vccnz .LBB0_707
	global_load_dword v105, v[92:93], off
	global_load_dword v107, v[92:93], off offset:32
	v_ashrrev_i32_e32 v43, 31, v0
	s_cbranch_execnz .LBB0_690

.LBB0_690:
	s_add_u32 s56, s38, s54
	s_addc_u32 s57, s39, s55
	v_mov_b64_e32 v[44:45], s[56:57]
	v_mad_u64_u32 v[46:47], s[56:57], v0, s11, v[44:45]
	v_mov_b32_e32 v0, v47
	v_mad_u64_u32 v[42:43], s[56:57], v43, s11, v[0:1]
	v_mov_b32_e32 v47, v42
	v_lshl_add_u64 v[42:43], v[140:141], 0, v[46:47]
	v_or_b32_e32 v0, 16, v90
	v_add_co_u32_e32 v42, vcc, 0x2000, v42
	v_mad_i64_i32 v[44:45], s[56:57], v0, s11, v[44:45]
	s_nop 0
	v_addc_co_u32_e32 v43, vcc, 0, v43, vcc
	v_lshl_add_u64 v[44:45], v[140:141], 0, v[44:45]
	v_add_co_u32_e32 v46, vcc, 0x2000, v44
	v_or_b32_e32 v0, 24, v90
	s_nop 0
	v_addc_co_u32_e32 v47, vcc, 0, v45, vcc
	global_load_dwordx4 v[42:45], v[42:43], off offset:2048 nt
	s_nop 0
	global_load_dwordx4 v[46:49], v[46:47], off offset:2048 nt
	s_and_b64 vcc, exec, s[36:37]
	s_cbranch_vccnz .LBB0_708
	global_load_dword v113, v[92:93], off offset:64
	global_load_dword v121, v[92:93], off offset:96
	s_waitcnt vmcnt(5)
	v_ashrrev_i32_e32 v59, 31, v0
	s_cbranch_execnz .LBB0_693

.LBB0_693:
	s_add_u32 s56, s38, s54
	s_addc_u32 s57, s39, s55
	s_waitcnt vmcnt(3)
	v_mov_b64_e32 v[60:61], s[56:57]
	v_mad_u64_u32 v[62:63], s[56:57], v0, s11, v[60:61]
	v_mov_b32_e32 v0, v63
	v_mad_u64_u32 v[58:59], s[56:57], v59, s11, v[0:1]
	v_mov_b32_e32 v63, v58
	v_lshl_add_u64 v[58:59], v[140:141], 0, v[62:63]
	v_or_b32_e32 v0, 32, v90
	v_add_co_u32_e32 v58, vcc, 0x2000, v58
	v_mad_i64_i32 v[60:61], s[56:57], v0, s11, v[60:61]
	s_nop 0
	v_addc_co_u32_e32 v59, vcc, 0, v59, vcc
	v_lshl_add_u64 v[60:61], v[140:141], 0, v[60:61]
	v_add_co_u32_e32 v62, vcc, 0x2000, v60
	v_or_b32_e32 v0, 40, v90
	s_nop 0
	v_addc_co_u32_e32 v63, vcc, 0, v61, vcc
	global_load_dwordx4 v[58:61], v[58:59], off offset:2048 nt
	s_nop 0
	global_load_dwordx4 v[62:65], v[62:63], off offset:2048 nt
	s_and_b64 vcc, exec, s[36:37]
	s_cbranch_vccnz .LBB0_709
	global_load_dword v131, v[92:93], off offset:128
	global_load_dword v133, v[92:93], off offset:160
	v_ashrrev_i32_e32 v75, 31, v0
	s_cbranch_execnz .LBB0_696

.LBB0_696:
	s_add_u32 s56, s38, s54
	s_addc_u32 s57, s39, s55
	v_mov_b64_e32 v[76:77], s[56:57]
	v_mad_u64_u32 v[78:79], s[56:57], v0, s11, v[76:77]
	v_mov_b32_e32 v0, v79
	v_mad_u64_u32 v[74:75], s[56:57], v75, s11, v[0:1]
	v_mov_b32_e32 v79, v74
	v_lshl_add_u64 v[74:75], v[140:141], 0, v[78:79]
	v_or_b32_e32 v0, 48, v90
	v_add_co_u32_e32 v74, vcc, 0x2000, v74
	v_mad_i64_i32 v[76:77], s[56:57], v0, s11, v[76:77]
	s_nop 0
	v_addc_co_u32_e32 v75, vcc, 0, v75, vcc
	v_lshl_add_u64 v[76:77], v[140:141], 0, v[76:77]
	v_add_co_u32_e32 v78, vcc, 0x2000, v76
	v_or_b32_e32 v0, 56, v90
	s_nop 0
	v_addc_co_u32_e32 v79, vcc, 0, v77, vcc
	global_load_dwordx4 v[74:77], v[74:75], off offset:2048 nt
	s_nop 0
	global_load_dwordx4 v[78:81], v[78:79], off offset:2048 nt
	s_and_b64 vcc, exec, s[36:37]
	s_cbranch_vccnz .LBB0_710
	global_load_dword v139, v[92:93], off offset:192
	global_load_dword v142, v[92:93], off offset:224
	v_ashrrev_i32_e32 v91, 31, v0
	s_cbranch_execnz .LBB0_699

.LBB0_699:
	s_add_u32 s36, s38, s54
	s_addc_u32 s37, s39, s55
	v_mov_b64_e32 v[92:93], s[36:37]
	v_mad_u64_u32 v[92:93], s[36:37], v0, s11, v[92:93]
	v_mov_b32_e32 v0, v93
	v_mad_u64_u32 v[90:91], s[36:37], v91, s11, v[0:1]
	v_mov_b32_e32 v93, v90
	v_lshl_add_u64 v[90:91], v[140:141], 0, v[92:93]
	v_add_co_u32_e32 v90, vcc, s94, v90
	s_add_i32 s36, s34, s52
	s_nop 0
	v_addc_co_u32_e32 v91, vcc, 0, v91, vcc
	global_load_dwordx4 v[90:93], v[90:91], off offset:2048 nt
	s_ashr_i32 s37, s36, 31
	s_lshl_b64 s[36:37], s[36:37], 11
	s_add_u32 s52, s35, s36
	s_addc_u32 s53, s58, s37
	s_ashr_i32 s47, s46, 31
	s_lshl_b64 s[36:37], s[46:47], 1
	s_add_u32 s46, s52, s36
	s_addc_u32 s47, s53, s37

.LBB0_711:
	s_sub_i32 s29, s30, s59
	s_ashr_i32 s34, s29, 31
	s_abs_i32 s29, s29
	s_mul_hi_u32 s36, s29, s27
	s_mul_i32 s36, s36, s33
	s_sub_i32 s29, s29, s36
	s_sub_i32 s36, s29, s33
	s_cmp_ge_u32 s29, s33
	s_cselect_b32 s29, s36, s29
	s_sub_i32 s36, s29, s33
	s_cmp_ge_u32 s29, s33
	s_cselect_b32 s29, s36, s29
	s_xor_b32 s29, s29, s34
	s_sub_i32 s29, s29, s34
	s_ashr_i32 s34, s29, 31
	s_and_b32 s34, s34, s72
	s_add_i32 s29, s34, s29
	s_cmp_lt_i32 s29, 48
	s_cselect_b64 s[46:47], -1, 0
	s_cmp_gt_i32 s29, 47
	s_cbranch_scc1 .LBB0_725
	s_mul_hi_i32 s34, s29, 0x55555556
	s_lshr_b32 s36, s34, 31
	s_add_i32 s34, s34, s36
	s_mul_i32 s36, s34, -3
	s_add_i32 s36, s36, s29
	s_lshl_b32 s48, s36, 5
	s_ashr_i32 s49, s48, 31
	s_lshl_b32 s38, s34, 6
	s_lshl_b64 s[36:37], s[48:49], 2
	s_add_u32 s36, s42, s36
	s_addc_u32 s37, s43, s37
	v_lshlrev_b32_e32 v0, 2, v104
	s_waitcnt vmcnt(7)
	v_lshl_add_u64 v[34:35], s[36:37], 0, v[0:1]
	s_mov_b64 s[36:37], 0x5000
	v_or_b32_e32 v36, s38, v102
	v_lshl_add_u64 v[34:35], v[34:35], 0, s[36:37]
	v_mad_i64_i32 v[38:39], s[36:37], v36, s11, v[34:35]
	global_load_dwordx4 v[62:65], v[38:39], off nt
	v_ashrrev_i32_e32 v37, 31, v36
	v_cndmask_b32_e64 v0, 0, 1, s[16:17]
	v_cmp_ne_u32_e64 s[36:37], 1, v0
	s_andn2_b64 vcc, exec, s[16:17]
	v_lshl_add_u64 v[38:39], v[36:37], 2, s[40:41]
	v_or_b32_e32 v0, 8, v36
	s_cbranch_vccnz .LBB0_973
	global_load_dword v140, v[38:39], off
	global_load_dword v142, v[38:39], off offset:32
	v_ashrrev_i32_e32 v37, 31, v0
	s_cbranch_execnz .LBB0_715

.LBB0_715:
	v_mad_u64_u32 v[40:41], s[50:51], v0, s11, v[34:35]
	v_mov_b32_e32 v0, v41
	s_waitcnt vmcnt(7)
	v_mad_u64_u32 v[42:43], s[50:51], v37, s11, v[0:1]
	v_mov_b32_e32 v41, v42
	v_or_b32_e32 v0, 16, v36
	v_mad_i64_i32 v[42:43], s[50:51], v0, s11, v[34:35]
	global_load_dwordx4 v[74:77], v[40:41], off nt
	global_load_dwordx4 v[70:73], v[42:43], off nt
	s_and_b64 vcc, exec, s[36:37]
	v_or_b32_e32 v0, 24, v36
	s_cbranch_vccnz .LBB0_974
	global_load_dword v146, v[38:39], off offset:64
	global_load_dword v144, v[38:39], off offset:96
	v_ashrrev_i32_e32 v37, 31, v0
	s_cbranch_execnz .LBB0_718

.LBB0_718:
	v_mad_u64_u32 v[40:41], s[50:51], v0, s11, v[34:35]
	v_mov_b32_e32 v0, v41
	v_mad_u64_u32 v[42:43], s[50:51], v37, s11, v[0:1]
	v_mov_b32_e32 v41, v42
	v_or_b32_e32 v0, 32, v36
	v_mad_i64_i32 v[42:43], s[50:51], v0, s11, v[34:35]
	global_load_dwordx4 v[82:85], v[40:41], off nt
	global_load_dwordx4 v[78:81], v[42:43], off nt
	s_and_b64 vcc, exec, s[36:37]
	v_or_b32_e32 v0, 40, v36
	s_cbranch_vccnz .LBB0_975
	global_load_dword v150, v[38:39], off offset:128
	global_load_dword v148, v[38:39], off offset:160
	v_ashrrev_i32_e32 v37, 31, v0
	s_cbranch_execnz .LBB0_721

.LBB0_721:
	v_mad_u64_u32 v[40:41], s[50:51], v0, s11, v[34:35]
	v_mov_b32_e32 v0, v41
	v_mad_u64_u32 v[42:43], s[50:51], v37, s11, v[0:1]
	v_mov_b32_e32 v41, v42
	v_or_b32_e32 v0, 48, v36
	v_mad_i64_i32 v[42:43], s[50:51], v0, s11, v[34:35]
	global_load_dwordx4 v[90:93], v[40:41], off nt
	global_load_dwordx4 v[86:89], v[42:43], off nt
	s_and_b64 vcc, exec, s[36:37]
	v_or_b32_e32 v0, 56, v36
	s_cbranch_vccnz .LBB0_976
	global_load_dword v154, v[38:39], off offset:192
	global_load_dword v152, v[38:39], off offset:224
	v_ashrrev_i32_e32 v37, 31, v0
	s_cbranch_execnz .LBB0_724

.LBB0_724:
	v_mad_u64_u32 v[34:35], s[36:37], v0, s11, v[34:35]
	v_mov_b32_e32 v0, v35
	v_mad_u64_u32 v[36:37], s[36:37], v37, s11, v[0:1]
	v_mov_b32_e32 v35, v36
	global_load_dwordx4 v[94:97], v[34:35], off nt
	s_lshl_b64 s[36:37], s[48:49], 11
	s_add_u32 s29, s35, s36
	s_addc_u32 s36, s58, s37
	s_ashr_i32 s39, s38, 31
	s_lshl_b64 s[34:35], s[38:39], 1
	s_add_u32 s29, s29, s34
	s_addc_u32 s34, s36, s35
	s_add_u32 s38, s29, 0xa00000
	s_addc_u32 s39, s34, 0

.LBB0_730:
	s_add_i32 s14, s59, 48
	s_ashr_i32 s15, s14, 31
	s_abs_i32 s14, s14
	s_mul_hi_u32 s29, s14, s27
	s_mul_i32 s29, s29, s33
	s_sub_i32 s14, s14, s29
	s_sub_i32 s29, s14, s33
	s_cmp_ge_u32 s14, s33
	s_cselect_b32 s14, s29, s14
	s_sub_i32 s29, s14, s33
	s_cmp_ge_u32 s14, s33
	s_cselect_b32 s14, s29, s14
	s_xor_b32 s14, s14, s15
	s_sub_i32 s29, s14, s15
	s_sub_i32 s14, s30, s29
	s_ashr_i32 s15, s14, 31
	s_abs_i32 s14, s14
	s_mul_hi_u32 s34, s14, s27
	s_mul_i32 s34, s34, s33
	s_sub_i32 s14, s14, s34
	s_sub_i32 s34, s14, s33
	s_cmp_ge_u32 s14, s33
	s_cselect_b32 s14, s34, s14
	s_sub_i32 s34, s14, s33
	s_cmp_ge_u32 s14, s33
	s_cselect_b32 s14, s34, s14
	s_xor_b32 s14, s14, s15
	s_sub_i32 s14, s14, s15
	s_ashr_i32 s15, s14, 31
	s_and_b32 s34, s15, s72
	s_add_i32 s34, s34, s14
	s_cmpk_lt_i32 s34, 0x600
	s_cselect_b64 s[46:47], -1, 0
	s_cmpk_gt_i32 s34, 0x5ff
	s_cbranch_scc1 .LBB0_744
	s_mul_hi_i32 s14, s34, 0x2aaaaaab
	s_lshr_b32 s15, s14, 31
	s_ashr_i32 s14, s14, 4
	s_add_i32 s14, s14, s15
	s_mul_i32 s15, s14, 0xffffffa0
	s_add_i32 s15, s15, s34
	s_lshl_b32 s48, s15, 5
	s_ashr_i32 s49, s48, 31
	s_lshl_b32 s14, s14, 6
	s_lshl_b64 s[34:35], s[48:49], 2
	s_add_u32 s34, s42, s34
	s_addc_u32 s35, s43, s35
	v_lshlrev_b32_e32 v0, 2, v104
	v_lshl_add_u64 v[2:3], s[34:35], 0, v[0:1]
	s_mov_b64 s[34:35], 0x5120
	v_or_b32_e32 v4, s14, v102
	v_lshl_add_u64 v[2:3], v[2:3], 0, s[34:35]
	v_mad_i64_i32 v[6:7], s[34:35], v4, s11, v[2:3]
	global_load_dwordx4 v[34:37], v[6:7], off nt
	v_ashrrev_i32_e32 v5, 31, v4
	v_cndmask_b32_e64 v0, 0, 1, s[16:17]
	v_cmp_ne_u32_e64 s[36:37], 1, v0
	s_andn2_b64 vcc, exec, s[16:17]
	v_lshl_add_u64 v[6:7], v[4:5], 2, s[40:41]
	v_or_b32_e32 v0, 8, v4
	s_cbranch_vccnz .LBB0_977
	global_load_dword v136, v[6:7], off
	global_load_dword v134, v[6:7], off offset:32
	v_ashrrev_i32_e32 v5, 31, v0
	s_cbranch_execnz .LBB0_734

.LBB0_734:
	v_mad_u64_u32 v[8:9], s[16:17], v0, s11, v[2:3]
	v_mov_b32_e32 v0, v9
	v_mad_u64_u32 v[10:11], s[16:17], v5, s11, v[0:1]
	v_mov_b32_e32 v9, v10
	v_or_b32_e32 v0, 16, v4
	v_mad_i64_i32 v[10:11], s[16:17], v0, s11, v[2:3]
	global_load_dwordx4 v[42:45], v[8:9], off nt
	global_load_dwordx4 v[38:41], v[10:11], off nt
	s_and_b64 vcc, exec, s[36:37]
	v_or_b32_e32 v0, 24, v4
	s_cbranch_vccnz .LBB0_978
	global_load_dword v138, v[6:7], off offset:64
	global_load_dword v130, v[6:7], off offset:96
	v_ashrrev_i32_e32 v5, 31, v0
	s_cbranch_execnz .LBB0_737

.LBB0_737:
	v_mad_u64_u32 v[8:9], s[16:17], v0, s11, v[2:3]
	v_mov_b32_e32 v0, v9
	v_mad_u64_u32 v[10:11], s[16:17], v5, s11, v[0:1]
	v_mov_b32_e32 v9, v10
	v_or_b32_e32 v0, 32, v4
	v_mad_i64_i32 v[10:11], s[16:17], v0, s11, v[2:3]
	global_load_dwordx4 v[50:53], v[8:9], off nt
	global_load_dwordx4 v[46:49], v[10:11], off nt
	s_and_b64 vcc, exec, s[36:37]
	v_or_b32_e32 v0, 40, v4
	s_cbranch_vccnz .LBB0_979
	global_load_dword v132, v[6:7], off offset:128
	global_load_dword v126, v[6:7], off offset:160
	v_ashrrev_i32_e32 v5, 31, v0
	s_cbranch_execnz .LBB0_740

.LBB0_740:
	v_mad_u64_u32 v[8:9], s[16:17], v0, s11, v[2:3]
	v_mov_b32_e32 v0, v9
	v_mad_u64_u32 v[10:11], s[16:17], v5, s11, v[0:1]
	v_mov_b32_e32 v9, v10
	v_or_b32_e32 v0, 48, v4
	v_mad_i64_i32 v[10:11], s[16:17], v0, s11, v[2:3]
	global_load_dwordx4 v[58:61], v[8:9], off nt
	global_load_dwordx4 v[54:57], v[10:11], off nt
	s_and_b64 vcc, exec, s[36:37]
	v_or_b32_e32 v0, 56, v4
	s_cbranch_vccnz .LBB0_980
	global_load_dword v128, v[6:7], off offset:192
	global_load_dword v120, v[6:7], off offset:224
	v_ashrrev_i32_e32 v5, 31, v0
	s_cbranch_execnz .LBB0_743

.LBB0_743:
	v_mad_u64_u32 v[2:3], s[16:17], v0, s11, v[2:3]
	v_mov_b32_e32 v0, v3
	v_mad_u64_u32 v[4:5], s[16:17], v5, s11, v[0:1]
	v_mov_b32_e32 v3, v4
	global_load_dwordx4 v[66:69], v[2:3], off nt
	s_lshl_b64 s[16:17], s[48:49], 11
	s_add_u32 s16, s74, s16
	s_addc_u32 s17, s75, s17
	s_ashr_i32 s15, s14, 31
	s_lshl_b64 s[14:15], s[14:15], 1
	s_add_u32 s14, s16, s14
	s_addc_u32 s15, s17, s15
	s_add_u32 s14, s14, 0x4700000
	s_addc_u32 s15, s15, 0

.LBB0_752:
	s_sub_i32 s36, s30, s29
	s_ashr_i32 s37, s36, 31
	s_abs_i32 s36, s36
	s_mul_hi_u32 s41, s36, s27
	s_mul_i32 s41, s41, s33
	s_sub_i32 s36, s36, s41
	s_sub_i32 s41, s36, s33
	s_cmp_ge_u32 s36, s33
	s_cselect_b32 s36, s41, s36
	s_sub_i32 s41, s36, s33
	s_cmp_ge_u32 s36, s33
	s_cselect_b32 s36, s41, s36
	s_xor_b32 s36, s36, s37
	s_sub_i32 s36, s36, s37
	s_ashr_i32 s37, s36, 31
	s_and_b32 s41, s37, s72
	s_add_i32 s41, s41, s36
	s_cmpk_lt_i32 s41, 0x100
	s_cselect_b64 s[36:37], -1, 0
	s_cmpk_gt_i32 s41, 0xff
	s_cbranch_scc1 .LBB0_754
	s_add_u32 s16, s39, s0
	s_addc_u32 s17, s40, s1
	s_ashr_i32 s42, s41, 31
	s_lshr_b32 s42, s42, 27
	s_add_i32 s42, s41, s42
	s_load_dwordx2 s[16:17], s[16:17], 0x0
	s_ashr_i32 s43, s42, 5
	s_lshl_b32 s42, s43, 6
	s_lshl_b32 s43, s43, 10
	s_lshl_b32 s41, s41, 5
	s_sub_i32 s46, s41, s43
	s_waitcnt vmcnt(1)
	v_or_b32_e32 v26, s42, v102
	s_ashr_i32 s47, s46, 31
	s_lshl_b64 s[48:49], s[46:47], 2
	v_ashrrev_i32_e32 v27, 31, v26
	s_waitcnt lgkmcnt(0)
	s_add_u32 s16, s16, s48
	v_lshlrev_b64 v[2:3], 12, v[26:27]
	v_or_b32_e32 v4, 8, v26
	v_or_b32_e32 v10, 16, v26
	v_or_b32_e32 v12, 24, v26
	v_or_b32_e32 v18, 32, v26
	v_or_b32_e32 v20, 40, v26
	s_waitcnt vmcnt(0)
	v_or_b32_e32 v30, 48, v26
	v_or_b32_e32 v26, 56, v26
	s_addc_u32 s17, s17, s49
	v_lshlrev_b32_e32 v0, 2, v104
	v_ashrrev_i32_e32 v5, 31, v4
	v_ashrrev_i32_e32 v11, 31, v10
	v_ashrrev_i32_e32 v13, 31, v12
	v_ashrrev_i32_e32 v19, 31, v18
	v_ashrrev_i32_e32 v21, 31, v20
	v_ashrrev_i32_e32 v31, 31, v30
	v_ashrrev_i32_e32 v27, 31, v26
	v_lshl_add_u64 v[28:29], s[16:17], 0, v[0:1]
	v_lshlrev_b64 v[4:5], 12, v[4:5]
	v_lshlrev_b64 v[10:11], 12, v[10:11]
	v_lshlrev_b64 v[12:13], 12, v[12:13]
	v_lshlrev_b64 v[18:19], 12, v[18:19]
	v_lshlrev_b64 v[20:21], 12, v[20:21]
	v_lshlrev_b64 v[30:31], 12, v[30:31]
	v_lshlrev_b64 v[26:27], 12, v[26:27]
	v_lshl_add_u64 v[2:3], v[28:29], 0, v[2:3]
	v_lshl_add_u64 v[6:7], v[28:29], 0, v[4:5]
	v_lshl_add_u64 v[10:11], v[28:29], 0, v[10:11]
	v_lshl_add_u64 v[14:15], v[28:29], 0, v[12:13]
	v_lshl_add_u64 v[18:19], v[28:29], 0, v[18:19]
	v_lshl_add_u64 v[22:23], v[28:29], 0, v[20:21]
	v_lshl_add_u64 v[30:31], v[28:29], 0, v[30:31]
	v_lshl_add_u64 v[32:33], v[28:29], 0, v[26:27]
	global_load_dwordx4 v[2:5], v[2:3], off nt
	s_nop 0
	global_load_dwordx4 v[6:9], v[6:7], off nt
	s_nop 0
	global_load_dwordx4 v[10:13], v[10:11], off nt
	s_nop 0
	global_load_dwordx4 v[14:17], v[14:15], off nt
	s_nop 0
	global_load_dwordx4 v[18:21], v[18:19], off nt
	s_nop 0
	global_load_dwordx4 v[22:25], v[22:23], off nt
	s_nop 0
	global_load_dwordx4 v[26:29], v[30:31], off nt
	s_nop 0
	global_load_dwordx4 v[30:33], v[32:33], off nt
	s_ashr_i32 s43, s42, 31
	s_lshl_b64 s[16:17], s[46:47], 10
	s_lshl_b64 s[42:43], s[42:43], 1
	s_add_u32 s16, s16, s42
	s_addc_u32 s17, s17, s43
	s_add_u32 s16, s35, s16
	s_addc_u32 s17, s38, s17

.LBB0_757:
	s_sub_i32 s0, s30, s29
	s_ashr_i32 s1, s0, 31
	s_abs_i32 s0, s0
	s_mul_hi_u32 s16, s0, s27
	s_mul_i32 s16, s16, s33
	s_sub_i32 s0, s0, s16
	s_sub_i32 s16, s0, s33
	s_cmp_ge_u32 s0, s33
	s_cselect_b32 s0, s16, s0
	s_sub_i32 s16, s0, s33
	s_cmp_ge_u32 s0, s33
	s_cselect_b32 s0, s16, s0
	s_xor_b32 s0, s0, s1
	s_sub_i32 s0, s0, s1
	s_ashr_i32 s1, s0, 31
	s_and_b32 s35, s1, s72
	s_add_i32 s35, s35, s0
	s_cmpk_lt_i32 s35, 0x200
	s_cselect_b64 s[16:17], -1, 0
	s_cmpk_gt_i32 s35, 0x1ff
	s_cbranch_scc1 .LBB0_759
	s_ashr_i32 s36, s35, 31
	s_lshr_b32 s36, s36, 27
	s_add_i32 s36, s35, s36
	s_load_dwordx2 s[0:1], s[44:45], 0x40
	s_ashr_i32 s37, s36, 5
	s_lshl_b32 s36, s37, 6
	s_lshl_b32 s37, s37, 10
	s_lshl_b32 s35, s35, 5
	s_sub_i32 s38, s35, s37
	s_ashr_i32 s39, s38, 31
	s_lshl_b64 s[40:41], s[38:39], 2
	s_waitcnt vmcnt(7)
	v_or_b32_e32 v2, s36, v102
	s_waitcnt lgkmcnt(0)
	s_add_u32 s0, s0, s40
	s_addc_u32 s1, s1, s41
	v_lshlrev_b32_e32 v0, 2, v104
	v_ashrrev_i32_e32 v3, 31, v2
	s_waitcnt vmcnt(6)
	v_or_b32_e32 v8, 8, v2
	v_lshl_add_u64 v[4:5], s[0:1], 0, v[0:1]
	v_lshlrev_b64 v[6:7], 12, v[2:3]
	v_ashrrev_i32_e32 v9, 31, v8
	v_lshl_add_u64 v[6:7], v[4:5], 0, v[6:7]
	v_lshlrev_b64 v[8:9], 12, v[8:9]
	v_lshl_add_u64 v[8:9], v[4:5], 0, v[8:9]
	global_load_dwordx4 v[30:33], v[6:7], off nt
	global_load_dwordx4 v[26:29], v[8:9], off nt
	v_or_b32_e32 v6, 16, v2
	v_ashrrev_i32_e32 v7, 31, v6
	v_or_b32_e32 v8, 24, v2
	v_lshlrev_b64 v[6:7], 12, v[6:7]
	v_ashrrev_i32_e32 v9, 31, v8
	v_lshl_add_u64 v[6:7], v[4:5], 0, v[6:7]
	v_lshlrev_b64 v[8:9], 12, v[8:9]
	v_lshl_add_u64 v[8:9], v[4:5], 0, v[8:9]
	global_load_dwordx4 v[22:25], v[6:7], off nt
	global_load_dwordx4 v[18:21], v[8:9], off nt
	v_or_b32_e32 v6, 32, v2
	v_ashrrev_i32_e32 v7, 31, v6
	v_or_b32_e32 v8, 40, v2
	v_lshlrev_b64 v[6:7], 12, v[6:7]
	v_ashrrev_i32_e32 v9, 31, v8
	v_lshl_add_u64 v[6:7], v[4:5], 0, v[6:7]
	v_lshlrev_b64 v[8:9], 12, v[8:9]
	v_lshl_add_u64 v[8:9], v[4:5], 0, v[8:9]
	global_load_dwordx4 v[14:17], v[6:7], off nt
	global_load_dwordx4 v[10:13], v[8:9], off nt
	v_or_b32_e32 v6, 48, v2
	v_or_b32_e32 v2, 56, v2
	v_ashrrev_i32_e32 v7, 31, v6
	v_ashrrev_i32_e32 v3, 31, v2
	v_lshlrev_b64 v[6:7], 12, v[6:7]
	v_lshlrev_b64 v[2:3], 12, v[2:3]
	v_lshl_add_u64 v[6:7], v[4:5], 0, v[6:7]
	v_lshl_add_u64 v[2:3], v[4:5], 0, v[2:3]
	global_load_dwordx4 v[6:9], v[6:7], off nt
	s_nop 0
	global_load_dwordx4 v[2:5], v[2:3], off nt
	s_lshl_b64 s[0:1], s[38:39], 11
	s_add_u32 s35, s74, s0
	s_addc_u32 s38, s75, s1
	s_ashr_i32 s37, s36, 31
	s_lshl_b64 s[0:1], s[36:37], 1
	s_add_u32 s0, s35, s0
	s_addc_u32 s1, s38, s1
	s_add_u32 s0, s0, 0x4200000
	s_addc_u32 s1, s1, 0

.LBB0_767:
	s_sub_i32 s36, s30, s29
	s_ashr_i32 s37, s36, 31
	s_abs_i32 s36, s36
	s_mul_hi_u32 s46, s36, s27
	s_mul_i32 s46, s46, s33
	s_sub_i32 s36, s36, s46
	s_sub_i32 s46, s36, s33
	s_cmp_ge_u32 s36, s33
	s_cselect_b32 s36, s46, s36
	s_sub_i32 s46, s36, s33
	s_cmp_ge_u32 s36, s33
	s_cselect_b32 s36, s46, s36
	s_xor_b32 s36, s36, s37
	s_sub_i32 s36, s36, s37
	s_ashr_i32 s37, s36, 31
	s_and_b32 s37, s37, s72
	s_add_i32 s36, s37, s36
	s_cmp_lt_i32 s36, 64
	s_cselect_b64 s[46:47], -1, 0
	s_cmp_gt_i32 s36, 63
	s_cbranch_scc1 .LBB0_781
	s_ashr_i32 s37, s36, 31
	s_lshr_b32 s37, s37, 30
	s_add_i32 s37, s36, s37
	s_ashr_i32 s37, s37, 2
	s_lshl_b32 s38, s37, 6
	s_lshl_b32 s37, s37, 7
	s_lshl_b32 s36, s36, 5
	s_sub_i32 s48, s36, s37
	s_ashr_i32 s49, s48, 31
	s_lshl_b64 s[50:51], s[48:49], 2
	s_add_u32 s36, s14, s50
	s_addc_u32 s37, s15, s51
	s_waitcnt vmcnt(0)
	v_or_b32_e32 v90, s38, v102
	v_mov_b64_e32 v[38:39], s[36:37]
	v_mad_i64_i32 v[38:39], s[36:37], v90, s3, v[38:39]
	v_lshl_add_u64 v[38:39], v[114:115], 0, v[38:39]
	global_load_dwordx4 v[38:41], v[38:39], off nt
	v_ashrrev_i32_e32 v91, 31, v90
	v_cndmask_b32_e64 v0, 0, 1, s[16:17]
	v_cmp_ne_u32_e64 s[36:37], 1, v0
	s_andn2_b64 vcc, exec, s[16:17]
	v_lshl_add_u64 v[92:93], v[90:91], 2, s[40:41]
	v_or_b32_e32 v0, 8, v90
	s_cbranch_vccnz .LBB0_802
	global_load_dword v109, v[92:93], off
	global_load_dword v111, v[92:93], off offset:32
	v_ashrrev_i32_e32 v47, 31, v0
	s_cbranch_execnz .LBB0_771

.LBB0_771:
	s_add_u32 s52, s14, s50
	s_addc_u32 s53, s15, s51
	v_mov_b64_e32 v[48:49], s[52:53]
	v_mad_u64_u32 v[54:55], s[52:53], v0, s3, v[48:49]
	v_mov_b32_e32 v0, v55
	v_mad_u64_u32 v[46:47], s[52:53], v47, s3, v[0:1]
	v_or_b32_e32 v0, 16, v90
	v_mov_b32_e32 v55, v46
	v_mad_i64_i32 v[48:49], s[52:53], v0, s3, v[48:49]
	v_lshl_add_u64 v[46:47], v[114:115], 0, v[54:55]
	v_lshl_add_u64 v[54:55], v[114:115], 0, v[48:49]
	global_load_dwordx4 v[46:49], v[46:47], off nt
	s_nop 0
	global_load_dwordx4 v[54:57], v[54:55], off nt
	s_and_b64 vcc, exec, s[36:37]
	v_or_b32_e32 v0, 24, v90
	s_cbranch_vccnz .LBB0_803
	global_load_dword v116, v[92:93], off offset:64
	global_load_dword v118, v[92:93], off offset:96
	v_ashrrev_i32_e32 v59, 31, v0
	s_cbranch_execnz .LBB0_774

.LBB0_774:
	s_add_u32 s52, s14, s50
	s_addc_u32 s53, s15, s51
	v_mov_b64_e32 v[60:61], s[52:53]
	v_mad_u64_u32 v[62:63], s[52:53], v0, s3, v[60:61]
	v_mov_b32_e32 v0, v63
	v_mad_u64_u32 v[58:59], s[52:53], v59, s3, v[0:1]
	v_or_b32_e32 v0, 32, v90
	v_mov_b32_e32 v63, v58
	v_mad_i64_i32 v[60:61], s[52:53], v0, s3, v[60:61]
	v_lshl_add_u64 v[58:59], v[114:115], 0, v[62:63]
	v_lshl_add_u64 v[62:63], v[114:115], 0, v[60:61]
	global_load_dwordx4 v[58:61], v[58:59], off nt
	s_nop 0
	global_load_dwordx4 v[62:65], v[62:63], off nt
	s_and_b64 vcc, exec, s[36:37]
	v_or_b32_e32 v0, 40, v90
	s_cbranch_vccnz .LBB0_804
	global_load_dword v119, v[92:93], off offset:128
	global_load_dword v121, v[92:93], off offset:160
	v_ashrrev_i32_e32 v75, 31, v0
	s_cbranch_execnz .LBB0_777

.LBB0_777:
	s_add_u32 s52, s14, s50
	s_addc_u32 s53, s15, s51
	v_mov_b64_e32 v[76:77], s[52:53]
	v_mad_u64_u32 v[78:79], s[52:53], v0, s3, v[76:77]
	v_mov_b32_e32 v0, v79
	v_mad_u64_u32 v[74:75], s[52:53], v75, s3, v[0:1]
	v_or_b32_e32 v0, 48, v90
	v_mov_b32_e32 v79, v74
	v_mad_i64_i32 v[76:77], s[52:53], v0, s3, v[76:77]
	v_lshl_add_u64 v[74:75], v[114:115], 0, v[78:79]
	v_lshl_add_u64 v[78:79], v[114:115], 0, v[76:77]
	global_load_dwordx4 v[74:77], v[74:75], off nt
	s_nop 0
	global_load_dwordx4 v[78:81], v[78:79], off nt
	s_and_b64 vcc, exec, s[36:37]
	v_or_b32_e32 v0, 56, v90
	s_cbranch_vccnz .LBB0_805
	global_load_dword v124, v[92:93], off offset:192
	global_load_dword v125, v[92:93], off offset:224
	v_ashrrev_i32_e32 v91, 31, v0
	s_cbranch_execnz .LBB0_780

.LBB0_780:
	s_add_u32 s36, s14, s50
	s_addc_u32 s37, s15, s51
	v_mov_b64_e32 v[92:93], s[36:37]
	v_mad_u64_u32 v[92:93], s[36:37], v0, s3, v[92:93]
	v_mov_b32_e32 v0, v93
	v_mad_u64_u32 v[90:91], s[36:37], v91, s3, v[0:1]
	v_mov_b32_e32 v93, v90
	v_lshl_add_u64 v[90:91], v[114:115], 0, v[92:93]
	global_load_dwordx4 v[90:93], v[90:91], off nt
	s_add_i32 s36, s55, s48
	s_addk_i32 s36, 0xff80
	s_ashr_i32 s37, s36, 31
	s_lshl_b64 s[36:37], s[36:37], 11
	s_add_u32 s48, s35, s36
	s_addc_u32 s49, s54, s37
	s_ashr_i32 s39, s38, 31
	s_lshl_b64 s[36:37], s[38:39], 1
	s_add_u32 s38, s48, s36
	s_addc_u32 s39, s49, s37

.LBB0_785:
	s_add_i32 s29, s29, 64
	s_ashr_i32 s36, s29, 31
	s_abs_i32 s29, s29
	s_mul_hi_u32 s37, s29, s27
	s_mul_i32 s37, s37, s33
	s_sub_i32 s29, s29, s37
	s_sub_i32 s37, s29, s33
	s_cmp_ge_u32 s29, s33
	s_cselect_b32 s29, s37, s29
	s_sub_i32 s37, s29, s33
	s_cmp_ge_u32 s29, s33
	s_cselect_b32 s29, s37, s29
	s_xor_b32 s29, s29, s36
	s_sub_i32 s29, s29, s36
	s_sub_i32 s36, s30, s29
	s_ashr_i32 s37, s36, 31
	s_abs_i32 s36, s36
	s_mul_hi_u32 s46, s36, s27
	s_mul_i32 s46, s46, s33
	s_sub_i32 s36, s36, s46
	s_sub_i32 s46, s36, s33
	s_cmp_ge_u32 s36, s33
	s_cselect_b32 s36, s46, s36
	s_sub_i32 s46, s36, s33
	s_cmp_ge_u32 s36, s33
	s_cselect_b32 s36, s46, s36
	s_xor_b32 s36, s36, s37
	s_sub_i32 s36, s36, s37
	s_ashr_i32 s37, s36, 31
	s_and_b32 s37, s37, s72
	s_add_i32 s36, s37, s36
	s_cmp_lt_i32 s36, 64
	s_cselect_b64 s[46:47], -1, 0
	s_cmp_gt_i32 s36, 63
	s_cbranch_scc1 .LBB0_799
	s_ashr_i32 s37, s36, 31
	s_lshr_b32 s37, s37, 30
	s_add_i32 s37, s36, s37
	s_ashr_i32 s37, s37, 2
	s_lshl_b32 s42, s37, 6
	s_lshl_b32 s37, s37, 7
	s_lshl_b32 s36, s36, 5
	s_sub_i32 s48, s36, s37
	s_ashr_i32 s49, s48, 31
	s_lshl_b64 s[50:51], s[48:49], 2
	s_add_u32 s36, s14, s50
	s_addc_u32 s37, s15, s51
	s_waitcnt vmcnt(0)
	v_or_b32_e32 v94, s42, v102
	v_mov_b64_e32 v[34:35], s[36:37]
	v_mad_i64_i32 v[34:35], s[36:37], v94, s3, v[34:35]
	v_lshl_add_u64 v[34:35], v[114:115], 0, v[34:35]
	v_add_co_u32_e32 v34, vcc, 0x2000, v34
	v_ashrrev_i32_e32 v95, 31, v94
	s_nop 0
	v_addc_co_u32_e32 v35, vcc, 0, v35, vcc
	global_load_dwordx4 v[34:37], v[34:35], off offset:3072 nt
	v_cndmask_b32_e64 v0, 0, 1, s[16:17]
	v_cmp_ne_u32_e64 s[36:37], 1, v0
	s_andn2_b64 vcc, exec, s[16:17]
	v_lshl_add_u64 v[96:97], v[94:95], 2, s[40:41]
	v_or_b32_e32 v0, 8, v94
	s_cbranch_vccnz .LBB0_806
	global_load_dword v105, v[96:97], off
	global_load_dword v107, v[96:97], off offset:32
	v_ashrrev_i32_e32 v43, 31, v0
	s_cbranch_execnz .LBB0_789

.LBB0_789:
	s_add_u32 s52, s14, s50
	s_addc_u32 s53, s15, s51
	v_mov_b64_e32 v[44:45], s[52:53]
	v_mad_u64_u32 v[50:51], s[52:53], v0, s3, v[44:45]
	v_mov_b32_e32 v0, v51
	v_mad_u64_u32 v[42:43], s[52:53], v43, s3, v[0:1]
	v_mov_b32_e32 v51, v42
	v_lshl_add_u64 v[42:43], v[114:115], 0, v[50:51]
	v_or_b32_e32 v0, 16, v94
	v_add_co_u32_e32 v42, vcc, 0x2000, v42
	v_mad_i64_i32 v[44:45], s[52:53], v0, s3, v[44:45]
	s_nop 0
	v_addc_co_u32_e32 v43, vcc, 0, v43, vcc
	v_lshl_add_u64 v[44:45], v[114:115], 0, v[44:45]
	v_add_co_u32_e32 v50, vcc, 0x2000, v44
	v_or_b32_e32 v0, 24, v94
	s_nop 0
	v_addc_co_u32_e32 v51, vcc, 0, v45, vcc
	global_load_dwordx4 v[42:45], v[42:43], off offset:3072 nt
	s_nop 0
	global_load_dwordx4 v[50:53], v[50:51], off offset:3072 nt
	s_and_b64 vcc, exec, s[36:37]
	s_cbranch_vccnz .LBB0_807
	global_load_dword v113, v[96:97], off offset:64
	global_load_dword v117, v[96:97], off offset:96
	v_ashrrev_i32_e32 v67, 31, v0
	s_cbranch_execnz .LBB0_792

.LBB0_792:
	s_add_u32 s52, s14, s50
	s_addc_u32 s53, s15, s51
	v_mov_b64_e32 v[68:69], s[52:53]
	v_mad_u64_u32 v[70:71], s[52:53], v0, s3, v[68:69]
	v_mov_b32_e32 v0, v71
	v_mad_u64_u32 v[66:67], s[52:53], v67, s3, v[0:1]
	v_mov_b32_e32 v71, v66
	v_lshl_add_u64 v[66:67], v[114:115], 0, v[70:71]
	v_or_b32_e32 v0, 32, v94
	v_add_co_u32_e32 v66, vcc, 0x2000, v66
	v_mad_i64_i32 v[68:69], s[52:53], v0, s3, v[68:69]
	s_nop 0
	v_addc_co_u32_e32 v67, vcc, 0, v67, vcc
	v_lshl_add_u64 v[68:69], v[114:115], 0, v[68:69]
	v_add_co_u32_e32 v70, vcc, 0x2000, v68
	v_or_b32_e32 v0, 40, v94
	s_nop 0
	v_addc_co_u32_e32 v71, vcc, 0, v69, vcc
	global_load_dwordx4 v[66:69], v[66:67], off offset:3072 nt
	s_nop 0
	global_load_dwordx4 v[70:73], v[70:71], off offset:3072 nt
	s_and_b64 vcc, exec, s[36:37]
	s_cbranch_vccnz .LBB0_808
	global_load_dword v122, v[96:97], off offset:128
	global_load_dword v123, v[96:97], off offset:160
	v_ashrrev_i32_e32 v83, 31, v0
	s_cbranch_execnz .LBB0_795

.LBB0_795:
	s_add_u32 s52, s14, s50
	s_addc_u32 s53, s15, s51
	v_mov_b64_e32 v[84:85], s[52:53]
	v_mad_u64_u32 v[86:87], s[52:53], v0, s3, v[84:85]
	v_mov_b32_e32 v0, v87
	v_mad_u64_u32 v[82:83], s[52:53], v83, s3, v[0:1]
	v_mov_b32_e32 v87, v82
	v_lshl_add_u64 v[82:83], v[114:115], 0, v[86:87]
	v_or_b32_e32 v0, 48, v94
	v_add_co_u32_e32 v82, vcc, 0x2000, v82
	v_mad_i64_i32 v[84:85], s[52:53], v0, s3, v[84:85]
	s_nop 0
	v_addc_co_u32_e32 v83, vcc, 0, v83, vcc
	v_lshl_add_u64 v[84:85], v[114:115], 0, v[84:85]
	v_add_co_u32_e32 v86, vcc, 0x2000, v84
	v_or_b32_e32 v0, 56, v94
	s_nop 0
	v_addc_co_u32_e32 v87, vcc, 0, v85, vcc
	global_load_dwordx4 v[82:85], v[82:83], off offset:3072 nt
	s_nop 0
	global_load_dwordx4 v[86:89], v[86:87], off offset:3072 nt
	s_and_b64 vcc, exec, s[36:37]
	s_cbranch_vccnz .LBB0_809
	global_load_dword v127, v[96:97], off offset:192
	global_load_dword v129, v[96:97], off offset:224
	v_ashrrev_i32_e32 v95, 31, v0
	s_cbranch_execnz .LBB0_798

.LBB0_798:
	s_add_u32 s36, s14, s50
	s_addc_u32 s37, s15, s51
	v_mov_b64_e32 v[96:97], s[36:37]
	v_mad_u64_u32 v[96:97], s[36:37], v0, s3, v[96:97]
	v_mov_b32_e32 v0, v97
	v_mad_u64_u32 v[94:95], s[36:37], v95, s3, v[0:1]
	v_mov_b32_e32 v97, v94
	v_lshl_add_u64 v[94:95], v[114:115], 0, v[96:97]
	v_add_co_u32_e32 v94, vcc, s94, v94
	s_add_i32 s36, s55, s48
	s_nop 0
	v_addc_co_u32_e32 v95, vcc, 0, v95, vcc
	global_load_dwordx4 v[94:97], v[94:95], off offset:3072 nt
	s_ashr_i32 s37, s36, 31
	s_lshl_b64 s[36:37], s[36:37], 11
	s_add_u32 s48, s35, s36
	s_addc_u32 s49, s54, s37
	s_ashr_i32 s43, s42, 31
	s_lshl_b64 s[36:37], s[42:43], 1
	s_add_u32 s42, s48, s36
	s_addc_u32 s43, s49, s37

.LBB0_810:
	s_sub_i32 s14, s30, s29
	s_ashr_i32 s15, s14, 31
	s_abs_i32 s14, s14
	s_mul_hi_u32 s16, s14, s27
	s_mul_i32 s16, s16, s33
	s_sub_i32 s14, s14, s16
	s_sub_i32 s16, s14, s33
	s_cmp_ge_u32 s14, s33
	s_cselect_b32 s14, s16, s14
	s_sub_i32 s16, s14, s33
	s_cmp_ge_u32 s14, s33
	s_cselect_b32 s14, s16, s14
	s_xor_b32 s14, s14, s15
	s_sub_i32 s14, s14, s15
	s_ashr_i32 s15, s14, 31
	s_and_b32 s29, s15, s72
	s_add_i32 s29, s29, s14
	s_cmpk_lt_i32 s29, 0x580
	s_cselect_b64 s[16:17], -1, 0
	s_cmpk_gt_i32 s29, 0x57f
	s_cbranch_scc1 .LBB0_812
	s_ashr_i32 s35, s29, 31
	s_lshr_b32 s35, s35, 27
	s_add_i32 s35, s29, s35
	s_load_dwordx2 s[14:15], s[44:45], 0x90
	s_ashr_i32 s35, s35, 5
	s_lshl_b32 s36, s35, 6
	s_lshl_b32 s35, s35, 10
	s_lshl_b32 s29, s29, 5
	s_sub_i32 s38, s29, s35
	s_ashr_i32 s39, s38, 31
	s_waitcnt vmcnt(7)
	v_or_b32_e32 v34, s36, v102
	s_lshl_b64 s[40:41], s[38:39], 2
	s_waitcnt lgkmcnt(0)
	s_add_u32 s14, s14, s40
	v_or_b32_e32 v40, 8, v34
	s_addc_u32 s15, s15, s41
	v_lshlrev_b32_e32 v0, 2, v104
	v_ashrrev_i32_e32 v35, 31, v34
	v_ashrrev_i32_e32 v41, 31, v40
	v_lshl_add_u64 v[36:37], s[14:15], 0, v[0:1]
	v_lshlrev_b64 v[38:39], 12, v[34:35]
	v_lshlrev_b64 v[40:41], 12, v[40:41]
	v_lshl_add_u64 v[38:39], v[36:37], 0, v[38:39]
	v_lshl_add_u64 v[40:41], v[36:37], 0, v[40:41]
	global_load_dwordx4 v[62:65], v[38:39], off nt
	global_load_dwordx4 v[50:53], v[40:41], off nt
	v_or_b32_e32 v38, 16, v34
	v_or_b32_e32 v40, 24, v34
	v_ashrrev_i32_e32 v39, 31, v38
	v_ashrrev_i32_e32 v41, 31, v40
	v_lshlrev_b64 v[38:39], 12, v[38:39]
	v_lshlrev_b64 v[40:41], 12, v[40:41]
	v_lshl_add_u64 v[38:39], v[36:37], 0, v[38:39]
	v_lshl_add_u64 v[40:41], v[36:37], 0, v[40:41]
	global_load_dwordx4 v[58:61], v[38:39], off nt
	global_load_dwordx4 v[42:45], v[40:41], off nt
	v_or_b32_e32 v38, 32, v34
	v_or_b32_e32 v40, 40, v34
	s_waitcnt vmcnt(10)
	v_or_b32_e32 v46, 48, v34
	v_or_b32_e32 v34, 56, v34
	v_ashrrev_i32_e32 v39, 31, v38
	v_ashrrev_i32_e32 v41, 31, v40
	v_ashrrev_i32_e32 v47, 31, v46
	v_ashrrev_i32_e32 v35, 31, v34
	v_lshlrev_b64 v[38:39], 12, v[38:39]
	v_lshlrev_b64 v[40:41], 12, v[40:41]
	v_lshlrev_b64 v[46:47], 12, v[46:47]
	v_lshlrev_b64 v[34:35], 12, v[34:35]
	v_lshl_add_u64 v[38:39], v[36:37], 0, v[38:39]
	v_lshl_add_u64 v[40:41], v[36:37], 0, v[40:41]
	v_lshl_add_u64 v[46:47], v[36:37], 0, v[46:47]
	v_lshl_add_u64 v[34:35], v[36:37], 0, v[34:35]
	global_load_dwordx4 v[54:57], v[38:39], off nt
	s_nop 0
	global_load_dwordx4 v[38:41], v[40:41], off nt
	s_nop 0
	global_load_dwordx4 v[46:49], v[46:47], off nt
	s_nop 0
	global_load_dwordx4 v[34:37], v[34:35], off nt
	s_mul_i32 s15, s38, 0x1600
	s_mul_hi_i32 s14, s38, 0x1600
	s_add_u32 s29, s74, s15
	s_addc_u32 s35, s75, s14
	s_ashr_i32 s37, s36, 31
	s_lshl_b64 s[14:15], s[36:37], 1
	s_add_u32 s14, s29, s14
	s_addc_u32 s15, s35, s15
	s_add_u32 s14, s14, 0x1c00000
	s_addc_u32 s15, s15, 0

.LBB0_824:
	s_ashr_i32 s31, s30, 31
	s_lshl_b64 s[0:1], s[30:31], 12
	s_waitcnt lgkmcnt(0)
	v_lshl_add_u64 v[2:3], v[54:55], 0, s[0:1]
	global_load_dwordx4 v[64:67], v[2:3], off nt
	global_load_dwordx4 v[68:71], v[2:3], off offset:1024 nt
	global_load_dwordx4 v[72:75], v[2:3], off offset:2048 nt
	global_load_dwordx4 v[50:53], v[2:3], off offset:3072 nt
	s_add_i32 s0, s30, s72
	s_ashr_i32 s1, s0, 31
	s_add_i32 s16, s37, s30
	s_lshl_b64 s[14:15], s[0:1], 12
	s_ashr_i32 s17, s16, 31
	v_lshl_add_u64 v[2:3], v[54:55], 0, s[14:15]
	s_lshl_b64 s[14:15], s[16:17], 12
	global_load_dwordx4 v[46:49], v[2:3], off nt
	global_load_dwordx4 v[42:45], v[2:3], off offset:1024 nt
	global_load_dwordx4 v[38:41], v[2:3], off offset:2048 nt
	global_load_dwordx4 v[34:37], v[2:3], off offset:3072 nt
	v_lshl_add_u64 v[2:3], v[54:55], 0, s[14:15]
	s_mul_i32 s14, s91, 24
	s_add_i32 s14, s14, s30
	s_ashr_i32 s15, s14, 31
	s_lshl_b64 s[34:35], s[14:15], 12
	global_load_dwordx4 v[30:33], v[2:3], off nt
	global_load_dwordx4 v[26:29], v[2:3], off offset:1024 nt
	global_load_dwordx4 v[22:25], v[2:3], off offset:2048 nt
	global_load_dwordx4 v[18:21], v[2:3], off offset:3072 nt
	v_lshl_add_u64 v[2:3], v[54:55], 0, s[34:35]
	global_load_dwordx4 v[14:17], v[2:3], off nt
	global_load_dwordx4 v[10:13], v[2:3], off offset:1024 nt
	global_load_dwordx4 v[6:9], v[2:3], off offset:2048 nt
	s_nop 0
	global_load_dwordx4 v[2:5], v[2:3], off offset:3072 nt
	s_lshl_b64 s[34:35], s[30:31], 11
	s_waitcnt vmcnt(15)
	v_mul_f32_e32 v0, v65, v65
	v_mul_f32_e32 v76, v67, v67
	v_fmac_f32_e32 v0, v64, v64
	v_fmac_f32_e32 v76, v66, v66
	v_cvt_pk_bf16_f32 v64, v64, v65
	v_cvt_pk_bf16_f32 v65, v66, v67
	v_lshl_add_u64 v[66:67], v[56:57], 0, s[34:35]
	global_store_dwordx2 v[66:67], v[64:65], off sc1
	s_waitcnt vmcnt(15)
	v_mul_f32_e32 v64, v69, v69
	v_mul_f32_e32 v65, v71, v71
	v_fmac_f32_e32 v64, v68, v68
	v_fmac_f32_e32 v65, v70, v70
	v_add_f32_e32 v0, v0, v76
	v_add_f32_e32 v64, v64, v65
	v_add_f32_e32 v0, v0, v64
	v_cvt_pk_bf16_f32 v64, v68, v69
	v_cvt_pk_bf16_f32 v65, v70, v71
	global_store_dwordx2 v[66:67], v[64:65], off offset:512 sc1
	s_waitcnt vmcnt(15)
	v_mul_f32_e32 v64, v73, v73
	v_mul_f32_e32 v65, v75, v75
	v_fmac_f32_e32 v64, v72, v72
	v_fmac_f32_e32 v65, v74, v74
	v_add_f32_e32 v64, v64, v65
	v_add_f32_e32 v0, v0, v64
	v_cvt_pk_bf16_f32 v64, v72, v73
	v_cvt_pk_bf16_f32 v65, v74, v75
	global_store_dwordx2 v[66:67], v[64:65], off offset:1024 sc1
	s_waitcnt vmcnt(15)
	v_mul_f32_e32 v64, v51, v51
	v_mul_f32_e32 v65, v53, v53
	v_fmac_f32_e32 v64, v50, v50
	v_fmac_f32_e32 v65, v52, v52
	v_add_f32_e32 v64, v64, v65
	v_add_f32_e32 v0, v0, v64
	v_cvt_pk_bf16_f32 v50, v50, v51
	v_cvt_pk_bf16_f32 v51, v52, v53
	global_store_dwordx2 v[66:67], v[50:51], off offset:1536 sc1
	ds_bpermute_b32 v50, v58, v0
	s_waitcnt lgkmcnt(0)
	v_add_f32_e32 v0, v0, v50
	ds_bpermute_b32 v50, v59, v0
	s_waitcnt lgkmcnt(0)
	v_add_f32_e32 v0, v0, v50
	ds_bpermute_b32 v50, v60, v0
	s_waitcnt lgkmcnt(0)
	v_add_f32_e32 v0, v0, v50
	ds_bpermute_b32 v50, v61, v0
	s_waitcnt lgkmcnt(0)
	v_add_f32_e32 v0, v0, v50
	ds_bpermute_b32 v50, v62, v0
	s_waitcnt lgkmcnt(0)
	v_add_f32_e32 v0, v0, v50
	ds_bpermute_b32 v50, v63, v0
	s_and_saveexec_b64 s[34:35], vcc
	s_cbranch_execz .LBB0_826
	s_waitcnt lgkmcnt(0)
	v_add_f32_e32 v0, v0, v50
	v_fma_f32 v0, v0, s40, 0.5
	v_trunc_f32_e32 v0, v0
	v_mul_f32_e32 v50, 0x2f800000, v0
	v_floor_f32_e32 v51, v50
	v_fmac_f32_e32 v0, 0xcf800000, v51
	v_cvt_u32_f32_e32 v50, v0
	v_cvt_u32_f32_e32 v51, v51
	s_lshl_b64 s[30:31], s[30:31], 3
	s_add_u32 s30, s29, s30
	s_addc_u32 s31, s36, s31
	global_store_dwordx2 v1, v[50:51], s[30:31] sc1
